# v56 + K-loops: 72 s_nop 0 wait states between M0 writes and LDS-DMA loads replaced by hoisting the M0 write above a neighbouring ds_read / address VALU
# speedup vs baseline: 1.0047x; 1.0047x over previous
; #define PG8_STAGE(bufoff, gbase, voff) do { _Pragma("unroll") for (int _i = 0; _i < 2; ++_i) \
;         __builtin_amdgcn_global_load_lds((const unsigned*)((const char*)(gbase) + (voff)[_i]), (PG8_LAS unsigned*)(lds + (bufoff) + ldsw + _i * 8192), 16, 0, 0); } while (0)
; #define PG8_LDA(dst, b, h) do { _Pragma("unroll") for (int m = 0; m < 4; ++m) _Pragma("unroll") for (int k = 0; k < 2; ++k) dst[m][k] = *(const PG8_LAS bf16x8*)(lds + PG8_SA(b, h) + aoff + m * 2048 + k * 1024); } while (0)
; #define PG8_LDB(dst, b, h) do { _Pragma("unroll") for (int n = 0; n < 2; ++n) _Pragma("unroll") for (int k = 0; k < 2; ++k) dst[n][k] = *(const PG8_LAS bf16x8*)(lds + PG8_SB(b, h) + boff + n * 2048 + k * 1024); } while (0)
; #define PG8_MMA(ai, bj, At, Bt) do { __builtin_amdgcn_s_setprio(1); _Pragma("unroll") for (int m = 0; m < 4; ++m) _Pragma("unroll") for (int n = 0; n < 2; ++n) _Pragma("unroll") for (int k = 0; k < 2; ++k) \
;         acc[ai][bj][m][n] = __builtin_amdgcn_mfma_f32_16x16x32_bf16(Bt[n][k], At[m][k], acc[ai][bj][m][n], 0, 0, 0); __builtin_amdgcn_s_setprio(0); } while (0)
; #define PG8_WAIT_V(n) asm volatile("s_waitcnt vmcnt(" #n ")" ::: "memory")
; #define PG8_WAIT_L(n) asm volatile("s_waitcnt lgkmcnt(" #n ")" ::: "memory")
; template <class Epi, class Sched, bool ALIGN_EPI = false, bool SP2 = false>
; __device__ __forceinline__ void gemm_phase(PG8_LAS unsigned char* lds, const Gemm g, const Sched& S, const Epi& E) {
;     ...
;             const bool last = (t == nt - 2);
;             const char* a1 = cA + (size_t)(t + 1) * kstep;
;             const char* a2 = last ? nA : cA + (size_t)(t + 2) * kstep; const char* b2 = last ? nB : cB + (size_t)(t + 2) * kstep;
;             const char* a3 = a2 + kstep; const char* b3 = b2 + kstep;
;             if (last && has_next) S.a_ready(nxt);
;             if constexpr (SP2) {
;             PG8_LDB(B0, 0, 0); PG8_LDB(B1, 0, 1); PG8_SCHED; PG8_LDA(At, 0, 0); PG8_STAGE(PG8_SA(1, 1), a1 + hstepA, voffA);
;             PG8_WAIT_V(8); PG8_WAIT_L(0); PG8_BAR; PG8_MMA(0, 0, At, B0); PG8_MMA(0, 1, At, B1); PG8_BAR; PG8_SCHED;
;             PG8_LDA(At, 0, 1); PG8_STAGE(PG8_SB(0, 0), b2, voffB); PG8_STAGE(PG8_SB(0, 1), b2 + hstepB, voffB); PG8_STAGE(PG8_SA(0, 0), a2, voffA);
;             PG8_WAIT_V(8); PG8_WAIT_L(0); PG8_BAR; PG8_MMA(1, 0, At, B0); PG8_MMA(1, 1, At, B1); PG8_BAR; PG8_SCHED;
.LBB0_152:
	s_ashr_i32 s15, s14, 31
	s_lshl_b64 s[16:17], s[14:15], 19
	s_add_u32 s16, s31, s16
	s_addc_u32 s17, s33, s17
	s_and_b64 s[18:19], s[2:3], exec
	s_cselect_b32 s15, s17, s25
	s_cselect_b32 s49, s16, s24
	s_ashr_i32 s13, s12, 31
	s_lshl_b64 s[18:19], s[12:13], 19
	s_add_u32 s18, s34, s18
	s_addc_u32 s19, s35, s19
	s_and_b64 s[26:27], s[2:3], exec
	s_cselect_b32 s13, s19, s23
	s_cselect_b32 s50, s18, s22
	s_add_u32 s51, s22, 0x100
	s_addc_u32 s52, s23, 0
	s_add_u32 s22, s24, 0x40080
	s_addc_u32 s23, s25, 0
	s_mov_b32 s53, -2
	s_add_u32 s24, s22, 0xfffc0080
	s_addc_u32 s25, s23, -1
	s_add_i32 s54, 0, 0x10000
	s_cmp_eq_u32 s53, 12
	s_cselect_b32 s27, s15, s25
	s_cselect_b32 s26, s49, s24
	v_add_u32_e32 v144, s54, v147
	s_cselect_b32 s25, s13, s52
	s_cselect_b32 s24, s50, s51
	s_add_i32 s56, 0, 0x14000
	ds_read_b128 v[150:153], v144
	ds_read_b128 v[154:157], v144 offset:1024
	ds_read_b128 v[158:161], v144 offset:2048
	ds_read_b128 v[162:165], v144 offset:3072
	v_add_u32_e32 v144, s56, v147
	ds_read_b128 v[166:169], v144
	ds_read_b128 v[170:173], v144 offset:1024
	ds_read_b128 v[174:177], v144 offset:2048
	ds_read_b128 v[178:181], v144 offset:3072
	v_lshl_add_u64 v[144:145], s[22:23], 0, v[142:143]
	s_add_i32 m0, s41, 0xc000
	ds_read_b128 v[182:185], v149
	ds_read_b128 v[186:189], v149 offset:1024
	ds_read_b128 v[190:193], v149 offset:2048
	ds_read_b128 v[194:197], v149 offset:3072
	ds_read_b128 v[210:213], v149 offset:4096
	ds_read_b128 v[226:229], v149 offset:5120
	ds_read_b128 v[230:233], v149 offset:6144
	ds_read_b128 v[234:237], v149 offset:7168
	s_mov_b32 m0, s45
	v_lshl_add_u64 v[244:245], v[240:241], 0, s[64:65]
	global_load_lds_dwordx4 v[244:245], off
	s_mov_b32 m0, s46
	v_lshl_add_u64 v[244:245], v[242:243], 0, s[64:65]
	global_load_lds_dwordx4 v[244:245], off
	s_add_i32 m0, s41, 0xc000
	s_nop 0
	global_load_lds_dwordx4 v[144:145], off
	s_add_i32 m0, s41, 0xe000
	v_lshl_add_u64 v[144:145], s[22:23], 0, v[140:141]
	global_load_lds_dwordx4 v[144:145], off
	s_waitcnt vmcnt(8)
	s_waitcnt lgkmcnt(0)
	s_barrier
	s_setprio 1
	s_waitcnt lgkmcnt(0)
	v_mfma_f32_16x16x32_bf16 v[128:131], v[150:153], v[182:185], 0
	v_mfma_f32_16x16x32_bf16 v[120:123], v[158:161], v[182:185], 0
	v_mfma_f32_16x16x32_bf16 v[112:115], v[150:153], v[190:193], 0
	v_mfma_f32_16x16x32_bf16 v[104:107], v[158:161], v[190:193], 0
	v_mfma_f32_16x16x32_bf16 v[96:99], v[150:153], v[210:213], 0
	v_mfma_f32_16x16x32_bf16 v[88:91], v[158:161], v[210:213], 0
	v_mfma_f32_16x16x32_bf16 v[80:83], v[150:153], v[230:233], 0
	v_mfma_f32_16x16x32_bf16 v[72:75], v[158:161], v[230:233], 0
	v_mfma_f32_16x16x32_bf16 v[128:131], v[154:157], v[186:189], v[128:131]
	v_mfma_f32_16x16x32_bf16 v[120:123], v[162:165], v[186:189], v[120:123]
	v_mfma_f32_16x16x32_bf16 v[112:115], v[154:157], v[194:197], v[112:115]
	v_mfma_f32_16x16x32_bf16 v[104:107], v[162:165], v[194:197], v[104:107]
	v_mfma_f32_16x16x32_bf16 v[96:99], v[154:157], v[226:229], v[96:99]
	v_mfma_f32_16x16x32_bf16 v[88:91], v[162:165], v[226:229], v[88:91]
	v_mfma_f32_16x16x32_bf16 v[80:83], v[154:157], v[234:237], v[80:83]
	v_mfma_f32_16x16x32_bf16 v[72:75], v[162:165], v[234:237], v[72:75]
	s_setprio 0
	s_setprio 1
	v_mfma_f32_16x16x32_bf16 v[124:127], v[166:169], v[182:185], 0
	v_mfma_f32_16x16x32_bf16 v[116:119], v[174:177], v[182:185], 0
	v_mfma_f32_16x16x32_bf16 v[108:111], v[166:169], v[190:193], 0
	v_mfma_f32_16x16x32_bf16 v[100:103], v[174:177], v[190:193], 0
	v_mfma_f32_16x16x32_bf16 v[92:95], v[166:169], v[210:213], 0
	v_mfma_f32_16x16x32_bf16 v[84:87], v[174:177], v[210:213], 0
	v_mfma_f32_16x16x32_bf16 v[76:79], v[166:169], v[230:233], 0
	v_mfma_f32_16x16x32_bf16 v[68:71], v[174:177], v[230:233], 0
	v_mfma_f32_16x16x32_bf16 v[124:127], v[170:173], v[186:189], v[124:127]
	v_mfma_f32_16x16x32_bf16 v[116:119], v[178:181], v[186:189], v[116:119]
	v_mfma_f32_16x16x32_bf16 v[108:111], v[170:173], v[194:197], v[108:111]
	v_mfma_f32_16x16x32_bf16 v[100:103], v[178:181], v[194:197], v[100:103]
	v_mfma_f32_16x16x32_bf16 v[92:95], v[170:173], v[226:229], v[92:95]
	v_mfma_f32_16x16x32_bf16 v[84:87], v[178:181], v[226:229], v[84:87]
	v_mfma_f32_16x16x32_bf16 v[76:79], v[170:173], v[234:237], v[76:79]
	v_mfma_f32_16x16x32_bf16 v[68:71], v[178:181], v[234:237], v[68:71]
	s_setprio 0
	s_barrier
	s_add_i32 s54, s54, s39
	v_lshl_add_u64 v[144:145], s[24:25], 0, v[136:137]
	s_mov_b32 m0, s54
	ds_read_b128 v[182:185], v149 offset:16384
	ds_read_b128 v[186:189], v149 offset:17408
	ds_read_b128 v[190:193], v149 offset:18432
	ds_read_b128 v[194:197], v149 offset:19456
	ds_read_b128 v[210:213], v149 offset:20480
	ds_read_b128 v[226:229], v149 offset:21504
	ds_read_b128 v[230:233], v149 offset:22528
	ds_read_b128 v[234:237], v149 offset:23552
	global_load_lds_dwordx4 v[144:145], off
	s_add_i32 m0, s54, 0x2000
	s_add_u32 s54, s24, 0x40000
	v_lshl_add_u64 v[238:239], s[24:25], 0, v[132:133]
	s_addc_u32 s55, s25, 0
	s_add_i32 s56, s56, s39
	global_load_lds_dwordx4 v[238:239], off
	v_lshl_add_u64 v[240:241], s[54:55], 0, v[136:137]
	s_mov_b32 m0, s56
	v_lshl_add_u64 v[242:243], s[26:27], 0, v[134:135]
	global_load_lds_dwordx4 v[240:241], off
	s_add_i32 m0, s56, 0x2000
	v_lshl_add_u64 v[240:241], s[54:55], 0, v[132:133]
	global_load_lds_dwordx4 v[240:241], off
	v_lshl_add_u64 v[240:241], s[26:27], 0, v[138:139]
	s_waitcnt vmcnt(6)
	s_waitcnt lgkmcnt(0)
	s_barrier
; #define PG8_STAGE(bufoff, gbase, voff) do { _Pragma("unroll") for (int _i = 0; _i < 2; ++_i) \
;         __builtin_amdgcn_global_load_lds((const unsigned*)((const char*)(gbase) + (voff)[_i]), (PG8_LAS unsigned*)(lds + (bufoff) + ldsw + _i * 8192), 16, 0, 0); } while (0)
; #define PG8_LDA(dst, b, h) do { _Pragma("unroll") for (int m = 0; m < 4; ++m) _Pragma("unroll") for (int k = 0; k < 2; ++k) dst[m][k] = *(const PG8_LAS bf16x8*)(lds + PG8_SA(b, h) + aoff + m * 2048 + k * 1024); } while (0)
; #define PG8_LDB(dst, b, h) do { _Pragma("unroll") for (int n = 0; n < 2; ++n) _Pragma("unroll") for (int k = 0; k < 2; ++k) dst[n][k] = *(const PG8_LAS bf16x8*)(lds + PG8_SB(b, h) + boff + n * 2048 + k * 1024); } while (0)
; #define PG8_MMA(ai, bj, At, Bt) do { __builtin_amdgcn_s_setprio(1); _Pragma("unroll") for (int m = 0; m < 4; ++m) _Pragma("unroll") for (int n = 0; n < 2; ++n) _Pragma("unroll") for (int k = 0; k < 2; ++k) \
;         acc[ai][bj][m][n] = __builtin_amdgcn_mfma_f32_16x16x32_bf16(Bt[n][k], At[m][k], acc[ai][bj][m][n], 0, 0, 0); __builtin_amdgcn_s_setprio(0); } while (0)
; #define PG8_WAIT_V(n) asm volatile("s_waitcnt vmcnt(" #n ")" ::: "memory")
; #define PG8_WAIT_L(n) asm volatile("s_waitcnt lgkmcnt(" #n ")" ::: "memory")
; #define PG8_BAR __builtin_amdgcn_s_barrier()
; #define PG8_SCHED __builtin_amdgcn_sched_barrier(0)
; template <class Epi, class Sched, bool ALIGN_EPI = false, bool SP2 = false>
; __device__ __forceinline__ void gemm_phase(PG8_LAS unsigned char* lds, const Gemm g, const Sched& S, const Epi& E) {
;     ...
;             PG8_WAIT_V(8); PG8_WAIT_L(0); PG8_BAR; PG8_MMA(1, 0, At, B0); PG8_MMA(1, 1, At, B1); PG8_BAR; PG8_SCHED;
;             PG8_LDB(B0, 1, 0); PG8_LDB(B1, 1, 1); PG8_SCHED; PG8_LDA(At, 1, 0); PG8_STAGE(PG8_SA(0, 1), a2 + hstepA, voffA);
;             PG8_WAIT_V(8); PG8_WAIT_L(0); PG8_BAR; PG8_MMA(0, 0, At, B0); PG8_MMA(0, 1, At, B1); PG8_BAR; PG8_SCHED;
	s_setprio 1
	s_waitcnt lgkmcnt(0)
	v_mfma_f32_16x16x32_bf16 v[64:67], v[150:153], v[182:185], 0
	v_mfma_f32_16x16x32_bf16 v[56:59], v[158:161], v[182:185], 0
	v_mfma_f32_16x16x32_bf16 v[48:51], v[150:153], v[190:193], 0
	v_mfma_f32_16x16x32_bf16 v[40:43], v[158:161], v[190:193], 0
	v_mfma_f32_16x16x32_bf16 v[32:35], v[150:153], v[210:213], 0
	v_mfma_f32_16x16x32_bf16 v[24:27], v[158:161], v[210:213], 0
	v_mfma_f32_16x16x32_bf16 v[16:19], v[150:153], v[230:233], 0
	v_mfma_f32_16x16x32_bf16 v[8:11], v[158:161], v[230:233], 0
	v_mfma_f32_16x16x32_bf16 v[64:67], v[154:157], v[186:189], v[64:67]
	v_mfma_f32_16x16x32_bf16 v[56:59], v[162:165], v[186:189], v[56:59]
	v_mfma_f32_16x16x32_bf16 v[48:51], v[154:157], v[194:197], v[48:51]
	v_mfma_f32_16x16x32_bf16 v[40:43], v[162:165], v[194:197], v[40:43]
	v_mfma_f32_16x16x32_bf16 v[32:35], v[154:157], v[226:229], v[32:35]
	v_mfma_f32_16x16x32_bf16 v[24:27], v[162:165], v[226:229], v[24:27]
	v_mfma_f32_16x16x32_bf16 v[16:19], v[154:157], v[234:237], v[16:19]
	v_mfma_f32_16x16x32_bf16 v[8:11], v[162:165], v[234:237], v[8:11]
	s_setprio 0
	s_setprio 1
	v_mfma_f32_16x16x32_bf16 v[60:63], v[166:169], v[182:185], 0
	v_mfma_f32_16x16x32_bf16 v[52:55], v[174:177], v[182:185], 0
	v_mfma_f32_16x16x32_bf16 v[44:47], v[166:169], v[190:193], 0
	v_mfma_f32_16x16x32_bf16 v[36:39], v[174:177], v[190:193], 0
	v_mfma_f32_16x16x32_bf16 v[28:31], v[166:169], v[210:213], 0
	v_mfma_f32_16x16x32_bf16 v[20:23], v[174:177], v[210:213], 0
	v_mfma_f32_16x16x32_bf16 v[12:15], v[166:169], v[230:233], 0
	v_mfma_f32_16x16x32_bf16 v[4:7], v[174:177], v[230:233], 0
	v_mfma_f32_16x16x32_bf16 v[60:63], v[170:173], v[186:189], v[60:63]
	v_mfma_f32_16x16x32_bf16 v[52:55], v[178:181], v[186:189], v[52:55]
	v_mfma_f32_16x16x32_bf16 v[44:47], v[170:173], v[194:197], v[44:47]
	v_mfma_f32_16x16x32_bf16 v[36:39], v[178:181], v[194:197], v[36:39]
	v_mfma_f32_16x16x32_bf16 v[28:31], v[170:173], v[226:229], v[28:31]
	v_mfma_f32_16x16x32_bf16 v[20:23], v[178:181], v[226:229], v[20:23]
	v_mfma_f32_16x16x32_bf16 v[12:15], v[170:173], v[234:237], v[12:15]
	v_mfma_f32_16x16x32_bf16 v[4:7], v[178:181], v[234:237], v[4:7]
	s_setprio 0
	s_barrier
	s_add_i32 s54, 0, 0x18000
	s_add_i32 s55, 0, 0x1c000
	v_add_u32_e32 v162, s54, v147
	v_add_u32_e32 v178, s55, v147
	ds_read_b128 v[150:153], v162
	ds_read_b128 v[154:157], v162 offset:1024
	ds_read_b128 v[158:161], v162 offset:2048
	ds_read_b128 v[162:165], v162 offset:3072
	ds_read_b128 v[166:169], v178
	ds_read_b128 v[170:173], v178 offset:1024
	ds_read_b128 v[174:177], v178 offset:2048
	ds_read_b128 v[178:181], v178 offset:3072
	s_add_u32 s26, s26, 0x40000
	s_addc_u32 s27, s27, 0
	s_mov_b32 m0, s43
	v_lshl_add_u64 v[244:245], s[26:27], 0, v[138:139]
	ds_read_b128 v[182:185], v149 offset:32768
	ds_read_b128 v[186:189], v149 offset:33792
	ds_read_b128 v[190:193], v149 offset:34816
	ds_read_b128 v[194:197], v149 offset:35840
	ds_read_b128 v[210:213], v149 offset:36864
	ds_read_b128 v[226:229], v149 offset:37888
	ds_read_b128 v[230:233], v149 offset:38912
	s_mov_b32 m0, s41
	ds_read_b128 v[234:237], v149 offset:39936
	global_load_lds_dwordx4 v[240:241], off
	s_mov_b32 m0, s42
	s_nop 0
	global_load_lds_dwordx4 v[242:243], off
	s_mov_b32 m0, s43
	s_nop 0
	global_load_lds_dwordx4 v[244:245], off
	s_mov_b32 m0, s44
	v_lshl_add_u64 v[244:245], s[26:27], 0, v[134:135]
	global_load_lds_dwordx4 v[244:245], off
	s_waitcnt vmcnt(8)
	s_waitcnt lgkmcnt(0)
	s_barrier
	s_setprio 1
	s_waitcnt lgkmcnt(0)
	v_mfma_f32_16x16x32_bf16 v[128:131], v[150:153], v[182:185], v[128:131]
	v_mfma_f32_16x16x32_bf16 v[120:123], v[158:161], v[182:185], v[120:123]
	v_mfma_f32_16x16x32_bf16 v[112:115], v[150:153], v[190:193], v[112:115]
	v_mfma_f32_16x16x32_bf16 v[104:107], v[158:161], v[190:193], v[104:107]
	v_mfma_f32_16x16x32_bf16 v[96:99], v[150:153], v[210:213], v[96:99]
	v_mfma_f32_16x16x32_bf16 v[88:91], v[158:161], v[210:213], v[88:91]
	v_mfma_f32_16x16x32_bf16 v[80:83], v[150:153], v[230:233], v[80:83]
	v_mfma_f32_16x16x32_bf16 v[72:75], v[158:161], v[230:233], v[72:75]
	v_mfma_f32_16x16x32_bf16 v[128:131], v[154:157], v[186:189], v[128:131]
	v_mfma_f32_16x16x32_bf16 v[120:123], v[162:165], v[186:189], v[120:123]
	v_mfma_f32_16x16x32_bf16 v[112:115], v[154:157], v[194:197], v[112:115]
	v_mfma_f32_16x16x32_bf16 v[104:107], v[162:165], v[194:197], v[104:107]
	v_mfma_f32_16x16x32_bf16 v[96:99], v[154:157], v[226:229], v[96:99]
	v_mfma_f32_16x16x32_bf16 v[88:91], v[162:165], v[226:229], v[88:91]
	v_mfma_f32_16x16x32_bf16 v[80:83], v[154:157], v[234:237], v[80:83]
	v_mfma_f32_16x16x32_bf16 v[72:75], v[162:165], v[234:237], v[72:75]
	s_setprio 0
	s_setprio 1
	v_mfma_f32_16x16x32_bf16 v[124:127], v[166:169], v[182:185], v[124:127]
	v_mfma_f32_16x16x32_bf16 v[116:119], v[174:177], v[182:185], v[116:119]
	v_mfma_f32_16x16x32_bf16 v[108:111], v[166:169], v[190:193], v[108:111]
	v_mfma_f32_16x16x32_bf16 v[100:103], v[174:177], v[190:193], v[100:103]
	v_mfma_f32_16x16x32_bf16 v[92:95], v[166:169], v[210:213], v[92:95]
	v_mfma_f32_16x16x32_bf16 v[84:87], v[174:177], v[210:213], v[84:87]
	v_mfma_f32_16x16x32_bf16 v[76:79], v[166:169], v[230:233], v[76:79]
	v_mfma_f32_16x16x32_bf16 v[68:71], v[174:177], v[230:233], v[68:71]
	v_mfma_f32_16x16x32_bf16 v[124:127], v[170:173], v[186:189], v[124:127]
	v_mfma_f32_16x16x32_bf16 v[116:119], v[178:181], v[186:189], v[116:119]
	v_mfma_f32_16x16x32_bf16 v[108:111], v[170:173], v[194:197], v[108:111]
	v_mfma_f32_16x16x32_bf16 v[100:103], v[178:181], v[194:197], v[100:103]
	v_mfma_f32_16x16x32_bf16 v[92:95], v[170:173], v[226:229], v[92:95]
	v_mfma_f32_16x16x32_bf16 v[84:87], v[178:181], v[226:229], v[84:87]
	v_mfma_f32_16x16x32_bf16 v[76:79], v[170:173], v[234:237], v[76:79]
	v_mfma_f32_16x16x32_bf16 v[68:71], v[178:181], v[234:237], v[68:71]
	s_setprio 0
	s_barrier
; #define PG8_STAGE(bufoff, gbase, voff) do { _Pragma("unroll") for (int _i = 0; _i < 2; ++_i) \
;         __builtin_amdgcn_global_load_lds((const unsigned*)((const char*)(gbase) + (voff)[_i]), (PG8_LAS unsigned*)(lds + (bufoff) + ldsw + _i * 8192), 16, 0, 0); } while (0)
; #define PG8_LDA(dst, b, h) do { _Pragma("unroll") for (int m = 0; m < 4; ++m) _Pragma("unroll") for (int k = 0; k < 2; ++k) dst[m][k] = *(const PG8_LAS bf16x8*)(lds + PG8_SA(b, h) + aoff + m * 2048 + k * 1024); } while (0)
; #define PG8_LDB(dst, b, h) do { _Pragma("unroll") for (int n = 0; n < 2; ++n) _Pragma("unroll") for (int k = 0; k < 2; ++k) dst[n][k] = *(const PG8_LAS bf16x8*)(lds + PG8_SB(b, h) + boff + n * 2048 + k * 1024); } while (0)
; #define PG8_MMA(ai, bj, At, Bt) do { __builtin_amdgcn_s_setprio(1); _Pragma("unroll") for (int m = 0; m < 4; ++m) _Pragma("unroll") for (int n = 0; n < 2; ++n) _Pragma("unroll") for (int k = 0; k < 2; ++k) \
;         acc[ai][bj][m][n] = __builtin_amdgcn_mfma_f32_16x16x32_bf16(Bt[n][k], At[m][k], acc[ai][bj][m][n], 0, 0, 0); __builtin_amdgcn_s_setprio(0); } while (0)
; #define PG8_WAIT_V(n) asm volatile("s_waitcnt vmcnt(" #n ")" ::: "memory")
; #define PG8_WAIT_L(n) asm volatile("s_waitcnt lgkmcnt(" #n ")" ::: "memory")
; template <class Epi, class Sched, bool ALIGN_EPI = false, bool SP2 = false>
; __device__ __forceinline__ void gemm_phase(PG8_LAS unsigned char* lds, const Gemm g, const Sched& S, const Epi& E) {
;     ...
;             const bool last = (t == nt - 2);
;             const char* a1 = cA + (size_t)(t + 1) * kstep;
;             const char* a2 = last ? nA : cA + (size_t)(t + 2) * kstep; const char* b2 = last ? nB : cB + (size_t)(t + 2) * kstep;
;             const char* a3 = a2 + kstep; const char* b3 = b2 + kstep;
;             if (last && has_next) S.a_ready(nxt);
;             if constexpr (SP2) {
;             PG8_LDB(B0, 0, 0); PG8_LDB(B1, 0, 1); PG8_SCHED; PG8_LDA(At, 0, 0); PG8_STAGE(PG8_SA(1, 1), a1 + hstepA, voffA);
;             PG8_WAIT_V(8); PG8_WAIT_L(0); PG8_BAR; PG8_MMA(0, 0, At, B0); PG8_MMA(0, 1, At, B1); PG8_BAR; PG8_SCHED;
;     ...
;             PG8_LDA(At, 1, 1); PG8_STAGE(PG8_SB(1, 0), b3, voffB); PG8_STAGE(PG8_SB(1, 1), b3 + hstepB, voffB); PG8_STAGE(PG8_SA(1, 0), a3, voffA);
;             PG8_WAIT_V(8); PG8_WAIT_L(0); PG8_BAR; PG8_MMA(1, 0, At, B0); PG8_MMA(1, 1, At, B1); PG8_BAR; PG8_SCHED;
	s_add_i32 s26, s54, s39
	v_lshl_add_u64 v[144:145], v[144:145], 0, s[64:65]
	s_mov_b32 m0, s26
	ds_read_b128 v[182:185], v149 offset:49152
	ds_read_b128 v[186:189], v149 offset:50176
	ds_read_b128 v[190:193], v149 offset:51200
	ds_read_b128 v[194:197], v149 offset:52224
	ds_read_b128 v[210:213], v149 offset:53248
	ds_read_b128 v[226:229], v149 offset:54272
	ds_read_b128 v[230:233], v149 offset:55296
	ds_read_b128 v[234:237], v149 offset:56320
	global_load_lds_dwordx4 v[144:145], off
	s_add_i32 m0, s26, 0x2000
	s_add_u32 s24, s24, 0x40080
	v_lshl_add_u64 v[144:145], v[238:239], 0, s[64:65]
	s_addc_u32 s25, s25, 0
	s_add_i32 s26, s55, s39
	global_load_lds_dwordx4 v[144:145], off
	s_mov_b32 m0, s26
	v_lshl_add_u64 v[144:145], s[24:25], 0, v[136:137]
	global_load_lds_dwordx4 v[144:145], off
	s_add_i32 m0, s26, 0x2000
	v_lshl_add_u64 v[144:145], s[24:25], 0, v[132:133]
	global_load_lds_dwordx4 v[144:145], off
	s_waitcnt vmcnt(6)
	s_waitcnt lgkmcnt(0)
	s_barrier
	s_setprio 1
	s_waitcnt lgkmcnt(0)
	v_mfma_f32_16x16x32_bf16 v[64:67], v[150:153], v[182:185], v[64:67]
	v_mfma_f32_16x16x32_bf16 v[56:59], v[158:161], v[182:185], v[56:59]
	v_mfma_f32_16x16x32_bf16 v[48:51], v[150:153], v[190:193], v[48:51]
	v_mfma_f32_16x16x32_bf16 v[40:43], v[158:161], v[190:193], v[40:43]
	v_mfma_f32_16x16x32_bf16 v[32:35], v[150:153], v[210:213], v[32:35]
	v_mfma_f32_16x16x32_bf16 v[24:27], v[158:161], v[210:213], v[24:27]
	v_mfma_f32_16x16x32_bf16 v[16:19], v[150:153], v[230:233], v[16:19]
	v_mfma_f32_16x16x32_bf16 v[8:11], v[158:161], v[230:233], v[8:11]
	v_mfma_f32_16x16x32_bf16 v[64:67], v[154:157], v[186:189], v[64:67]
	v_mfma_f32_16x16x32_bf16 v[56:59], v[162:165], v[186:189], v[56:59]
	v_mfma_f32_16x16x32_bf16 v[48:51], v[154:157], v[194:197], v[48:51]
	v_mfma_f32_16x16x32_bf16 v[40:43], v[162:165], v[194:197], v[40:43]
	v_mfma_f32_16x16x32_bf16 v[32:35], v[154:157], v[226:229], v[32:35]
	v_mfma_f32_16x16x32_bf16 v[24:27], v[162:165], v[226:229], v[24:27]
	v_mfma_f32_16x16x32_bf16 v[16:19], v[154:157], v[234:237], v[16:19]
	v_mfma_f32_16x16x32_bf16 v[8:11], v[162:165], v[234:237], v[8:11]
	s_setprio 0
	s_setprio 1
	v_mfma_f32_16x16x32_bf16 v[60:63], v[166:169], v[182:185], v[60:63]
	v_mfma_f32_16x16x32_bf16 v[52:55], v[174:177], v[182:185], v[52:55]
	v_mfma_f32_16x16x32_bf16 v[44:47], v[166:169], v[190:193], v[44:47]
	v_mfma_f32_16x16x32_bf16 v[36:39], v[174:177], v[190:193], v[36:39]
	v_mfma_f32_16x16x32_bf16 v[28:31], v[166:169], v[210:213], v[28:31]
	v_mfma_f32_16x16x32_bf16 v[20:23], v[174:177], v[210:213], v[20:23]
	v_mfma_f32_16x16x32_bf16 v[12:15], v[166:169], v[230:233], v[12:15]
	v_mfma_f32_16x16x32_bf16 v[4:7], v[174:177], v[230:233], v[4:7]
	v_mfma_f32_16x16x32_bf16 v[60:63], v[170:173], v[186:189], v[60:63]
	v_mfma_f32_16x16x32_bf16 v[52:55], v[178:181], v[186:189], v[52:55]
	v_mfma_f32_16x16x32_bf16 v[44:47], v[170:173], v[194:197], v[44:47]
	v_mfma_f32_16x16x32_bf16 v[36:39], v[178:181], v[194:197], v[36:39]
	v_mfma_f32_16x16x32_bf16 v[28:31], v[170:173], v[226:229], v[28:31]
	v_mfma_f32_16x16x32_bf16 v[20:23], v[178:181], v[226:229], v[20:23]
	v_mfma_f32_16x16x32_bf16 v[12:15], v[170:173], v[234:237], v[12:15]
	v_mfma_f32_16x16x32_bf16 v[4:7], v[178:181], v[234:237], v[4:7]
	s_setprio 0
	s_barrier
	s_add_i32 s53, s53, 2
	s_add_u32 s51, s51, 0x100
	s_addc_u32 s52, s52, 0
	s_add_u32 s22, s22, 0x100
	s_addc_u32 s23, s23, 0
	s_cmp_gt_u32 s53, 13
	s_cbranch_scc1 .Lpeel_exit_0
.LBB0_153:
	s_add_u32 s24, s22, 0xfffc0080
	s_addc_u32 s25, s23, -1
	s_add_i32 s54, 0, 0x10000
	s_cmp_eq_u32 s53, 12
	s_cselect_b32 s27, s15, s25
	s_cselect_b32 s26, s49, s24
	v_add_u32_e32 v144, s54, v147
	s_cselect_b32 s25, s13, s52
	s_cselect_b32 s24, s50, s51
	s_add_i32 s56, 0, 0x14000
	ds_read_b128 v[150:153], v144
	ds_read_b128 v[154:157], v144 offset:1024
	ds_read_b128 v[158:161], v144 offset:2048
	ds_read_b128 v[162:165], v144 offset:3072
	v_add_u32_e32 v144, s56, v147
	ds_read_b128 v[166:169], v144
	ds_read_b128 v[170:173], v144 offset:1024
	ds_read_b128 v[174:177], v144 offset:2048
	ds_read_b128 v[178:181], v144 offset:3072
	v_lshl_add_u64 v[144:145], s[22:23], 0, v[142:143]
	s_add_i32 m0, s41, 0xc000
	ds_read_b128 v[182:185], v149
	ds_read_b128 v[186:189], v149 offset:1024
	ds_read_b128 v[190:193], v149 offset:2048
	ds_read_b128 v[194:197], v149 offset:3072
	ds_read_b128 v[210:213], v149 offset:4096
	ds_read_b128 v[226:229], v149 offset:5120
	ds_read_b128 v[230:233], v149 offset:6144
	ds_read_b128 v[234:237], v149 offset:7168
	s_mov_b32 m0, s45
	v_lshl_add_u64 v[244:245], v[240:241], 0, s[64:65]
	global_load_lds_dwordx4 v[244:245], off
	s_mov_b32 m0, s46
	v_lshl_add_u64 v[244:245], v[242:243], 0, s[64:65]
	global_load_lds_dwordx4 v[244:245], off
	s_add_i32 m0, s41, 0xc000
	s_nop 0
	global_load_lds_dwordx4 v[144:145], off
	s_add_i32 m0, s41, 0xe000
	v_lshl_add_u64 v[144:145], s[22:23], 0, v[140:141]
	global_load_lds_dwordx4 v[144:145], off
	s_waitcnt vmcnt(8)
	s_waitcnt lgkmcnt(0)
	s_barrier
; #define PG8_STAGE(bufoff, gbase, voff) do { _Pragma("unroll") for (int _i = 0; _i < 2; ++_i) \
;         __builtin_amdgcn_global_load_lds((const unsigned*)((const char*)(gbase) + (voff)[_i]), (PG8_LAS unsigned*)(lds + (bufoff) + ldsw + _i * 8192), 16, 0, 0); } while (0)
; #define PG8_LDA(dst, b, h) do { _Pragma("unroll") for (int m = 0; m < 4; ++m) _Pragma("unroll") for (int k = 0; k < 2; ++k) dst[m][k] = *(const PG8_LAS bf16x8*)(lds + PG8_SA(b, h) + aoff + m * 2048 + k * 1024); } while (0)
; #define PG8_MMA(ai, bj, At, Bt) do { __builtin_amdgcn_s_setprio(1); _Pragma("unroll") for (int m = 0; m < 4; ++m) _Pragma("unroll") for (int n = 0; n < 2; ++n) _Pragma("unroll") for (int k = 0; k < 2; ++k) \
;         acc[ai][bj][m][n] = __builtin_amdgcn_mfma_f32_16x16x32_bf16(Bt[n][k], At[m][k], acc[ai][bj][m][n], 0, 0, 0); __builtin_amdgcn_s_setprio(0); } while (0)
; #define PG8_WAIT_V(n) asm volatile("s_waitcnt vmcnt(" #n ")" ::: "memory")
; #define PG8_WAIT_L(n) asm volatile("s_waitcnt lgkmcnt(" #n ")" ::: "memory")
; #define PG8_BAR __builtin_amdgcn_s_barrier()
; #define PG8_SCHED __builtin_amdgcn_sched_barrier(0)
; template <class Epi, class Sched, bool ALIGN_EPI = false, bool SP2 = false>
; __device__ __forceinline__ void gemm_phase(PG8_LAS unsigned char* lds, const Gemm g, const Sched& S, const Epi& E) {
;     ...
;             PG8_WAIT_V(8); PG8_WAIT_L(0); PG8_BAR; PG8_MMA(0, 0, At, B0); PG8_MMA(0, 1, At, B1); PG8_BAR; PG8_SCHED;
;             PG8_LDA(At, 0, 1); PG8_STAGE(PG8_SB(0, 0), b2, voffB); PG8_STAGE(PG8_SB(0, 1), b2 + hstepB, voffB); PG8_STAGE(PG8_SA(0, 0), a2, voffA);
;             PG8_WAIT_V(8); PG8_WAIT_L(0); PG8_BAR; PG8_MMA(1, 0, At, B0); PG8_MMA(1, 1, At, B1); PG8_BAR; PG8_SCHED;
	s_setprio 1
	s_waitcnt lgkmcnt(0)
	v_mfma_f32_16x16x32_bf16 v[128:131], v[150:153], v[182:185], v[128:131]
	v_mfma_f32_16x16x32_bf16 v[120:123], v[158:161], v[182:185], v[120:123]
	v_mfma_f32_16x16x32_bf16 v[112:115], v[150:153], v[190:193], v[112:115]
	v_mfma_f32_16x16x32_bf16 v[104:107], v[158:161], v[190:193], v[104:107]
	v_mfma_f32_16x16x32_bf16 v[96:99], v[150:153], v[210:213], v[96:99]
	v_mfma_f32_16x16x32_bf16 v[88:91], v[158:161], v[210:213], v[88:91]
	v_mfma_f32_16x16x32_bf16 v[80:83], v[150:153], v[230:233], v[80:83]
	v_mfma_f32_16x16x32_bf16 v[72:75], v[158:161], v[230:233], v[72:75]
	v_mfma_f32_16x16x32_bf16 v[128:131], v[154:157], v[186:189], v[128:131]
	v_mfma_f32_16x16x32_bf16 v[120:123], v[162:165], v[186:189], v[120:123]
	v_mfma_f32_16x16x32_bf16 v[112:115], v[154:157], v[194:197], v[112:115]
	v_mfma_f32_16x16x32_bf16 v[104:107], v[162:165], v[194:197], v[104:107]
	v_mfma_f32_16x16x32_bf16 v[96:99], v[154:157], v[226:229], v[96:99]
	v_mfma_f32_16x16x32_bf16 v[88:91], v[162:165], v[226:229], v[88:91]
	v_mfma_f32_16x16x32_bf16 v[80:83], v[154:157], v[234:237], v[80:83]
	v_mfma_f32_16x16x32_bf16 v[72:75], v[162:165], v[234:237], v[72:75]
	s_setprio 0
	s_setprio 1
	v_mfma_f32_16x16x32_bf16 v[124:127], v[166:169], v[182:185], v[124:127]
	v_mfma_f32_16x16x32_bf16 v[116:119], v[174:177], v[182:185], v[116:119]
	v_mfma_f32_16x16x32_bf16 v[108:111], v[166:169], v[190:193], v[108:111]
	v_mfma_f32_16x16x32_bf16 v[100:103], v[174:177], v[190:193], v[100:103]
	v_mfma_f32_16x16x32_bf16 v[92:95], v[166:169], v[210:213], v[92:95]
	v_mfma_f32_16x16x32_bf16 v[84:87], v[174:177], v[210:213], v[84:87]
	v_mfma_f32_16x16x32_bf16 v[76:79], v[166:169], v[230:233], v[76:79]
	v_mfma_f32_16x16x32_bf16 v[68:71], v[174:177], v[230:233], v[68:71]
	v_mfma_f32_16x16x32_bf16 v[124:127], v[170:173], v[186:189], v[124:127]
	v_mfma_f32_16x16x32_bf16 v[116:119], v[178:181], v[186:189], v[116:119]
	v_mfma_f32_16x16x32_bf16 v[108:111], v[170:173], v[194:197], v[108:111]
	v_mfma_f32_16x16x32_bf16 v[100:103], v[178:181], v[194:197], v[100:103]
	v_mfma_f32_16x16x32_bf16 v[92:95], v[170:173], v[226:229], v[92:95]
	v_mfma_f32_16x16x32_bf16 v[84:87], v[178:181], v[226:229], v[84:87]
	v_mfma_f32_16x16x32_bf16 v[76:79], v[170:173], v[234:237], v[76:79]
	v_mfma_f32_16x16x32_bf16 v[68:71], v[178:181], v[234:237], v[68:71]
	s_setprio 0
	s_barrier
	s_add_i32 s54, s54, s39
	v_lshl_add_u64 v[144:145], s[24:25], 0, v[136:137]
	s_mov_b32 m0, s54
	ds_read_b128 v[182:185], v149 offset:16384
	ds_read_b128 v[186:189], v149 offset:17408
	ds_read_b128 v[190:193], v149 offset:18432
	ds_read_b128 v[194:197], v149 offset:19456
	ds_read_b128 v[210:213], v149 offset:20480
	ds_read_b128 v[226:229], v149 offset:21504
	ds_read_b128 v[230:233], v149 offset:22528
	ds_read_b128 v[234:237], v149 offset:23552
	global_load_lds_dwordx4 v[144:145], off
	s_add_i32 m0, s54, 0x2000
	s_add_u32 s54, s24, 0x40000
	v_lshl_add_u64 v[238:239], s[24:25], 0, v[132:133]
	s_addc_u32 s55, s25, 0
	s_add_i32 s56, s56, s39
	global_load_lds_dwordx4 v[238:239], off
	v_lshl_add_u64 v[240:241], s[54:55], 0, v[136:137]
	s_mov_b32 m0, s56
	v_lshl_add_u64 v[242:243], s[26:27], 0, v[134:135]
	global_load_lds_dwordx4 v[240:241], off
	s_add_i32 m0, s56, 0x2000
	v_lshl_add_u64 v[240:241], s[54:55], 0, v[132:133]
	global_load_lds_dwordx4 v[240:241], off
	v_lshl_add_u64 v[240:241], s[26:27], 0, v[138:139]
	s_waitcnt vmcnt(6)
	s_waitcnt lgkmcnt(0)
	s_barrier
	s_setprio 1
	s_waitcnt lgkmcnt(0)
	v_mfma_f32_16x16x32_bf16 v[64:67], v[150:153], v[182:185], v[64:67]
	v_mfma_f32_16x16x32_bf16 v[56:59], v[158:161], v[182:185], v[56:59]
	v_mfma_f32_16x16x32_bf16 v[48:51], v[150:153], v[190:193], v[48:51]
	v_mfma_f32_16x16x32_bf16 v[40:43], v[158:161], v[190:193], v[40:43]
	v_mfma_f32_16x16x32_bf16 v[32:35], v[150:153], v[210:213], v[32:35]
	v_mfma_f32_16x16x32_bf16 v[24:27], v[158:161], v[210:213], v[24:27]
	v_mfma_f32_16x16x32_bf16 v[16:19], v[150:153], v[230:233], v[16:19]
	v_mfma_f32_16x16x32_bf16 v[8:11], v[158:161], v[230:233], v[8:11]
	v_mfma_f32_16x16x32_bf16 v[64:67], v[154:157], v[186:189], v[64:67]
	v_mfma_f32_16x16x32_bf16 v[56:59], v[162:165], v[186:189], v[56:59]
	v_mfma_f32_16x16x32_bf16 v[48:51], v[154:157], v[194:197], v[48:51]
	v_mfma_f32_16x16x32_bf16 v[40:43], v[162:165], v[194:197], v[40:43]
	v_mfma_f32_16x16x32_bf16 v[32:35], v[154:157], v[226:229], v[32:35]
	v_mfma_f32_16x16x32_bf16 v[24:27], v[162:165], v[226:229], v[24:27]
	v_mfma_f32_16x16x32_bf16 v[16:19], v[154:157], v[234:237], v[16:19]
	v_mfma_f32_16x16x32_bf16 v[8:11], v[162:165], v[234:237], v[8:11]
	s_setprio 0
	s_setprio 1
	v_mfma_f32_16x16x32_bf16 v[60:63], v[166:169], v[182:185], v[60:63]
	v_mfma_f32_16x16x32_bf16 v[52:55], v[174:177], v[182:185], v[52:55]
	v_mfma_f32_16x16x32_bf16 v[44:47], v[166:169], v[190:193], v[44:47]
	v_mfma_f32_16x16x32_bf16 v[36:39], v[174:177], v[190:193], v[36:39]
	v_mfma_f32_16x16x32_bf16 v[28:31], v[166:169], v[210:213], v[28:31]
	v_mfma_f32_16x16x32_bf16 v[20:23], v[174:177], v[210:213], v[20:23]
	v_mfma_f32_16x16x32_bf16 v[12:15], v[166:169], v[230:233], v[12:15]
	v_mfma_f32_16x16x32_bf16 v[4:7], v[174:177], v[230:233], v[4:7]
	v_mfma_f32_16x16x32_bf16 v[60:63], v[170:173], v[186:189], v[60:63]
	v_mfma_f32_16x16x32_bf16 v[52:55], v[178:181], v[186:189], v[52:55]
	v_mfma_f32_16x16x32_bf16 v[44:47], v[170:173], v[194:197], v[44:47]
	v_mfma_f32_16x16x32_bf16 v[36:39], v[178:181], v[194:197], v[36:39]
	v_mfma_f32_16x16x32_bf16 v[28:31], v[170:173], v[226:229], v[28:31]
	v_mfma_f32_16x16x32_bf16 v[20:23], v[178:181], v[226:229], v[20:23]
	v_mfma_f32_16x16x32_bf16 v[12:15], v[170:173], v[234:237], v[12:15]
	v_mfma_f32_16x16x32_bf16 v[4:7], v[178:181], v[234:237], v[4:7]
	s_setprio 0
	s_barrier
; #define PG8_STAGE(bufoff, gbase, voff) do { _Pragma("unroll") for (int _i = 0; _i < 2; ++_i) \
;         __builtin_amdgcn_global_load_lds((const unsigned*)((const char*)(gbase) + (voff)[_i]), (PG8_LAS unsigned*)(lds + (bufoff) + ldsw + _i * 8192), 16, 0, 0); } while (0)
; #define PG8_LDA(dst, b, h) do { _Pragma("unroll") for (int m = 0; m < 4; ++m) _Pragma("unroll") for (int k = 0; k < 2; ++k) dst[m][k] = *(const PG8_LAS bf16x8*)(lds + PG8_SA(b, h) + aoff + m * 2048 + k * 1024); } while (0)
; #define PG8_LDB(dst, b, h) do { _Pragma("unroll") for (int n = 0; n < 2; ++n) _Pragma("unroll") for (int k = 0; k < 2; ++k) dst[n][k] = *(const PG8_LAS bf16x8*)(lds + PG8_SB(b, h) + boff + n * 2048 + k * 1024); } while (0)
; #define PG8_MMA(ai, bj, At, Bt) do { __builtin_amdgcn_s_setprio(1); _Pragma("unroll") for (int m = 0; m < 4; ++m) _Pragma("unroll") for (int n = 0; n < 2; ++n) _Pragma("unroll") for (int k = 0; k < 2; ++k) \
;         acc[ai][bj][m][n] = __builtin_amdgcn_mfma_f32_16x16x32_bf16(Bt[n][k], At[m][k], acc[ai][bj][m][n], 0, 0, 0); __builtin_amdgcn_s_setprio(0); } while (0)
; #define PG8_WAIT_V(n) asm volatile("s_waitcnt vmcnt(" #n ")" ::: "memory")
; #define PG8_WAIT_L(n) asm volatile("s_waitcnt lgkmcnt(" #n ")" ::: "memory")
; #define PG8_BAR __builtin_amdgcn_s_barrier()
; #define PG8_SCHED __builtin_amdgcn_sched_barrier(0)
; template <class Epi, class Sched, bool ALIGN_EPI = false, bool SP2 = false>
; __device__ __forceinline__ void gemm_phase(PG8_LAS unsigned char* lds, const Gemm g, const Sched& S, const Epi& E) {
;     ...
;             PG8_LDB(B0, 1, 0); PG8_LDB(B1, 1, 1); PG8_SCHED; PG8_LDA(At, 1, 0); PG8_STAGE(PG8_SA(0, 1), a2 + hstepA, voffA);
;             PG8_WAIT_V(8); PG8_WAIT_L(0); PG8_BAR; PG8_MMA(0, 0, At, B0); PG8_MMA(0, 1, At, B1); PG8_BAR; PG8_SCHED;
	s_add_i32 s54, 0, 0x18000
	s_add_i32 s55, 0, 0x1c000
	v_add_u32_e32 v162, s54, v147
	v_add_u32_e32 v178, s55, v147
	ds_read_b128 v[150:153], v162
	ds_read_b128 v[154:157], v162 offset:1024
	ds_read_b128 v[158:161], v162 offset:2048
	ds_read_b128 v[162:165], v162 offset:3072
	ds_read_b128 v[166:169], v178
	ds_read_b128 v[170:173], v178 offset:1024
	ds_read_b128 v[174:177], v178 offset:2048
	ds_read_b128 v[178:181], v178 offset:3072
	s_add_u32 s26, s26, 0x40000
	s_addc_u32 s27, s27, 0
	s_mov_b32 m0, s43
	v_lshl_add_u64 v[244:245], s[26:27], 0, v[138:139]
	ds_read_b128 v[182:185], v149 offset:32768
	ds_read_b128 v[186:189], v149 offset:33792
	ds_read_b128 v[190:193], v149 offset:34816
	ds_read_b128 v[194:197], v149 offset:35840
	ds_read_b128 v[210:213], v149 offset:36864
	ds_read_b128 v[226:229], v149 offset:37888
	ds_read_b128 v[230:233], v149 offset:38912
	s_mov_b32 m0, s41
	ds_read_b128 v[234:237], v149 offset:39936
	global_load_lds_dwordx4 v[240:241], off
	s_mov_b32 m0, s42
	s_nop 0
	global_load_lds_dwordx4 v[242:243], off
	s_mov_b32 m0, s43
	s_nop 0
	global_load_lds_dwordx4 v[244:245], off
	s_mov_b32 m0, s44
	v_lshl_add_u64 v[244:245], s[26:27], 0, v[134:135]
	global_load_lds_dwordx4 v[244:245], off
	s_waitcnt vmcnt(8)
	s_waitcnt lgkmcnt(0)
	s_barrier
	s_setprio 1
	s_waitcnt lgkmcnt(0)
	v_mfma_f32_16x16x32_bf16 v[128:131], v[150:153], v[182:185], v[128:131]
	v_mfma_f32_16x16x32_bf16 v[120:123], v[158:161], v[182:185], v[120:123]
	v_mfma_f32_16x16x32_bf16 v[112:115], v[150:153], v[190:193], v[112:115]
	v_mfma_f32_16x16x32_bf16 v[104:107], v[158:161], v[190:193], v[104:107]
	v_mfma_f32_16x16x32_bf16 v[96:99], v[150:153], v[210:213], v[96:99]
	v_mfma_f32_16x16x32_bf16 v[88:91], v[158:161], v[210:213], v[88:91]
	v_mfma_f32_16x16x32_bf16 v[80:83], v[150:153], v[230:233], v[80:83]
	v_mfma_f32_16x16x32_bf16 v[72:75], v[158:161], v[230:233], v[72:75]
	v_mfma_f32_16x16x32_bf16 v[128:131], v[154:157], v[186:189], v[128:131]
	v_mfma_f32_16x16x32_bf16 v[120:123], v[162:165], v[186:189], v[120:123]
	v_mfma_f32_16x16x32_bf16 v[112:115], v[154:157], v[194:197], v[112:115]
	v_mfma_f32_16x16x32_bf16 v[104:107], v[162:165], v[194:197], v[104:107]
	v_mfma_f32_16x16x32_bf16 v[96:99], v[154:157], v[226:229], v[96:99]
	v_mfma_f32_16x16x32_bf16 v[88:91], v[162:165], v[226:229], v[88:91]
	v_mfma_f32_16x16x32_bf16 v[80:83], v[154:157], v[234:237], v[80:83]
	v_mfma_f32_16x16x32_bf16 v[72:75], v[162:165], v[234:237], v[72:75]
	s_setprio 0
	s_setprio 1
	v_mfma_f32_16x16x32_bf16 v[124:127], v[166:169], v[182:185], v[124:127]
	v_mfma_f32_16x16x32_bf16 v[116:119], v[174:177], v[182:185], v[116:119]
	v_mfma_f32_16x16x32_bf16 v[108:111], v[166:169], v[190:193], v[108:111]
	v_mfma_f32_16x16x32_bf16 v[100:103], v[174:177], v[190:193], v[100:103]
	v_mfma_f32_16x16x32_bf16 v[92:95], v[166:169], v[210:213], v[92:95]
	v_mfma_f32_16x16x32_bf16 v[84:87], v[174:177], v[210:213], v[84:87]
	v_mfma_f32_16x16x32_bf16 v[76:79], v[166:169], v[230:233], v[76:79]
	v_mfma_f32_16x16x32_bf16 v[68:71], v[174:177], v[230:233], v[68:71]
	v_mfma_f32_16x16x32_bf16 v[124:127], v[170:173], v[186:189], v[124:127]
	v_mfma_f32_16x16x32_bf16 v[116:119], v[178:181], v[186:189], v[116:119]
	v_mfma_f32_16x16x32_bf16 v[108:111], v[170:173], v[194:197], v[108:111]
	v_mfma_f32_16x16x32_bf16 v[100:103], v[178:181], v[194:197], v[100:103]
	v_mfma_f32_16x16x32_bf16 v[92:95], v[170:173], v[226:229], v[92:95]
	v_mfma_f32_16x16x32_bf16 v[84:87], v[178:181], v[226:229], v[84:87]
	v_mfma_f32_16x16x32_bf16 v[76:79], v[170:173], v[234:237], v[76:79]
	v_mfma_f32_16x16x32_bf16 v[68:71], v[178:181], v[234:237], v[68:71]
	s_setprio 0
	s_barrier
; #define PG8_STAGE(bufoff, gbase, voff) do { _Pragma("unroll") for (int _i = 0; _i < 2; ++_i) \
;         __builtin_amdgcn_global_load_lds((const unsigned*)((const char*)(gbase) + (voff)[_i]), (PG8_LAS unsigned*)(lds + (bufoff) + ldsw + _i * 8192), 16, 0, 0); } while (0)
; #define PG8_LDA(dst, b, h) do { _Pragma("unroll") for (int m = 0; m < 4; ++m) _Pragma("unroll") for (int k = 0; k < 2; ++k) dst[m][k] = *(const PG8_LAS bf16x8*)(lds + PG8_SA(b, h) + aoff + m * 2048 + k * 1024); } while (0)
; #define PG8_MMA(ai, bj, At, Bt) do { __builtin_amdgcn_s_setprio(1); _Pragma("unroll") for (int m = 0; m < 4; ++m) _Pragma("unroll") for (int n = 0; n < 2; ++n) _Pragma("unroll") for (int k = 0; k < 2; ++k) \
;         acc[ai][bj][m][n] = __builtin_amdgcn_mfma_f32_16x16x32_bf16(Bt[n][k], At[m][k], acc[ai][bj][m][n], 0, 0, 0); __builtin_amdgcn_s_setprio(0); } while (0)
; #define PG8_WAIT_V(n) asm volatile("s_waitcnt vmcnt(" #n ")" ::: "memory")
; #define PG8_WAIT_L(n) asm volatile("s_waitcnt lgkmcnt(" #n ")" ::: "memory")
; #define PG8_BAR __builtin_amdgcn_s_barrier()
; #define PG8_SCHED __builtin_amdgcn_sched_barrier(0)
; template <class Epi, class Sched, bool ALIGN_EPI = false, bool SP2 = false>
; __device__ __forceinline__ void gemm_phase(PG8_LAS unsigned char* lds, const Gemm g, const Sched& S, const Epi& E) {
;     ...
;             PG8_LDA(At, 1, 1); PG8_STAGE(PG8_SB(1, 0), b3, voffB); PG8_STAGE(PG8_SB(1, 1), b3 + hstepB, voffB); PG8_STAGE(PG8_SA(1, 0), a3, voffA);
;             PG8_WAIT_V(8); PG8_WAIT_L(0); PG8_BAR; PG8_MMA(1, 0, At, B0); PG8_MMA(1, 1, At, B1); PG8_BAR; PG8_SCHED;
	s_add_i32 s26, s54, s39
	v_lshl_add_u64 v[144:145], v[144:145], 0, s[64:65]
	s_mov_b32 m0, s26
	ds_read_b128 v[182:185], v149 offset:49152
	ds_read_b128 v[186:189], v149 offset:50176
	ds_read_b128 v[190:193], v149 offset:51200
	ds_read_b128 v[194:197], v149 offset:52224
	ds_read_b128 v[210:213], v149 offset:53248
	ds_read_b128 v[226:229], v149 offset:54272
	ds_read_b128 v[230:233], v149 offset:55296
	ds_read_b128 v[234:237], v149 offset:56320
	global_load_lds_dwordx4 v[144:145], off
	s_add_i32 m0, s26, 0x2000
	s_add_u32 s24, s24, 0x40080
	v_lshl_add_u64 v[144:145], v[238:239], 0, s[64:65]
	s_addc_u32 s25, s25, 0
	s_add_i32 s26, s55, s39
	global_load_lds_dwordx4 v[144:145], off
	s_mov_b32 m0, s26
	v_lshl_add_u64 v[144:145], s[24:25], 0, v[136:137]
	global_load_lds_dwordx4 v[144:145], off
	s_add_i32 m0, s26, 0x2000
	v_lshl_add_u64 v[144:145], s[24:25], 0, v[132:133]
	global_load_lds_dwordx4 v[144:145], off
	s_waitcnt vmcnt(6)
	s_waitcnt lgkmcnt(0)
	s_barrier
	s_setprio 1
	s_waitcnt lgkmcnt(0)
	v_mfma_f32_16x16x32_bf16 v[64:67], v[150:153], v[182:185], v[64:67]
	v_mfma_f32_16x16x32_bf16 v[56:59], v[158:161], v[182:185], v[56:59]
	v_mfma_f32_16x16x32_bf16 v[48:51], v[150:153], v[190:193], v[48:51]
	v_mfma_f32_16x16x32_bf16 v[40:43], v[158:161], v[190:193], v[40:43]
	v_mfma_f32_16x16x32_bf16 v[32:35], v[150:153], v[210:213], v[32:35]
	v_mfma_f32_16x16x32_bf16 v[24:27], v[158:161], v[210:213], v[24:27]
	v_mfma_f32_16x16x32_bf16 v[16:19], v[150:153], v[230:233], v[16:19]
	v_mfma_f32_16x16x32_bf16 v[8:11], v[158:161], v[230:233], v[8:11]
	v_mfma_f32_16x16x32_bf16 v[64:67], v[154:157], v[186:189], v[64:67]
	v_mfma_f32_16x16x32_bf16 v[56:59], v[162:165], v[186:189], v[56:59]
	v_mfma_f32_16x16x32_bf16 v[48:51], v[154:157], v[194:197], v[48:51]
	v_mfma_f32_16x16x32_bf16 v[40:43], v[162:165], v[194:197], v[40:43]
	v_mfma_f32_16x16x32_bf16 v[32:35], v[154:157], v[226:229], v[32:35]
	v_mfma_f32_16x16x32_bf16 v[24:27], v[162:165], v[226:229], v[24:27]
	v_mfma_f32_16x16x32_bf16 v[16:19], v[154:157], v[234:237], v[16:19]
	v_mfma_f32_16x16x32_bf16 v[8:11], v[162:165], v[234:237], v[8:11]
	s_setprio 0
	s_setprio 1
	v_mfma_f32_16x16x32_bf16 v[60:63], v[166:169], v[182:185], v[60:63]
	v_mfma_f32_16x16x32_bf16 v[52:55], v[174:177], v[182:185], v[52:55]
	v_mfma_f32_16x16x32_bf16 v[44:47], v[166:169], v[190:193], v[44:47]
	v_mfma_f32_16x16x32_bf16 v[36:39], v[174:177], v[190:193], v[36:39]
	v_mfma_f32_16x16x32_bf16 v[28:31], v[166:169], v[210:213], v[28:31]
	v_mfma_f32_16x16x32_bf16 v[20:23], v[174:177], v[210:213], v[20:23]
	v_mfma_f32_16x16x32_bf16 v[12:15], v[166:169], v[230:233], v[12:15]
	v_mfma_f32_16x16x32_bf16 v[4:7], v[174:177], v[230:233], v[4:7]
	v_mfma_f32_16x16x32_bf16 v[60:63], v[170:173], v[186:189], v[60:63]
	v_mfma_f32_16x16x32_bf16 v[52:55], v[178:181], v[186:189], v[52:55]
	v_mfma_f32_16x16x32_bf16 v[44:47], v[170:173], v[194:197], v[44:47]
	v_mfma_f32_16x16x32_bf16 v[36:39], v[178:181], v[194:197], v[36:39]
	v_mfma_f32_16x16x32_bf16 v[28:31], v[170:173], v[226:229], v[28:31]
	v_mfma_f32_16x16x32_bf16 v[20:23], v[178:181], v[226:229], v[20:23]
	v_mfma_f32_16x16x32_bf16 v[12:15], v[170:173], v[234:237], v[12:15]
	v_mfma_f32_16x16x32_bf16 v[4:7], v[178:181], v[234:237], v[4:7]
	s_setprio 0
	s_barrier
	s_add_i32 s53, s53, 2
	s_add_u32 s51, s51, 0x100
	s_addc_u32 s52, s52, 0
	s_add_u32 s22, s22, 0x100
	s_addc_u32 s23, s23, 0
	s_cmp_gt_u32 s53, 13
	s_cbranch_scc0 .LBB0_153

; #define PG8_STAGE(bufoff, gbase, voff) do { _Pragma("unroll") for (int _i = 0; _i < 2; ++_i) \
;         __builtin_amdgcn_global_load_lds((const unsigned*)((const char*)(gbase) + (voff)[_i]), (PG8_LAS unsigned*)(lds + (bufoff) + ldsw + _i * 8192), 16, 0, 0); } while (0)
; #define PG8_LDA(dst, b, h) do { _Pragma("unroll") for (int m = 0; m < 4; ++m) _Pragma("unroll") for (int k = 0; k < 2; ++k) dst[m][k] = *(const PG8_LAS bf16x8*)(lds + PG8_SA(b, h) + aoff + m * 2048 + k * 1024); } while (0)
; #define PG8_LDB(dst, b, h) do { _Pragma("unroll") for (int n = 0; n < 2; ++n) _Pragma("unroll") for (int k = 0; k < 2; ++k) dst[n][k] = *(const PG8_LAS bf16x8*)(lds + PG8_SB(b, h) + boff + n * 2048 + k * 1024); } while (0)
; #define PG8_MMA(ai, bj, At, Bt) do { __builtin_amdgcn_s_setprio(1); _Pragma("unroll") for (int m = 0; m < 4; ++m) _Pragma("unroll") for (int n = 0; n < 2; ++n) _Pragma("unroll") for (int k = 0; k < 2; ++k) \
;         acc[ai][bj][m][n] = __builtin_amdgcn_mfma_f32_16x16x32_bf16(Bt[n][k], At[m][k], acc[ai][bj][m][n], 0, 0, 0); __builtin_amdgcn_s_setprio(0); } while (0)
; #define PG8_WAIT_V(n) asm volatile("s_waitcnt vmcnt(" #n ")" ::: "memory")
; #define PG8_WAIT_L(n) asm volatile("s_waitcnt lgkmcnt(" #n ")" ::: "memory")
; template <class Epi, class Sched, bool ALIGN_EPI = false, bool SP2 = false>
; __device__ __forceinline__ void gemm_phase(PG8_LAS unsigned char* lds, const Gemm g, const Sched& S, const Epi& E) {
;     ...
;             const bool last = (t == nt - 2);
;             const char* a1 = cA + (size_t)(t + 1) * kstep;
;             const char* a2 = last ? nA : cA + (size_t)(t + 2) * kstep; const char* b2 = last ? nB : cB + (size_t)(t + 2) * kstep;
;             const char* a3 = a2 + kstep; const char* b3 = b2 + kstep;
;             if (last && has_next) S.a_ready(nxt);
;             if constexpr (SP2) {
;             PG8_LDB(B0, 0, 0); PG8_LDB(B1, 0, 1); PG8_SCHED; PG8_LDA(At, 0, 0); PG8_STAGE(PG8_SA(1, 1), a1 + hstepA, voffA);
;             PG8_WAIT_V(8); PG8_WAIT_L(0); PG8_BAR; PG8_MMA(0, 0, At, B0); PG8_MMA(0, 1, At, B1); PG8_BAR; PG8_SCHED;
;             PG8_LDA(At, 0, 1); PG8_STAGE(PG8_SB(0, 0), b2, voffB); PG8_STAGE(PG8_SB(0, 1), b2 + hstepB, voffB); PG8_STAGE(PG8_SA(0, 0), a2, voffA);
;             PG8_WAIT_V(8); PG8_WAIT_L(0); PG8_BAR; PG8_MMA(1, 0, At, B0); PG8_MMA(1, 1, At, B1); PG8_BAR; PG8_SCHED;
.LBB0_669:
	s_add_u32 s16, s14, 0x100
	s_addc_u32 s17, s15, 0
	s_add_i32 s47, 0, 0x10000
	s_cmp_eq_u32 s46, 40
	s_cselect_b32 s21, s5, s17
	s_cselect_b32 s20, s4, s16
	v_add_u32_e32 v144, s47, v146
	s_cselect_b32 s19, s13, s45
	s_cselect_b32 s18, s12, s44
	s_add_i32 s48, 0, 0x14000
	ds_read_b128 v[150:153], v144
	ds_read_b128 v[154:157], v144 offset:1024
	ds_read_b128 v[158:161], v144 offset:2048
	ds_read_b128 v[162:165], v144 offset:3072
	v_add_u32_e32 v144, s48, v146
	ds_read_b128 v[166:169], v144
	ds_read_b128 v[170:173], v144 offset:1024
	ds_read_b128 v[174:177], v144 offset:2048
	ds_read_b128 v[178:181], v144 offset:3072
	v_lshl_add_u64 v[144:145], s[14:15], 0, v[142:143]
	s_add_i32 m0, s28, 0xc000
	ds_read_b128 v[182:185], v148
	ds_read_b128 v[186:189], v148 offset:1024
	ds_read_b128 v[190:193], v148 offset:2048
	ds_read_b128 v[194:197], v148 offset:3072
	ds_read_b128 v[210:213], v148 offset:4096
	ds_read_b128 v[226:229], v148 offset:5120
	ds_read_b128 v[230:233], v148 offset:6144
	ds_read_b128 v[234:237], v148 offset:7168
	s_mov_b32 m0, s33
	v_lshl_add_u64 v[244:245], v[240:241], 0, s[64:65]
	global_load_lds_dwordx4 v[244:245], off
	s_mov_b32 m0, s34
	v_lshl_add_u64 v[244:245], v[242:243], 0, s[64:65]
	global_load_lds_dwordx4 v[244:245], off
	s_add_i32 m0, s28, 0xc000
	s_nop 0
	global_load_lds_dwordx4 v[144:145], off
	s_add_i32 m0, s28, 0xe000
	v_lshl_add_u64 v[144:145], s[14:15], 0, v[140:141]
	global_load_lds_dwordx4 v[144:145], off
	s_waitcnt vmcnt(8)
	s_waitcnt lgkmcnt(0)
	s_barrier
	s_setprio 1
	s_waitcnt lgkmcnt(0)
	v_mfma_f32_16x16x32_bf16 v[128:131], v[150:153], v[182:185], v[128:131]
	v_mfma_f32_16x16x32_bf16 v[124:127], v[158:161], v[182:185], v[124:127]
	v_mfma_f32_16x16x32_bf16 v[120:123], v[150:153], v[190:193], v[120:123]
	v_mfma_f32_16x16x32_bf16 v[112:115], v[158:161], v[190:193], v[112:115]
	v_mfma_f32_16x16x32_bf16 v[104:107], v[150:153], v[210:213], v[104:107]
	v_mfma_f32_16x16x32_bf16 v[96:99], v[158:161], v[210:213], v[96:99]
	v_mfma_f32_16x16x32_bf16 v[88:91], v[150:153], v[230:233], v[88:91]
	v_mfma_f32_16x16x32_bf16 v[80:83], v[158:161], v[230:233], v[80:83]
	v_mfma_f32_16x16x32_bf16 v[128:131], v[154:157], v[186:189], v[128:131]
	v_mfma_f32_16x16x32_bf16 v[124:127], v[162:165], v[186:189], v[124:127]
	v_mfma_f32_16x16x32_bf16 v[120:123], v[154:157], v[194:197], v[120:123]
	v_mfma_f32_16x16x32_bf16 v[112:115], v[162:165], v[194:197], v[112:115]
	v_mfma_f32_16x16x32_bf16 v[104:107], v[154:157], v[226:229], v[104:107]
	v_mfma_f32_16x16x32_bf16 v[96:99], v[162:165], v[226:229], v[96:99]
	v_mfma_f32_16x16x32_bf16 v[88:91], v[154:157], v[234:237], v[88:91]
	v_mfma_f32_16x16x32_bf16 v[80:83], v[162:165], v[234:237], v[80:83]
	s_setprio 0
	s_setprio 1
	v_mfma_f32_16x16x32_bf16 v[116:119], v[166:169], v[182:185], v[116:119]
	v_mfma_f32_16x16x32_bf16 v[108:111], v[174:177], v[182:185], v[108:111]
	v_mfma_f32_16x16x32_bf16 v[100:103], v[166:169], v[190:193], v[100:103]
	v_mfma_f32_16x16x32_bf16 v[92:95], v[174:177], v[190:193], v[92:95]
	v_mfma_f32_16x16x32_bf16 v[84:87], v[166:169], v[210:213], v[84:87]
	v_mfma_f32_16x16x32_bf16 v[76:79], v[174:177], v[210:213], v[76:79]
	v_mfma_f32_16x16x32_bf16 v[72:75], v[166:169], v[230:233], v[72:75]
	v_mfma_f32_16x16x32_bf16 v[68:71], v[174:177], v[230:233], v[68:71]
	v_mfma_f32_16x16x32_bf16 v[116:119], v[170:173], v[186:189], v[116:119]
	v_mfma_f32_16x16x32_bf16 v[108:111], v[178:181], v[186:189], v[108:111]
	v_mfma_f32_16x16x32_bf16 v[100:103], v[170:173], v[194:197], v[100:103]
	v_mfma_f32_16x16x32_bf16 v[92:95], v[178:181], v[194:197], v[92:95]
	v_mfma_f32_16x16x32_bf16 v[84:87], v[170:173], v[226:229], v[84:87]
	v_mfma_f32_16x16x32_bf16 v[76:79], v[178:181], v[226:229], v[76:79]
	v_mfma_f32_16x16x32_bf16 v[72:75], v[170:173], v[234:237], v[72:75]
	v_mfma_f32_16x16x32_bf16 v[68:71], v[178:181], v[234:237], v[68:71]
	s_setprio 0
	s_barrier
	s_add_i32 s14, s47, s27
	v_lshl_add_u64 v[144:145], s[18:19], 0, v[134:135]
	s_mov_b32 m0, s14
	ds_read_b128 v[182:185], v148 offset:16384
	ds_read_b128 v[186:189], v148 offset:17408
	ds_read_b128 v[190:193], v148 offset:18432
	ds_read_b128 v[194:197], v148 offset:19456
	ds_read_b128 v[210:213], v148 offset:20480
	ds_read_b128 v[226:229], v148 offset:21504
	ds_read_b128 v[230:233], v148 offset:22528
	ds_read_b128 v[234:237], v148 offset:23552
	global_load_lds_dwordx4 v[144:145], off
	s_add_i32 m0, s14, 0x2000
	s_add_u32 s14, s18, 0xb0000
	v_lshl_add_u64 v[238:239], s[18:19], 0, v[138:139]
	s_addc_u32 s15, s19, 0
	s_add_i32 s47, s48, s27
	global_load_lds_dwordx4 v[238:239], off
	v_lshl_add_u64 v[240:241], s[14:15], 0, v[134:135]
	s_mov_b32 m0, s47
	v_lshl_add_u64 v[242:243], s[20:21], 0, v[136:137]
	global_load_lds_dwordx4 v[240:241], off
	s_add_i32 m0, s47, 0x2000
	v_lshl_add_u64 v[240:241], s[14:15], 0, v[138:139]
	global_load_lds_dwordx4 v[240:241], off
	v_lshl_add_u64 v[240:241], s[20:21], 0, v[132:133]
	s_waitcnt vmcnt(6)
	s_waitcnt lgkmcnt(0)
	s_barrier
; #define PG8_STAGE(bufoff, gbase, voff) do { _Pragma("unroll") for (int _i = 0; _i < 2; ++_i) \
;         __builtin_amdgcn_global_load_lds((const unsigned*)((const char*)(gbase) + (voff)[_i]), (PG8_LAS unsigned*)(lds + (bufoff) + ldsw + _i * 8192), 16, 0, 0); } while (0)
; #define PG8_LDA(dst, b, h) do { _Pragma("unroll") for (int m = 0; m < 4; ++m) _Pragma("unroll") for (int k = 0; k < 2; ++k) dst[m][k] = *(const PG8_LAS bf16x8*)(lds + PG8_SA(b, h) + aoff + m * 2048 + k * 1024); } while (0)
; #define PG8_LDB(dst, b, h) do { _Pragma("unroll") for (int n = 0; n < 2; ++n) _Pragma("unroll") for (int k = 0; k < 2; ++k) dst[n][k] = *(const PG8_LAS bf16x8*)(lds + PG8_SB(b, h) + boff + n * 2048 + k * 1024); } while (0)
; #define PG8_MMA(ai, bj, At, Bt) do { __builtin_amdgcn_s_setprio(1); _Pragma("unroll") for (int m = 0; m < 4; ++m) _Pragma("unroll") for (int n = 0; n < 2; ++n) _Pragma("unroll") for (int k = 0; k < 2; ++k) \
;         acc[ai][bj][m][n] = __builtin_amdgcn_mfma_f32_16x16x32_bf16(Bt[n][k], At[m][k], acc[ai][bj][m][n], 0, 0, 0); __builtin_amdgcn_s_setprio(0); } while (0)
; #define PG8_WAIT_V(n) asm volatile("s_waitcnt vmcnt(" #n ")" ::: "memory")
; #define PG8_WAIT_L(n) asm volatile("s_waitcnt lgkmcnt(" #n ")" ::: "memory")
; #define PG8_BAR __builtin_amdgcn_s_barrier()
; #define PG8_SCHED __builtin_amdgcn_sched_barrier(0)
; template <class Epi, class Sched, bool ALIGN_EPI = false, bool SP2 = false>
; __device__ __forceinline__ void gemm_phase(PG8_LAS unsigned char* lds, const Gemm g, const Sched& S, const Epi& E) {
;     ...
;             PG8_WAIT_V(8); PG8_WAIT_L(0); PG8_BAR; PG8_MMA(1, 0, At, B0); PG8_MMA(1, 1, At, B1); PG8_BAR; PG8_SCHED;
;             PG8_LDB(B0, 1, 0); PG8_LDB(B1, 1, 1); PG8_SCHED; PG8_LDA(At, 1, 0); PG8_STAGE(PG8_SA(0, 1), a2 + hstepA, voffA);
;             PG8_WAIT_V(8); PG8_WAIT_L(0); PG8_BAR; PG8_MMA(0, 0, At, B0); PG8_MMA(0, 1, At, B1); PG8_BAR; PG8_SCHED;
	s_setprio 1
	s_waitcnt lgkmcnt(0)
	v_mfma_f32_16x16x32_bf16 v[64:67], v[150:153], v[182:185], v[64:67]
	v_mfma_f32_16x16x32_bf16 v[60:63], v[158:161], v[182:185], v[60:63]
	v_mfma_f32_16x16x32_bf16 v[56:59], v[150:153], v[190:193], v[56:59]
	v_mfma_f32_16x16x32_bf16 v[48:51], v[158:161], v[190:193], v[48:51]
	v_mfma_f32_16x16x32_bf16 v[40:43], v[150:153], v[210:213], v[40:43]
	v_mfma_f32_16x16x32_bf16 v[32:35], v[158:161], v[210:213], v[32:35]
	v_mfma_f32_16x16x32_bf16 v[24:27], v[150:153], v[230:233], v[24:27]
	v_mfma_f32_16x16x32_bf16 v[16:19], v[158:161], v[230:233], v[16:19]
	v_mfma_f32_16x16x32_bf16 v[64:67], v[154:157], v[186:189], v[64:67]
	v_mfma_f32_16x16x32_bf16 v[60:63], v[162:165], v[186:189], v[60:63]
	v_mfma_f32_16x16x32_bf16 v[56:59], v[154:157], v[194:197], v[56:59]
	v_mfma_f32_16x16x32_bf16 v[48:51], v[162:165], v[194:197], v[48:51]
	v_mfma_f32_16x16x32_bf16 v[40:43], v[154:157], v[226:229], v[40:43]
	v_mfma_f32_16x16x32_bf16 v[32:35], v[162:165], v[226:229], v[32:35]
	v_mfma_f32_16x16x32_bf16 v[24:27], v[154:157], v[234:237], v[24:27]
	v_mfma_f32_16x16x32_bf16 v[16:19], v[162:165], v[234:237], v[16:19]
	s_setprio 0
	s_setprio 1
	v_mfma_f32_16x16x32_bf16 v[52:55], v[166:169], v[182:185], v[52:55]
	v_mfma_f32_16x16x32_bf16 v[44:47], v[174:177], v[182:185], v[44:47]
	v_mfma_f32_16x16x32_bf16 v[36:39], v[166:169], v[190:193], v[36:39]
	v_mfma_f32_16x16x32_bf16 v[28:31], v[174:177], v[190:193], v[28:31]
	v_mfma_f32_16x16x32_bf16 v[20:23], v[166:169], v[210:213], v[20:23]
	v_mfma_f32_16x16x32_bf16 v[12:15], v[174:177], v[210:213], v[12:15]
	v_mfma_f32_16x16x32_bf16 v[8:11], v[166:169], v[230:233], v[8:11]
	v_mfma_f32_16x16x32_bf16 v[4:7], v[174:177], v[230:233], v[4:7]
	v_mfma_f32_16x16x32_bf16 v[52:55], v[170:173], v[186:189], v[52:55]
	v_mfma_f32_16x16x32_bf16 v[44:47], v[178:181], v[186:189], v[44:47]
	v_mfma_f32_16x16x32_bf16 v[36:39], v[170:173], v[194:197], v[36:39]
	v_mfma_f32_16x16x32_bf16 v[28:31], v[178:181], v[194:197], v[28:31]
	v_mfma_f32_16x16x32_bf16 v[20:23], v[170:173], v[226:229], v[20:23]
	v_mfma_f32_16x16x32_bf16 v[12:15], v[178:181], v[226:229], v[12:15]
	v_mfma_f32_16x16x32_bf16 v[8:11], v[170:173], v[234:237], v[8:11]
	v_mfma_f32_16x16x32_bf16 v[4:7], v[178:181], v[234:237], v[4:7]
	s_setprio 0
	s_barrier
	s_add_i32 s47, 0, 0x18000
	v_add_u32_e32 v149, s47, v146
	s_add_i32 s48, 0, 0x1c000
	ds_read_b128 v[150:153], v149
	ds_read_b128 v[154:157], v149 offset:1024
	ds_read_b128 v[158:161], v149 offset:2048
	ds_read_b128 v[162:165], v149 offset:3072
	v_add_u32_e32 v149, s48, v146
	ds_read_b128 v[166:169], v149
	ds_read_b128 v[170:173], v149 offset:1024
	ds_read_b128 v[174:177], v149 offset:2048
	ds_read_b128 v[178:181], v149 offset:3072
	s_add_u32 s14, s20, 0xb0000
	s_addc_u32 s15, s21, 0
	s_mov_b32 m0, s30
	v_lshl_add_u64 v[244:245], s[14:15], 0, v[132:133]
	ds_read_b128 v[182:185], v148 offset:32768
	ds_read_b128 v[186:189], v148 offset:33792
	ds_read_b128 v[190:193], v148 offset:34816
	ds_read_b128 v[194:197], v148 offset:35840
	ds_read_b128 v[210:213], v148 offset:36864
	ds_read_b128 v[226:229], v148 offset:37888
	ds_read_b128 v[230:233], v148 offset:38912
	s_mov_b32 m0, s28
	ds_read_b128 v[234:237], v148 offset:39936
	global_load_lds_dwordx4 v[240:241], off
	s_mov_b32 m0, s29
	s_nop 0
	global_load_lds_dwordx4 v[242:243], off
	s_mov_b32 m0, s30
	s_nop 0
	global_load_lds_dwordx4 v[244:245], off
	s_mov_b32 m0, s31
	v_lshl_add_u64 v[244:245], s[14:15], 0, v[136:137]
	global_load_lds_dwordx4 v[244:245], off
	s_waitcnt vmcnt(8)
	s_waitcnt lgkmcnt(0)
	s_barrier
; #define PG8_STAGE(bufoff, gbase, voff) do { _Pragma("unroll") for (int _i = 0; _i < 2; ++_i) \
;         __builtin_amdgcn_global_load_lds((const unsigned*)((const char*)(gbase) + (voff)[_i]), (PG8_LAS unsigned*)(lds + (bufoff) + ldsw + _i * 8192), 16, 0, 0); } while (0)
; #define PG8_LDA(dst, b, h) do { _Pragma("unroll") for (int m = 0; m < 4; ++m) _Pragma("unroll") for (int k = 0; k < 2; ++k) dst[m][k] = *(const PG8_LAS bf16x8*)(lds + PG8_SA(b, h) + aoff + m * 2048 + k * 1024); } while (0)
; #define PG8_MMA(ai, bj, At, Bt) do { __builtin_amdgcn_s_setprio(1); _Pragma("unroll") for (int m = 0; m < 4; ++m) _Pragma("unroll") for (int n = 0; n < 2; ++n) _Pragma("unroll") for (int k = 0; k < 2; ++k) \
;         acc[ai][bj][m][n] = __builtin_amdgcn_mfma_f32_16x16x32_bf16(Bt[n][k], At[m][k], acc[ai][bj][m][n], 0, 0, 0); __builtin_amdgcn_s_setprio(0); } while (0)
; #define PG8_WAIT_V(n) asm volatile("s_waitcnt vmcnt(" #n ")" ::: "memory")
; #define PG8_WAIT_L(n) asm volatile("s_waitcnt lgkmcnt(" #n ")" ::: "memory")
; #define PG8_BAR __builtin_amdgcn_s_barrier()
; #define PG8_SCHED __builtin_amdgcn_sched_barrier(0)
; template <class Epi, class Sched, bool ALIGN_EPI = false, bool SP2 = false>
; __device__ __forceinline__ void gemm_phase(PG8_LAS unsigned char* lds, const Gemm g, const Sched& S, const Epi& E) {
;     ...
;             PG8_WAIT_V(8); PG8_WAIT_L(0); PG8_BAR; PG8_MMA(0, 0, At, B0); PG8_MMA(0, 1, At, B1); PG8_BAR; PG8_SCHED;
;             PG8_LDA(At, 1, 1); PG8_STAGE(PG8_SB(1, 0), b3, voffB); PG8_STAGE(PG8_SB(1, 1), b3 + hstepB, voffB); PG8_STAGE(PG8_SA(1, 0), a3, voffA);
;             PG8_WAIT_V(8); PG8_WAIT_L(0); PG8_BAR; PG8_MMA(1, 0, At, B0); PG8_MMA(1, 1, At, B1); PG8_BAR; PG8_SCHED;
;     ...
;         if constexpr (ALIGN_EPI) { if (wr == 0) PG8_BAR; }
	s_setprio 1
	s_waitcnt lgkmcnt(0)
	v_mfma_f32_16x16x32_bf16 v[128:131], v[150:153], v[182:185], v[128:131]
	v_mfma_f32_16x16x32_bf16 v[124:127], v[158:161], v[182:185], v[124:127]
	v_mfma_f32_16x16x32_bf16 v[120:123], v[150:153], v[190:193], v[120:123]
	v_mfma_f32_16x16x32_bf16 v[112:115], v[158:161], v[190:193], v[112:115]
	v_mfma_f32_16x16x32_bf16 v[104:107], v[150:153], v[210:213], v[104:107]
	v_mfma_f32_16x16x32_bf16 v[96:99], v[158:161], v[210:213], v[96:99]
	v_mfma_f32_16x16x32_bf16 v[88:91], v[150:153], v[230:233], v[88:91]
	v_mfma_f32_16x16x32_bf16 v[80:83], v[158:161], v[230:233], v[80:83]
	v_mfma_f32_16x16x32_bf16 v[128:131], v[154:157], v[186:189], v[128:131]
	v_mfma_f32_16x16x32_bf16 v[124:127], v[162:165], v[186:189], v[124:127]
	v_mfma_f32_16x16x32_bf16 v[120:123], v[154:157], v[194:197], v[120:123]
	v_mfma_f32_16x16x32_bf16 v[112:115], v[162:165], v[194:197], v[112:115]
	v_mfma_f32_16x16x32_bf16 v[104:107], v[154:157], v[226:229], v[104:107]
	v_mfma_f32_16x16x32_bf16 v[96:99], v[162:165], v[226:229], v[96:99]
	v_mfma_f32_16x16x32_bf16 v[88:91], v[154:157], v[234:237], v[88:91]
	v_mfma_f32_16x16x32_bf16 v[80:83], v[162:165], v[234:237], v[80:83]
	s_setprio 0
	s_setprio 1
	v_mfma_f32_16x16x32_bf16 v[116:119], v[166:169], v[182:185], v[116:119]
	v_mfma_f32_16x16x32_bf16 v[108:111], v[174:177], v[182:185], v[108:111]
	v_mfma_f32_16x16x32_bf16 v[100:103], v[166:169], v[190:193], v[100:103]
	v_mfma_f32_16x16x32_bf16 v[92:95], v[174:177], v[190:193], v[92:95]
	v_mfma_f32_16x16x32_bf16 v[84:87], v[166:169], v[210:213], v[84:87]
	v_mfma_f32_16x16x32_bf16 v[76:79], v[174:177], v[210:213], v[76:79]
	v_mfma_f32_16x16x32_bf16 v[72:75], v[166:169], v[230:233], v[72:75]
	v_mfma_f32_16x16x32_bf16 v[68:71], v[174:177], v[230:233], v[68:71]
	v_mfma_f32_16x16x32_bf16 v[116:119], v[170:173], v[186:189], v[116:119]
	v_mfma_f32_16x16x32_bf16 v[108:111], v[178:181], v[186:189], v[108:111]
	v_mfma_f32_16x16x32_bf16 v[100:103], v[170:173], v[194:197], v[100:103]
	v_mfma_f32_16x16x32_bf16 v[92:95], v[178:181], v[194:197], v[92:95]
	v_mfma_f32_16x16x32_bf16 v[84:87], v[170:173], v[226:229], v[84:87]
	v_mfma_f32_16x16x32_bf16 v[76:79], v[178:181], v[226:229], v[76:79]
	v_mfma_f32_16x16x32_bf16 v[72:75], v[170:173], v[234:237], v[72:75]
	v_mfma_f32_16x16x32_bf16 v[68:71], v[178:181], v[234:237], v[68:71]
	s_setprio 0
	s_barrier
	s_add_i32 s14, s47, s27
	v_lshl_add_u64 v[144:145], v[144:145], 0, s[64:65]
	s_mov_b32 m0, s14
	ds_read_b128 v[182:185], v148 offset:49152
	ds_read_b128 v[186:189], v148 offset:50176
	ds_read_b128 v[190:193], v148 offset:51200
	ds_read_b128 v[194:197], v148 offset:52224
	ds_read_b128 v[210:213], v148 offset:53248
	ds_read_b128 v[226:229], v148 offset:54272
	ds_read_b128 v[230:233], v148 offset:55296
	ds_read_b128 v[234:237], v148 offset:56320
	global_load_lds_dwordx4 v[144:145], off
	s_add_i32 m0, s14, 0x2000
	s_add_u32 s14, s18, 0xb0080
	v_lshl_add_u64 v[144:145], v[238:239], 0, s[64:65]
	s_addc_u32 s15, s19, 0
	s_add_i32 s18, s48, s27
	global_load_lds_dwordx4 v[144:145], off
	s_mov_b32 m0, s18
	v_lshl_add_u64 v[144:145], s[14:15], 0, v[134:135]
	global_load_lds_dwordx4 v[144:145], off
	s_add_i32 m0, s18, 0x2000
	v_lshl_add_u64 v[144:145], s[14:15], 0, v[138:139]
	global_load_lds_dwordx4 v[144:145], off
	s_waitcnt vmcnt(6)
	s_waitcnt lgkmcnt(0)
	s_barrier
	s_setprio 1
	s_waitcnt lgkmcnt(0)
	v_mfma_f32_16x16x32_bf16 v[64:67], v[150:153], v[182:185], v[64:67]
	v_mfma_f32_16x16x32_bf16 v[60:63], v[158:161], v[182:185], v[60:63]
	v_mfma_f32_16x16x32_bf16 v[56:59], v[150:153], v[190:193], v[56:59]
	v_mfma_f32_16x16x32_bf16 v[48:51], v[158:161], v[190:193], v[48:51]
	v_mfma_f32_16x16x32_bf16 v[40:43], v[150:153], v[210:213], v[40:43]
	v_mfma_f32_16x16x32_bf16 v[32:35], v[158:161], v[210:213], v[32:35]
	v_mfma_f32_16x16x32_bf16 v[24:27], v[150:153], v[230:233], v[24:27]
	v_mfma_f32_16x16x32_bf16 v[16:19], v[158:161], v[230:233], v[16:19]
	v_mfma_f32_16x16x32_bf16 v[64:67], v[154:157], v[186:189], v[64:67]
	v_mfma_f32_16x16x32_bf16 v[60:63], v[162:165], v[186:189], v[60:63]
	v_mfma_f32_16x16x32_bf16 v[56:59], v[154:157], v[194:197], v[56:59]
	v_mfma_f32_16x16x32_bf16 v[48:51], v[162:165], v[194:197], v[48:51]
	v_mfma_f32_16x16x32_bf16 v[40:43], v[154:157], v[226:229], v[40:43]
	v_mfma_f32_16x16x32_bf16 v[32:35], v[162:165], v[226:229], v[32:35]
	v_mfma_f32_16x16x32_bf16 v[24:27], v[154:157], v[234:237], v[24:27]
	v_mfma_f32_16x16x32_bf16 v[16:19], v[162:165], v[234:237], v[16:19]
	s_setprio 0
	s_setprio 1
	v_mfma_f32_16x16x32_bf16 v[52:55], v[166:169], v[182:185], v[52:55]
	v_mfma_f32_16x16x32_bf16 v[44:47], v[174:177], v[182:185], v[44:47]
	v_mfma_f32_16x16x32_bf16 v[36:39], v[166:169], v[190:193], v[36:39]
	v_mfma_f32_16x16x32_bf16 v[28:31], v[174:177], v[190:193], v[28:31]
	v_mfma_f32_16x16x32_bf16 v[20:23], v[166:169], v[210:213], v[20:23]
	v_mfma_f32_16x16x32_bf16 v[12:15], v[174:177], v[210:213], v[12:15]
	v_mfma_f32_16x16x32_bf16 v[8:11], v[166:169], v[230:233], v[8:11]
	v_mfma_f32_16x16x32_bf16 v[4:7], v[174:177], v[230:233], v[4:7]
	v_mfma_f32_16x16x32_bf16 v[52:55], v[170:173], v[186:189], v[52:55]
	v_mfma_f32_16x16x32_bf16 v[44:47], v[178:181], v[186:189], v[44:47]
	v_mfma_f32_16x16x32_bf16 v[36:39], v[170:173], v[194:197], v[36:39]
	v_mfma_f32_16x16x32_bf16 v[28:31], v[178:181], v[194:197], v[28:31]
	v_mfma_f32_16x16x32_bf16 v[20:23], v[170:173], v[226:229], v[20:23]
	v_mfma_f32_16x16x32_bf16 v[12:15], v[178:181], v[226:229], v[12:15]
	v_mfma_f32_16x16x32_bf16 v[8:11], v[170:173], v[234:237], v[8:11]
	v_mfma_f32_16x16x32_bf16 v[4:7], v[178:181], v[234:237], v[4:7]
	s_setprio 0
	s_barrier
	s_add_i32 s46, s46, 2
	s_add_u32 s44, s44, 0x100
	s_addc_u32 s45, s45, 0
	s_cmp_gt_u32 s46, 41
	s_mov_b64 s[14:15], s[16:17]
	s_cbranch_scc0 .LBB0_669
	s_and_b64 vcc, exec, s[10:11]
	s_cbranch_vccz .LBB0_672
	s_barrier

; #define PG8_STAGE(bufoff, gbase, voff) do { _Pragma("unroll") for (int _i = 0; _i < 2; ++_i) \
;         __builtin_amdgcn_global_load_lds((const unsigned*)((const char*)(gbase) + (voff)[_i]), (PG8_LAS unsigned*)(lds + (bufoff) + ldsw + _i * 8192), 16, 0, 0); } while (0)
; #define PG8_LDA(dst, b, h) do { _Pragma("unroll") for (int m = 0; m < 4; ++m) _Pragma("unroll") for (int k = 0; k < 2; ++k) dst[m][k] = *(const PG8_LAS bf16x8*)(lds + PG8_SA(b, h) + aoff + m * 2048 + k * 1024); } while (0)
; #define PG8_LDB(dst, b, h) do { _Pragma("unroll") for (int n = 0; n < 2; ++n) _Pragma("unroll") for (int k = 0; k < 2; ++k) dst[n][k] = *(const PG8_LAS bf16x8*)(lds + PG8_SB(b, h) + boff + n * 2048 + k * 1024); } while (0)
; #define PG8_MMA(ai, bj, At, Bt) do { __builtin_amdgcn_s_setprio(1); _Pragma("unroll") for (int m = 0; m < 4; ++m) _Pragma("unroll") for (int n = 0; n < 2; ++n) _Pragma("unroll") for (int k = 0; k < 2; ++k) \
;         acc[ai][bj][m][n] = __builtin_amdgcn_mfma_f32_16x16x32_bf16(Bt[n][k], At[m][k], acc[ai][bj][m][n], 0, 0, 0); __builtin_amdgcn_s_setprio(0); } while (0)
; #define PG8_WAIT_V(n) asm volatile("s_waitcnt vmcnt(" #n ")" ::: "memory")
; #define PG8_WAIT_L(n) asm volatile("s_waitcnt lgkmcnt(" #n ")" ::: "memory")
; template <class Epi, class Sched, bool ALIGN_EPI = false, bool SP2 = false>
; __device__ __forceinline__ void gemm_phase(PG8_LAS unsigned char* lds, const Gemm g, const Sched& S, const Epi& E) {
;     ...
;             const bool last = (t == nt - 2);
;             const char* a1 = cA + (size_t)(t + 1) * kstep;
;             const char* a2 = last ? nA : cA + (size_t)(t + 2) * kstep; const char* b2 = last ? nB : cB + (size_t)(t + 2) * kstep;
;             const char* a3 = a2 + kstep; const char* b3 = b2 + kstep;
;             if (last && has_next) S.a_ready(nxt);
;             if constexpr (SP2) {
;             PG8_LDB(B0, 0, 0); PG8_LDB(B1, 0, 1); PG8_SCHED; PG8_LDA(At, 0, 0); PG8_STAGE(PG8_SA(1, 1), a1 + hstepA, voffA);
;             PG8_WAIT_V(8); PG8_WAIT_L(0); PG8_BAR; PG8_MMA(0, 0, At, B0); PG8_MMA(0, 1, At, B1); PG8_BAR; PG8_SCHED;
;             PG8_LDA(At, 0, 1); PG8_STAGE(PG8_SB(0, 0), b2, voffB); PG8_STAGE(PG8_SB(0, 1), b2 + hstepB, voffB); PG8_STAGE(PG8_SA(0, 0), a2, voffA);
;             PG8_WAIT_V(8); PG8_WAIT_L(0); PG8_BAR; PG8_MMA(1, 0, At, B0); PG8_MMA(1, 1, At, B1); PG8_BAR; PG8_SCHED;
.LBB0_816:
	s_add_u32 s28, s26, 0xfffc0080
	s_addc_u32 s29, s27, -1
	s_add_i32 s52, 0, 0x10000
	s_cmp_eq_u32 s51, 12
	s_cselect_b32 s31, s19, s29
	s_cselect_b32 s30, s25, s28
	v_add_u32_e32 v2, s52, v153
	s_cselect_b32 s29, s17, s50
	s_cselect_b32 s28, s48, s49
	s_add_i32 s54, 0, 0x14000
	ds_read_b128 v[148:151], v2
	ds_read_b128 v[156:159], v2 offset:1024
	ds_read_b128 v[160:163], v2 offset:2048
	ds_read_b128 v[164:167], v2 offset:3072
	v_add_u32_e32 v2, s54, v153
	ds_read_b128 v[168:171], v2
	ds_read_b128 v[172:175], v2 offset:1024
	ds_read_b128 v[176:179], v2 offset:2048
	ds_read_b128 v[180:183], v2 offset:3072
	v_lshl_add_u64 v[196:197], s[26:27], 0, v[144:145]
	s_add_i32 m0, s35, 0xc000
	ds_read_b128 v[184:187], v154
	ds_read_b128 v[188:191], v154 offset:1024
	ds_read_b128 v[192:195], v154 offset:2048
	ds_read_b128 v[210:213], v154 offset:3072
	ds_read_b128 v[226:229], v154 offset:4096
	ds_read_b128 v[230:233], v154 offset:5120
	ds_read_b128 v[234:237], v154 offset:6144
	ds_read_b128 v[238:241], v154 offset:7168
	s_mov_b32 m0, s43
	v_lshl_add_u64 v[248:249], v[244:245], 0, s[64:65]
	global_load_lds_dwordx4 v[248:249], off
	s_mov_b32 m0, s44
	v_lshl_add_u64 v[248:249], v[246:247], 0, s[64:65]
	global_load_lds_dwordx4 v[248:249], off
	s_add_i32 m0, s35, 0xc000
	s_nop 0
	global_load_lds_dwordx4 v[196:197], off
	s_add_i32 m0, s35, 0xe000
	v_lshl_add_u64 v[196:197], s[26:27], 0, v[142:143]
	global_load_lds_dwordx4 v[196:197], off
	s_waitcnt vmcnt(8)
	s_waitcnt lgkmcnt(0)
	s_barrier
	s_setprio 1
	s_waitcnt lgkmcnt(0)
	v_mfma_f32_16x16x32_bf16 v[128:131], v[148:151], v[184:187], v[128:131]
	v_mfma_f32_16x16x32_bf16 v[124:127], v[160:163], v[184:187], v[124:127]
	v_mfma_f32_16x16x32_bf16 v[116:119], v[148:151], v[192:195], v[116:119]
	v_mfma_f32_16x16x32_bf16 v[108:111], v[160:163], v[192:195], v[108:111]
	v_mfma_f32_16x16x32_bf16 v[100:103], v[148:151], v[226:229], v[100:103]
	v_mfma_f32_16x16x32_bf16 v[92:95], v[160:163], v[226:229], v[92:95]
	v_mfma_f32_16x16x32_bf16 v[84:87], v[148:151], v[234:237], v[84:87]
	v_mfma_f32_16x16x32_bf16 v[76:79], v[160:163], v[234:237], v[76:79]
	v_mfma_f32_16x16x32_bf16 v[128:131], v[156:159], v[188:191], v[128:131]
	v_mfma_f32_16x16x32_bf16 v[124:127], v[164:167], v[188:191], v[124:127]
	v_mfma_f32_16x16x32_bf16 v[116:119], v[156:159], v[210:213], v[116:119]
	v_mfma_f32_16x16x32_bf16 v[108:111], v[164:167], v[210:213], v[108:111]
	v_mfma_f32_16x16x32_bf16 v[100:103], v[156:159], v[230:233], v[100:103]
	v_mfma_f32_16x16x32_bf16 v[92:95], v[164:167], v[230:233], v[92:95]
	v_mfma_f32_16x16x32_bf16 v[84:87], v[156:159], v[238:241], v[84:87]
	v_mfma_f32_16x16x32_bf16 v[76:79], v[164:167], v[238:241], v[76:79]
	s_setprio 0
	s_setprio 1
	v_mfma_f32_16x16x32_bf16 v[120:123], v[168:171], v[184:187], v[120:123]
	v_mfma_f32_16x16x32_bf16 v[112:115], v[176:179], v[184:187], v[112:115]
	v_mfma_f32_16x16x32_bf16 v[104:107], v[168:171], v[192:195], v[104:107]
	v_mfma_f32_16x16x32_bf16 v[96:99], v[176:179], v[192:195], v[96:99]
	v_mfma_f32_16x16x32_bf16 v[88:91], v[168:171], v[226:229], v[88:91]
	v_mfma_f32_16x16x32_bf16 v[80:83], v[176:179], v[226:229], v[80:83]
	v_mfma_f32_16x16x32_bf16 v[72:75], v[168:171], v[234:237], v[72:75]
	v_mfma_f32_16x16x32_bf16 v[68:71], v[176:179], v[234:237], v[68:71]
	v_mfma_f32_16x16x32_bf16 v[120:123], v[172:175], v[188:191], v[120:123]
	v_mfma_f32_16x16x32_bf16 v[112:115], v[180:183], v[188:191], v[112:115]
	v_mfma_f32_16x16x32_bf16 v[104:107], v[172:175], v[210:213], v[104:107]
	v_mfma_f32_16x16x32_bf16 v[96:99], v[180:183], v[210:213], v[96:99]
	v_mfma_f32_16x16x32_bf16 v[88:91], v[172:175], v[230:233], v[88:91]
	v_mfma_f32_16x16x32_bf16 v[80:83], v[180:183], v[230:233], v[80:83]
	v_mfma_f32_16x16x32_bf16 v[72:75], v[172:175], v[238:241], v[72:75]
	v_mfma_f32_16x16x32_bf16 v[68:71], v[180:183], v[238:241], v[68:71]
	s_setprio 0
	s_barrier
	s_add_i32 s52, s52, s33
	v_lshl_add_u64 v[196:197], s[28:29], 0, v[136:137]
	s_mov_b32 m0, s52
	ds_read_b128 v[184:187], v154 offset:16384
	ds_read_b128 v[188:191], v154 offset:17408
	ds_read_b128 v[192:195], v154 offset:18432
	ds_read_b128 v[210:213], v154 offset:19456
	ds_read_b128 v[226:229], v154 offset:20480
	ds_read_b128 v[230:233], v154 offset:21504
	ds_read_b128 v[234:237], v154 offset:22528
	ds_read_b128 v[238:241], v154 offset:23552
	global_load_lds_dwordx4 v[196:197], off
	s_add_i32 m0, s52, 0x2000
	s_add_u32 s52, s28, 0x40000
	v_lshl_add_u64 v[242:243], s[28:29], 0, v[132:133]
	s_addc_u32 s53, s29, 0
	s_add_i32 s54, s54, s33
	global_load_lds_dwordx4 v[242:243], off
	v_lshl_add_u64 v[244:245], s[52:53], 0, v[136:137]
	s_mov_b32 m0, s54
	v_lshl_add_u64 v[246:247], s[30:31], 0, v[134:135]
	global_load_lds_dwordx4 v[244:245], off
	s_add_i32 m0, s54, 0x2000
	v_lshl_add_u64 v[244:245], s[52:53], 0, v[132:133]
	global_load_lds_dwordx4 v[244:245], off
	v_lshl_add_u64 v[244:245], s[30:31], 0, v[138:139]
	s_waitcnt vmcnt(6)
	s_waitcnt lgkmcnt(0)
	s_barrier
; #define PG8_STAGE(bufoff, gbase, voff) do { _Pragma("unroll") for (int _i = 0; _i < 2; ++_i) \
;         __builtin_amdgcn_global_load_lds((const unsigned*)((const char*)(gbase) + (voff)[_i]), (PG8_LAS unsigned*)(lds + (bufoff) + ldsw + _i * 8192), 16, 0, 0); } while (0)
; #define PG8_LDA(dst, b, h) do { _Pragma("unroll") for (int m = 0; m < 4; ++m) _Pragma("unroll") for (int k = 0; k < 2; ++k) dst[m][k] = *(const PG8_LAS bf16x8*)(lds + PG8_SA(b, h) + aoff + m * 2048 + k * 1024); } while (0)
; #define PG8_LDB(dst, b, h) do { _Pragma("unroll") for (int n = 0; n < 2; ++n) _Pragma("unroll") for (int k = 0; k < 2; ++k) dst[n][k] = *(const PG8_LAS bf16x8*)(lds + PG8_SB(b, h) + boff + n * 2048 + k * 1024); } while (0)
; #define PG8_MMA(ai, bj, At, Bt) do { __builtin_amdgcn_s_setprio(1); _Pragma("unroll") for (int m = 0; m < 4; ++m) _Pragma("unroll") for (int n = 0; n < 2; ++n) _Pragma("unroll") for (int k = 0; k < 2; ++k) \
;         acc[ai][bj][m][n] = __builtin_amdgcn_mfma_f32_16x16x32_bf16(Bt[n][k], At[m][k], acc[ai][bj][m][n], 0, 0, 0); __builtin_amdgcn_s_setprio(0); } while (0)
; #define PG8_WAIT_V(n) asm volatile("s_waitcnt vmcnt(" #n ")" ::: "memory")
; #define PG8_WAIT_L(n) asm volatile("s_waitcnt lgkmcnt(" #n ")" ::: "memory")
; #define PG8_BAR __builtin_amdgcn_s_barrier()
; #define PG8_SCHED __builtin_amdgcn_sched_barrier(0)
; template <class Epi, class Sched, bool ALIGN_EPI = false, bool SP2 = false>
; __device__ __forceinline__ void gemm_phase(PG8_LAS unsigned char* lds, const Gemm g, const Sched& S, const Epi& E) {
;     ...
;             PG8_WAIT_V(8); PG8_WAIT_L(0); PG8_BAR; PG8_MMA(1, 0, At, B0); PG8_MMA(1, 1, At, B1); PG8_BAR; PG8_SCHED;
;             PG8_LDB(B0, 1, 0); PG8_LDB(B1, 1, 1); PG8_SCHED; PG8_LDA(At, 1, 0); PG8_STAGE(PG8_SA(0, 1), a2 + hstepA, voffA);
;             PG8_WAIT_V(8); PG8_WAIT_L(0); PG8_BAR; PG8_MMA(0, 0, At, B0); PG8_MMA(0, 1, At, B1); PG8_BAR; PG8_SCHED;
	s_setprio 1
	s_waitcnt lgkmcnt(0)
	v_mfma_f32_16x16x32_bf16 v[64:67], v[148:151], v[184:187], v[64:67]
	v_mfma_f32_16x16x32_bf16 v[60:63], v[160:163], v[184:187], v[60:63]
	v_mfma_f32_16x16x32_bf16 v[52:55], v[148:151], v[192:195], v[52:55]
	v_mfma_f32_16x16x32_bf16 v[44:47], v[160:163], v[192:195], v[44:47]
	v_mfma_f32_16x16x32_bf16 v[36:39], v[148:151], v[226:229], v[36:39]
	v_mfma_f32_16x16x32_bf16 v[28:31], v[160:163], v[226:229], v[28:31]
	v_mfma_f32_16x16x32_bf16 v[20:23], v[148:151], v[234:237], v[20:23]
	v_mfma_f32_16x16x32_bf16 v[12:15], v[160:163], v[234:237], v[12:15]
	v_mfma_f32_16x16x32_bf16 v[64:67], v[156:159], v[188:191], v[64:67]
	v_mfma_f32_16x16x32_bf16 v[60:63], v[164:167], v[188:191], v[60:63]
	v_mfma_f32_16x16x32_bf16 v[52:55], v[156:159], v[210:213], v[52:55]
	v_mfma_f32_16x16x32_bf16 v[44:47], v[164:167], v[210:213], v[44:47]
	v_mfma_f32_16x16x32_bf16 v[36:39], v[156:159], v[230:233], v[36:39]
	v_mfma_f32_16x16x32_bf16 v[28:31], v[164:167], v[230:233], v[28:31]
	v_mfma_f32_16x16x32_bf16 v[20:23], v[156:159], v[238:241], v[20:23]
	v_mfma_f32_16x16x32_bf16 v[12:15], v[164:167], v[238:241], v[12:15]
	s_setprio 0
	s_setprio 1
	v_mfma_f32_16x16x32_bf16 v[56:59], v[168:171], v[184:187], v[56:59]
	v_mfma_f32_16x16x32_bf16 v[48:51], v[176:179], v[184:187], v[48:51]
	v_mfma_f32_16x16x32_bf16 v[40:43], v[168:171], v[192:195], v[40:43]
	v_mfma_f32_16x16x32_bf16 v[32:35], v[176:179], v[192:195], v[32:35]
	v_mfma_f32_16x16x32_bf16 v[24:27], v[168:171], v[226:229], v[24:27]
	v_mfma_f32_16x16x32_bf16 v[16:19], v[176:179], v[226:229], v[16:19]
	v_mfma_f32_16x16x32_bf16 v[8:11], v[168:171], v[234:237], v[8:11]
	v_mfma_f32_16x16x32_bf16 v[4:7], v[176:179], v[234:237], v[4:7]
	v_mfma_f32_16x16x32_bf16 v[56:59], v[172:175], v[188:191], v[56:59]
	v_mfma_f32_16x16x32_bf16 v[48:51], v[180:183], v[188:191], v[48:51]
	v_mfma_f32_16x16x32_bf16 v[40:43], v[172:175], v[210:213], v[40:43]
	v_mfma_f32_16x16x32_bf16 v[32:35], v[180:183], v[210:213], v[32:35]
	v_mfma_f32_16x16x32_bf16 v[24:27], v[172:175], v[230:233], v[24:27]
	v_mfma_f32_16x16x32_bf16 v[16:19], v[180:183], v[230:233], v[16:19]
	v_mfma_f32_16x16x32_bf16 v[8:11], v[172:175], v[238:241], v[8:11]
	v_mfma_f32_16x16x32_bf16 v[4:7], v[180:183], v[238:241], v[4:7]
	s_setprio 0
	s_barrier
	s_add_i32 s52, 0, 0x18000
	v_add_u32_e32 v2, s52, v153
	s_add_i32 s53, 0, 0x1c000
	ds_read_b128 v[148:151], v2
	ds_read_b128 v[156:159], v2 offset:1024
	ds_read_b128 v[160:163], v2 offset:2048
	ds_read_b128 v[164:167], v2 offset:3072
	v_add_u32_e32 v2, s53, v153
	ds_read_b128 v[168:171], v2
	ds_read_b128 v[172:175], v2 offset:1024
	ds_read_b128 v[176:179], v2 offset:2048
	ds_read_b128 v[180:183], v2 offset:3072
	s_add_u32 s30, s30, 0x40000
	s_addc_u32 s31, s31, 0
	s_mov_b32 m0, s39
	v_lshl_add_u64 v[248:249], s[30:31], 0, v[138:139]
	ds_read_b128 v[184:187], v154 offset:32768
	ds_read_b128 v[188:191], v154 offset:33792
	ds_read_b128 v[192:195], v154 offset:34816
	ds_read_b128 v[210:213], v154 offset:35840
	ds_read_b128 v[226:229], v154 offset:36864
	ds_read_b128 v[230:233], v154 offset:37888
	ds_read_b128 v[234:237], v154 offset:38912
	s_mov_b32 m0, s35
	ds_read_b128 v[238:241], v154 offset:39936
	global_load_lds_dwordx4 v[244:245], off
	s_mov_b32 m0, s37
	s_nop 0
	global_load_lds_dwordx4 v[246:247], off
	s_mov_b32 m0, s39
	s_nop 0
	global_load_lds_dwordx4 v[248:249], off
	s_mov_b32 m0, s40
	v_lshl_add_u64 v[248:249], s[30:31], 0, v[134:135]
	global_load_lds_dwordx4 v[248:249], off
	s_waitcnt vmcnt(8)
	s_waitcnt lgkmcnt(0)
	s_barrier
	s_setprio 1
	s_waitcnt lgkmcnt(0)
	v_mfma_f32_16x16x32_bf16 v[128:131], v[148:151], v[184:187], v[128:131]
	v_mfma_f32_16x16x32_bf16 v[124:127], v[160:163], v[184:187], v[124:127]
	v_mfma_f32_16x16x32_bf16 v[116:119], v[148:151], v[192:195], v[116:119]
	v_mfma_f32_16x16x32_bf16 v[108:111], v[160:163], v[192:195], v[108:111]
	v_mfma_f32_16x16x32_bf16 v[100:103], v[148:151], v[226:229], v[100:103]
	v_mfma_f32_16x16x32_bf16 v[92:95], v[160:163], v[226:229], v[92:95]
	v_mfma_f32_16x16x32_bf16 v[84:87], v[148:151], v[234:237], v[84:87]
	v_mfma_f32_16x16x32_bf16 v[76:79], v[160:163], v[234:237], v[76:79]
	v_mfma_f32_16x16x32_bf16 v[128:131], v[156:159], v[188:191], v[128:131]
	v_mfma_f32_16x16x32_bf16 v[124:127], v[164:167], v[188:191], v[124:127]
	v_mfma_f32_16x16x32_bf16 v[116:119], v[156:159], v[210:213], v[116:119]
	v_mfma_f32_16x16x32_bf16 v[108:111], v[164:167], v[210:213], v[108:111]
	v_mfma_f32_16x16x32_bf16 v[100:103], v[156:159], v[230:233], v[100:103]
	v_mfma_f32_16x16x32_bf16 v[92:95], v[164:167], v[230:233], v[92:95]
	v_mfma_f32_16x16x32_bf16 v[84:87], v[156:159], v[238:241], v[84:87]
	v_mfma_f32_16x16x32_bf16 v[76:79], v[164:167], v[238:241], v[76:79]
	s_setprio 0
	s_setprio 1
	v_mfma_f32_16x16x32_bf16 v[120:123], v[168:171], v[184:187], v[120:123]
	v_mfma_f32_16x16x32_bf16 v[112:115], v[176:179], v[184:187], v[112:115]
	v_mfma_f32_16x16x32_bf16 v[104:107], v[168:171], v[192:195], v[104:107]
	v_mfma_f32_16x16x32_bf16 v[96:99], v[176:179], v[192:195], v[96:99]
	v_mfma_f32_16x16x32_bf16 v[88:91], v[168:171], v[226:229], v[88:91]
	v_mfma_f32_16x16x32_bf16 v[80:83], v[176:179], v[226:229], v[80:83]
	v_mfma_f32_16x16x32_bf16 v[72:75], v[168:171], v[234:237], v[72:75]
	v_mfma_f32_16x16x32_bf16 v[68:71], v[176:179], v[234:237], v[68:71]
	v_mfma_f32_16x16x32_bf16 v[120:123], v[172:175], v[188:191], v[120:123]
	v_mfma_f32_16x16x32_bf16 v[112:115], v[180:183], v[188:191], v[112:115]
	v_mfma_f32_16x16x32_bf16 v[104:107], v[172:175], v[210:213], v[104:107]
	v_mfma_f32_16x16x32_bf16 v[96:99], v[180:183], v[210:213], v[96:99]
	v_mfma_f32_16x16x32_bf16 v[88:91], v[172:175], v[230:233], v[88:91]
	v_mfma_f32_16x16x32_bf16 v[80:83], v[180:183], v[230:233], v[80:83]
	v_mfma_f32_16x16x32_bf16 v[72:75], v[172:175], v[238:241], v[72:75]
	v_mfma_f32_16x16x32_bf16 v[68:71], v[180:183], v[238:241], v[68:71]
	s_setprio 0
	s_barrier
; #define PG8_STAGE(bufoff, gbase, voff) do { _Pragma("unroll") for (int _i = 0; _i < 2; ++_i) \
;         __builtin_amdgcn_global_load_lds((const unsigned*)((const char*)(gbase) + (voff)[_i]), (PG8_LAS unsigned*)(lds + (bufoff) + ldsw + _i * 8192), 16, 0, 0); } while (0)
; #define PG8_LDA(dst, b, h) do { _Pragma("unroll") for (int m = 0; m < 4; ++m) _Pragma("unroll") for (int k = 0; k < 2; ++k) dst[m][k] = *(const PG8_LAS bf16x8*)(lds + PG8_SA(b, h) + aoff + m * 2048 + k * 1024); } while (0)
; #define PG8_MMA(ai, bj, At, Bt) do { __builtin_amdgcn_s_setprio(1); _Pragma("unroll") for (int m = 0; m < 4; ++m) _Pragma("unroll") for (int n = 0; n < 2; ++n) _Pragma("unroll") for (int k = 0; k < 2; ++k) \
;         acc[ai][bj][m][n] = __builtin_amdgcn_mfma_f32_16x16x32_bf16(Bt[n][k], At[m][k], acc[ai][bj][m][n], 0, 0, 0); __builtin_amdgcn_s_setprio(0); } while (0)
; #define PG8_WAIT_V(n) asm volatile("s_waitcnt vmcnt(" #n ")" ::: "memory")
; #define PG8_WAIT_L(n) asm volatile("s_waitcnt lgkmcnt(" #n ")" ::: "memory")
; #define PG8_BAR __builtin_amdgcn_s_barrier()
; #define PG8_SCHED __builtin_amdgcn_sched_barrier(0)
; template <class Epi, class Sched, bool ALIGN_EPI = false, bool SP2 = false>
; __device__ __forceinline__ void gemm_phase(PG8_LAS unsigned char* lds, const Gemm g, const Sched& S, const Epi& E) {
;     ...
;             PG8_LDA(At, 1, 1); PG8_STAGE(PG8_SB(1, 0), b3, voffB); PG8_STAGE(PG8_SB(1, 1), b3 + hstepB, voffB); PG8_STAGE(PG8_SA(1, 0), a3, voffA);
;             PG8_WAIT_V(8); PG8_WAIT_L(0); PG8_BAR; PG8_MMA(1, 0, At, B0); PG8_MMA(1, 1, At, B1); PG8_BAR; PG8_SCHED;
	s_add_i32 s30, s52, s33
	v_lshl_add_u64 v[196:197], v[196:197], 0, s[64:65]
	s_mov_b32 m0, s30
	ds_read_b128 v[184:187], v154 offset:49152
	ds_read_b128 v[188:191], v154 offset:50176
	ds_read_b128 v[192:195], v154 offset:51200
	ds_read_b128 v[210:213], v154 offset:52224
	ds_read_b128 v[226:229], v154 offset:53248
	ds_read_b128 v[230:233], v154 offset:54272
	ds_read_b128 v[234:237], v154 offset:55296
	ds_read_b128 v[238:241], v154 offset:56320
	global_load_lds_dwordx4 v[196:197], off
	s_add_i32 m0, s30, 0x2000
	s_add_u32 s28, s28, 0x40080
	v_lshl_add_u64 v[196:197], v[242:243], 0, s[64:65]
	s_addc_u32 s29, s29, 0
	s_add_i32 s30, s53, s33
	global_load_lds_dwordx4 v[196:197], off
	s_mov_b32 m0, s30
	v_lshl_add_u64 v[196:197], s[28:29], 0, v[136:137]
	global_load_lds_dwordx4 v[196:197], off
	s_add_i32 m0, s30, 0x2000
	v_lshl_add_u64 v[196:197], s[28:29], 0, v[132:133]
	global_load_lds_dwordx4 v[196:197], off
	s_waitcnt vmcnt(6)
	s_waitcnt lgkmcnt(0)
	s_barrier
	s_setprio 1
	s_waitcnt lgkmcnt(0)
	v_mfma_f32_16x16x32_bf16 v[64:67], v[148:151], v[184:187], v[64:67]
	v_mfma_f32_16x16x32_bf16 v[60:63], v[160:163], v[184:187], v[60:63]
	v_mfma_f32_16x16x32_bf16 v[52:55], v[148:151], v[192:195], v[52:55]
	v_mfma_f32_16x16x32_bf16 v[44:47], v[160:163], v[192:195], v[44:47]
	v_mfma_f32_16x16x32_bf16 v[36:39], v[148:151], v[226:229], v[36:39]
	v_mfma_f32_16x16x32_bf16 v[28:31], v[160:163], v[226:229], v[28:31]
	v_mfma_f32_16x16x32_bf16 v[20:23], v[148:151], v[234:237], v[20:23]
	v_mfma_f32_16x16x32_bf16 v[12:15], v[160:163], v[234:237], v[12:15]
	v_mfma_f32_16x16x32_bf16 v[64:67], v[156:159], v[188:191], v[64:67]
	v_mfma_f32_16x16x32_bf16 v[60:63], v[164:167], v[188:191], v[60:63]
	v_mfma_f32_16x16x32_bf16 v[52:55], v[156:159], v[210:213], v[52:55]
	v_mfma_f32_16x16x32_bf16 v[44:47], v[164:167], v[210:213], v[44:47]
	v_mfma_f32_16x16x32_bf16 v[36:39], v[156:159], v[230:233], v[36:39]
	v_mfma_f32_16x16x32_bf16 v[28:31], v[164:167], v[230:233], v[28:31]
	v_mfma_f32_16x16x32_bf16 v[20:23], v[156:159], v[238:241], v[20:23]
	v_mfma_f32_16x16x32_bf16 v[12:15], v[164:167], v[238:241], v[12:15]
	s_setprio 0
	s_setprio 1
	v_mfma_f32_16x16x32_bf16 v[56:59], v[168:171], v[184:187], v[56:59]
	v_mfma_f32_16x16x32_bf16 v[48:51], v[176:179], v[184:187], v[48:51]
	v_mfma_f32_16x16x32_bf16 v[40:43], v[168:171], v[192:195], v[40:43]
	v_mfma_f32_16x16x32_bf16 v[32:35], v[176:179], v[192:195], v[32:35]
	v_mfma_f32_16x16x32_bf16 v[24:27], v[168:171], v[226:229], v[24:27]
	v_mfma_f32_16x16x32_bf16 v[16:19], v[176:179], v[226:229], v[16:19]
	v_mfma_f32_16x16x32_bf16 v[8:11], v[168:171], v[234:237], v[8:11]
	v_mfma_f32_16x16x32_bf16 v[4:7], v[176:179], v[234:237], v[4:7]
	v_mfma_f32_16x16x32_bf16 v[56:59], v[172:175], v[188:191], v[56:59]
	v_mfma_f32_16x16x32_bf16 v[48:51], v[180:183], v[188:191], v[48:51]
	v_mfma_f32_16x16x32_bf16 v[40:43], v[172:175], v[210:213], v[40:43]
	v_mfma_f32_16x16x32_bf16 v[32:35], v[180:183], v[210:213], v[32:35]
	v_mfma_f32_16x16x32_bf16 v[24:27], v[172:175], v[230:233], v[24:27]
	v_mfma_f32_16x16x32_bf16 v[16:19], v[180:183], v[230:233], v[16:19]
	v_mfma_f32_16x16x32_bf16 v[8:11], v[172:175], v[238:241], v[8:11]
	v_mfma_f32_16x16x32_bf16 v[4:7], v[180:183], v[238:241], v[4:7]
	s_setprio 0
	s_barrier
	s_add_i32 s51, s51, 2
	s_add_u32 s49, s49, 0x100
	s_addc_u32 s50, s50, 0
	s_add_u32 s26, s26, 0x100
	s_addc_u32 s27, s27, 0
	s_cmp_gt_u32 s51, 13
	s_cbranch_scc0 .LBB0_816
	s_and_b64 vcc, exec, s[14:15]
	s_cbranch_vccnz .LBB0_821
	v_lshl_add_u32 v150, s24, 8, v152
	s_cmp_gt_i32 s47, 11
	s_mov_b64 s[24:25], -1
	s_cbranch_scc1 .LBB0_822

; #define PG8_STAGE(bufoff, gbase, voff) do { _Pragma("unroll") for (int _i = 0; _i < 2; ++_i) \
;         __builtin_amdgcn_global_load_lds((const unsigned*)((const char*)(gbase) + (voff)[_i]), (PG8_LAS unsigned*)(lds + (bufoff) + ldsw + _i * 8192), 16, 0, 0); } while (0)
; #define PG8_LDA(dst, b, h) do { _Pragma("unroll") for (int m = 0; m < 4; ++m) _Pragma("unroll") for (int k = 0; k < 2; ++k) dst[m][k] = *(const PG8_LAS bf16x8*)(lds + PG8_SA(b, h) + aoff + m * 2048 + k * 1024); } while (0)
; #define PG8_LDB(dst, b, h) do { _Pragma("unroll") for (int n = 0; n < 2; ++n) _Pragma("unroll") for (int k = 0; k < 2; ++k) dst[n][k] = *(const PG8_LAS bf16x8*)(lds + PG8_SB(b, h) + boff + n * 2048 + k * 1024); } while (0)
; #define PG8_MMA(ai, bj, At, Bt) do { __builtin_amdgcn_s_setprio(1); _Pragma("unroll") for (int m = 0; m < 4; ++m) _Pragma("unroll") for (int n = 0; n < 2; ++n) _Pragma("unroll") for (int k = 0; k < 2; ++k) \
;         acc[ai][bj][m][n] = __builtin_amdgcn_mfma_f32_16x16x32_bf16(Bt[n][k], At[m][k], acc[ai][bj][m][n], 0, 0, 0); __builtin_amdgcn_s_setprio(0); } while (0)
; #define PG8_WAIT_V(n) asm volatile("s_waitcnt vmcnt(" #n ")" ::: "memory")
; #define PG8_WAIT_L(n) asm volatile("s_waitcnt lgkmcnt(" #n ")" ::: "memory")
; template <class Epi, class Sched, bool ALIGN_EPI = false, bool SP2 = false>
; __device__ __forceinline__ void gemm_phase(PG8_LAS unsigned char* lds, const Gemm g, const Sched& S, const Epi& E) {
;     ...
;             const bool last = (t == nt - 2);
;             const char* a1 = cA + (size_t)(t + 1) * kstep;
;             const char* a2 = last ? nA : cA + (size_t)(t + 2) * kstep; const char* b2 = last ? nB : cB + (size_t)(t + 2) * kstep;
;             const char* a3 = a2 + kstep; const char* b3 = b2 + kstep;
;             if (last && has_next) S.a_ready(nxt);
;             if constexpr (SP2) {
;             PG8_LDB(B0, 0, 0); PG8_LDB(B1, 0, 1); PG8_SCHED; PG8_LDA(At, 0, 0); PG8_STAGE(PG8_SA(1, 1), a1 + hstepA, voffA);
;             PG8_WAIT_V(8); PG8_WAIT_L(0); PG8_BAR; PG8_MMA(0, 0, At, B0); PG8_MMA(0, 1, At, B1); PG8_BAR; PG8_SCHED;
;             PG8_LDA(At, 0, 1); PG8_STAGE(PG8_SB(0, 0), b2, voffB); PG8_STAGE(PG8_SB(0, 1), b2 + hstepB, voffB); PG8_STAGE(PG8_SA(0, 0), a2, voffA);
;             PG8_WAIT_V(8); PG8_WAIT_L(0); PG8_BAR; PG8_MMA(1, 0, At, B0); PG8_MMA(1, 1, At, B1); PG8_BAR; PG8_SCHED;
.LBB0_1093:
	s_add_u32 s24, s22, 0xfffc0080
	s_addc_u32 s25, s23, -1
	s_add_i32 s49, 0, 0x10000
	s_cmp_eq_u32 s48, 12
	s_cselect_b32 s27, s15, s25
	s_cselect_b32 s26, s44, s24
	v_add_u32_e32 v144, s49, v146
	s_cselect_b32 s25, s13, s47
	s_cselect_b32 s24, s45, s46
	s_add_i32 s52, 0, 0x14000
	ds_read_b128 v[150:153], v144
	ds_read_b128 v[154:157], v144 offset:1024
	ds_read_b128 v[158:161], v144 offset:2048
	ds_read_b128 v[162:165], v144 offset:3072
	v_add_u32_e32 v144, s52, v146
	ds_read_b128 v[166:169], v144
	ds_read_b128 v[170:173], v144 offset:1024
	ds_read_b128 v[174:177], v144 offset:2048
	ds_read_b128 v[178:181], v144 offset:3072
	v_lshl_add_u64 v[144:145], s[22:23], 0, v[142:143]
	s_add_i32 m0, s17, 0xc000
	ds_read_b128 v[182:185], v148
	ds_read_b128 v[186:189], v148 offset:1024
	ds_read_b128 v[190:193], v148 offset:2048
	ds_read_b128 v[194:197], v148 offset:3072
	ds_read_b128 v[210:213], v148 offset:4096
	ds_read_b128 v[226:229], v148 offset:5120
	ds_read_b128 v[230:233], v148 offset:6144
	ds_read_b128 v[234:237], v148 offset:7168
	s_mov_b32 m0, s39
	v_lshl_add_u64 v[244:245], v[240:241], 0, s[64:65]
	global_load_lds_dwordx4 v[244:245], off
	s_mov_b32 m0, s40
	v_lshl_add_u64 v[244:245], v[242:243], 0, s[64:65]
	global_load_lds_dwordx4 v[244:245], off
	s_add_i32 m0, s17, 0xc000
	s_nop 0
	global_load_lds_dwordx4 v[144:145], off
	s_add_i32 m0, s17, 0xe000
	v_lshl_add_u64 v[144:145], s[22:23], 0, v[140:141]
	global_load_lds_dwordx4 v[144:145], off
	s_waitcnt vmcnt(8)
	s_waitcnt lgkmcnt(0)
	s_barrier
	s_setprio 1
	s_waitcnt lgkmcnt(0)
	v_mfma_f32_16x16x32_bf16 v[128:131], v[150:153], v[182:185], v[128:131]
	v_mfma_f32_16x16x32_bf16 v[124:127], v[158:161], v[182:185], v[124:127]
	v_mfma_f32_16x16x32_bf16 v[120:123], v[150:153], v[190:193], v[120:123]
	v_mfma_f32_16x16x32_bf16 v[112:115], v[158:161], v[190:193], v[112:115]
	v_mfma_f32_16x16x32_bf16 v[104:107], v[150:153], v[210:213], v[104:107]
	v_mfma_f32_16x16x32_bf16 v[96:99], v[158:161], v[210:213], v[96:99]
	v_mfma_f32_16x16x32_bf16 v[88:91], v[150:153], v[230:233], v[88:91]
	v_mfma_f32_16x16x32_bf16 v[80:83], v[158:161], v[230:233], v[80:83]
	v_mfma_f32_16x16x32_bf16 v[128:131], v[154:157], v[186:189], v[128:131]
	v_mfma_f32_16x16x32_bf16 v[124:127], v[162:165], v[186:189], v[124:127]
	v_mfma_f32_16x16x32_bf16 v[120:123], v[154:157], v[194:197], v[120:123]
	v_mfma_f32_16x16x32_bf16 v[112:115], v[162:165], v[194:197], v[112:115]
	v_mfma_f32_16x16x32_bf16 v[104:107], v[154:157], v[226:229], v[104:107]
	v_mfma_f32_16x16x32_bf16 v[96:99], v[162:165], v[226:229], v[96:99]
	v_mfma_f32_16x16x32_bf16 v[88:91], v[154:157], v[234:237], v[88:91]
	v_mfma_f32_16x16x32_bf16 v[80:83], v[162:165], v[234:237], v[80:83]
	s_setprio 0
	s_setprio 1
	v_mfma_f32_16x16x32_bf16 v[116:119], v[166:169], v[182:185], v[116:119]
	v_mfma_f32_16x16x32_bf16 v[108:111], v[174:177], v[182:185], v[108:111]
	v_mfma_f32_16x16x32_bf16 v[100:103], v[166:169], v[190:193], v[100:103]
	v_mfma_f32_16x16x32_bf16 v[92:95], v[174:177], v[190:193], v[92:95]
	v_mfma_f32_16x16x32_bf16 v[84:87], v[166:169], v[210:213], v[84:87]
	v_mfma_f32_16x16x32_bf16 v[76:79], v[174:177], v[210:213], v[76:79]
	v_mfma_f32_16x16x32_bf16 v[72:75], v[166:169], v[230:233], v[72:75]
	v_mfma_f32_16x16x32_bf16 v[68:71], v[174:177], v[230:233], v[68:71]
	v_mfma_f32_16x16x32_bf16 v[116:119], v[170:173], v[186:189], v[116:119]
	v_mfma_f32_16x16x32_bf16 v[108:111], v[178:181], v[186:189], v[108:111]
	v_mfma_f32_16x16x32_bf16 v[100:103], v[170:173], v[194:197], v[100:103]
	v_mfma_f32_16x16x32_bf16 v[92:95], v[178:181], v[194:197], v[92:95]
	v_mfma_f32_16x16x32_bf16 v[84:87], v[170:173], v[226:229], v[84:87]
	v_mfma_f32_16x16x32_bf16 v[76:79], v[178:181], v[226:229], v[76:79]
	v_mfma_f32_16x16x32_bf16 v[72:75], v[170:173], v[234:237], v[72:75]
	v_mfma_f32_16x16x32_bf16 v[68:71], v[178:181], v[234:237], v[68:71]
	s_setprio 0
	s_barrier
	s_add_i32 s49, s49, s34
	v_lshl_add_u64 v[144:145], s[24:25], 0, v[134:135]
	s_mov_b32 m0, s49
	ds_read_b128 v[182:185], v148 offset:16384
	ds_read_b128 v[186:189], v148 offset:17408
	ds_read_b128 v[190:193], v148 offset:18432
	ds_read_b128 v[194:197], v148 offset:19456
	ds_read_b128 v[210:213], v148 offset:20480
	ds_read_b128 v[226:229], v148 offset:21504
	ds_read_b128 v[230:233], v148 offset:22528
	ds_read_b128 v[234:237], v148 offset:23552
	global_load_lds_dwordx4 v[144:145], off
	s_add_i32 m0, s49, 0x2000
	s_add_u32 s50, s24, 0x40000
	v_lshl_add_u64 v[238:239], s[24:25], 0, v[138:139]
	s_addc_u32 s51, s25, 0
	s_add_i32 s49, s52, s34
	global_load_lds_dwordx4 v[238:239], off
	v_lshl_add_u64 v[240:241], s[50:51], 0, v[134:135]
	s_mov_b32 m0, s49
	v_lshl_add_u64 v[242:243], s[26:27], 0, v[136:137]
	global_load_lds_dwordx4 v[240:241], off
	s_add_i32 m0, s49, 0x2000
	v_lshl_add_u64 v[240:241], s[50:51], 0, v[138:139]
	global_load_lds_dwordx4 v[240:241], off
	v_lshl_add_u64 v[240:241], s[26:27], 0, v[132:133]
	s_waitcnt vmcnt(6)
	s_waitcnt lgkmcnt(0)
	s_barrier
; #define PG8_STAGE(bufoff, gbase, voff) do { _Pragma("unroll") for (int _i = 0; _i < 2; ++_i) \
;         __builtin_amdgcn_global_load_lds((const unsigned*)((const char*)(gbase) + (voff)[_i]), (PG8_LAS unsigned*)(lds + (bufoff) + ldsw + _i * 8192), 16, 0, 0); } while (0)
; #define PG8_LDA(dst, b, h) do { _Pragma("unroll") for (int m = 0; m < 4; ++m) _Pragma("unroll") for (int k = 0; k < 2; ++k) dst[m][k] = *(const PG8_LAS bf16x8*)(lds + PG8_SA(b, h) + aoff + m * 2048 + k * 1024); } while (0)
; #define PG8_LDB(dst, b, h) do { _Pragma("unroll") for (int n = 0; n < 2; ++n) _Pragma("unroll") for (int k = 0; k < 2; ++k) dst[n][k] = *(const PG8_LAS bf16x8*)(lds + PG8_SB(b, h) + boff + n * 2048 + k * 1024); } while (0)
; #define PG8_MMA(ai, bj, At, Bt) do { __builtin_amdgcn_s_setprio(1); _Pragma("unroll") for (int m = 0; m < 4; ++m) _Pragma("unroll") for (int n = 0; n < 2; ++n) _Pragma("unroll") for (int k = 0; k < 2; ++k) \
;         acc[ai][bj][m][n] = __builtin_amdgcn_mfma_f32_16x16x32_bf16(Bt[n][k], At[m][k], acc[ai][bj][m][n], 0, 0, 0); __builtin_amdgcn_s_setprio(0); } while (0)
; #define PG8_WAIT_V(n) asm volatile("s_waitcnt vmcnt(" #n ")" ::: "memory")
; #define PG8_WAIT_L(n) asm volatile("s_waitcnt lgkmcnt(" #n ")" ::: "memory")
; #define PG8_BAR __builtin_amdgcn_s_barrier()
; #define PG8_SCHED __builtin_amdgcn_sched_barrier(0)
; template <class Epi, class Sched, bool ALIGN_EPI = false, bool SP2 = false>
; __device__ __forceinline__ void gemm_phase(PG8_LAS unsigned char* lds, const Gemm g, const Sched& S, const Epi& E) {
;     ...
;             PG8_WAIT_V(8); PG8_WAIT_L(0); PG8_BAR; PG8_MMA(1, 0, At, B0); PG8_MMA(1, 1, At, B1); PG8_BAR; PG8_SCHED;
;             PG8_LDB(B0, 1, 0); PG8_LDB(B1, 1, 1); PG8_SCHED; PG8_LDA(At, 1, 0); PG8_STAGE(PG8_SA(0, 1), a2 + hstepA, voffA);
;             PG8_WAIT_V(8); PG8_WAIT_L(0); PG8_BAR; PG8_MMA(0, 0, At, B0); PG8_MMA(0, 1, At, B1); PG8_BAR; PG8_SCHED;
	s_setprio 1
	s_waitcnt lgkmcnt(0)
	v_mfma_f32_16x16x32_bf16 v[64:67], v[150:153], v[182:185], v[64:67]
	v_mfma_f32_16x16x32_bf16 v[60:63], v[158:161], v[182:185], v[60:63]
	v_mfma_f32_16x16x32_bf16 v[56:59], v[150:153], v[190:193], v[56:59]
	v_mfma_f32_16x16x32_bf16 v[48:51], v[158:161], v[190:193], v[48:51]
	v_mfma_f32_16x16x32_bf16 v[40:43], v[150:153], v[210:213], v[40:43]
	v_mfma_f32_16x16x32_bf16 v[32:35], v[158:161], v[210:213], v[32:35]
	v_mfma_f32_16x16x32_bf16 v[24:27], v[150:153], v[230:233], v[24:27]
	v_mfma_f32_16x16x32_bf16 v[16:19], v[158:161], v[230:233], v[16:19]
	v_mfma_f32_16x16x32_bf16 v[64:67], v[154:157], v[186:189], v[64:67]
	v_mfma_f32_16x16x32_bf16 v[60:63], v[162:165], v[186:189], v[60:63]
	v_mfma_f32_16x16x32_bf16 v[56:59], v[154:157], v[194:197], v[56:59]
	v_mfma_f32_16x16x32_bf16 v[48:51], v[162:165], v[194:197], v[48:51]
	v_mfma_f32_16x16x32_bf16 v[40:43], v[154:157], v[226:229], v[40:43]
	v_mfma_f32_16x16x32_bf16 v[32:35], v[162:165], v[226:229], v[32:35]
	v_mfma_f32_16x16x32_bf16 v[24:27], v[154:157], v[234:237], v[24:27]
	v_mfma_f32_16x16x32_bf16 v[16:19], v[162:165], v[234:237], v[16:19]
	s_setprio 0
	s_setprio 1
	v_mfma_f32_16x16x32_bf16 v[52:55], v[166:169], v[182:185], v[52:55]
	v_mfma_f32_16x16x32_bf16 v[44:47], v[174:177], v[182:185], v[44:47]
	v_mfma_f32_16x16x32_bf16 v[36:39], v[166:169], v[190:193], v[36:39]
	v_mfma_f32_16x16x32_bf16 v[28:31], v[174:177], v[190:193], v[28:31]
	v_mfma_f32_16x16x32_bf16 v[20:23], v[166:169], v[210:213], v[20:23]
	v_mfma_f32_16x16x32_bf16 v[12:15], v[174:177], v[210:213], v[12:15]
	v_mfma_f32_16x16x32_bf16 v[8:11], v[166:169], v[230:233], v[8:11]
	v_mfma_f32_16x16x32_bf16 v[4:7], v[174:177], v[230:233], v[4:7]
	v_mfma_f32_16x16x32_bf16 v[52:55], v[170:173], v[186:189], v[52:55]
	v_mfma_f32_16x16x32_bf16 v[44:47], v[178:181], v[186:189], v[44:47]
	v_mfma_f32_16x16x32_bf16 v[36:39], v[170:173], v[194:197], v[36:39]
	v_mfma_f32_16x16x32_bf16 v[28:31], v[178:181], v[194:197], v[28:31]
	v_mfma_f32_16x16x32_bf16 v[20:23], v[170:173], v[226:229], v[20:23]
	v_mfma_f32_16x16x32_bf16 v[12:15], v[178:181], v[226:229], v[12:15]
	v_mfma_f32_16x16x32_bf16 v[8:11], v[170:173], v[234:237], v[8:11]
	v_mfma_f32_16x16x32_bf16 v[4:7], v[178:181], v[234:237], v[4:7]
	s_setprio 0
	s_barrier
	s_add_i32 s49, 0, 0x18000
	v_add_u32_e32 v149, s49, v146
	s_add_i32 s50, 0, 0x1c000
	ds_read_b128 v[150:153], v149
	ds_read_b128 v[154:157], v149 offset:1024
	ds_read_b128 v[158:161], v149 offset:2048
	ds_read_b128 v[162:165], v149 offset:3072
	v_add_u32_e32 v149, s50, v146
	ds_read_b128 v[166:169], v149
	ds_read_b128 v[170:173], v149 offset:1024
	ds_read_b128 v[174:177], v149 offset:2048
	ds_read_b128 v[178:181], v149 offset:3072
	s_add_u32 s26, s26, 0x40000
	s_addc_u32 s27, s27, 0
	s_mov_b32 m0, s37
	v_lshl_add_u64 v[244:245], s[26:27], 0, v[132:133]
	ds_read_b128 v[182:185], v148 offset:32768
	ds_read_b128 v[186:189], v148 offset:33792
	ds_read_b128 v[190:193], v148 offset:34816
	ds_read_b128 v[194:197], v148 offset:35840
	ds_read_b128 v[210:213], v148 offset:36864
	ds_read_b128 v[226:229], v148 offset:37888
	ds_read_b128 v[230:233], v148 offset:38912
	s_mov_b32 m0, s17
	ds_read_b128 v[234:237], v148 offset:39936
	global_load_lds_dwordx4 v[240:241], off
	s_mov_b32 m0, s35
	s_nop 0
	global_load_lds_dwordx4 v[242:243], off
	s_mov_b32 m0, s37
	s_nop 0
	global_load_lds_dwordx4 v[244:245], off
	s_mov_b32 m0, s38
	v_lshl_add_u64 v[244:245], s[26:27], 0, v[136:137]
	global_load_lds_dwordx4 v[244:245], off
	s_waitcnt vmcnt(8)
	s_waitcnt lgkmcnt(0)
	s_barrier
; #define PG8_STAGE(bufoff, gbase, voff) do { _Pragma("unroll") for (int _i = 0; _i < 2; ++_i) \
;         __builtin_amdgcn_global_load_lds((const unsigned*)((const char*)(gbase) + (voff)[_i]), (PG8_LAS unsigned*)(lds + (bufoff) + ldsw + _i * 8192), 16, 0, 0); } while (0)
; #define PG8_LDA(dst, b, h) do { _Pragma("unroll") for (int m = 0; m < 4; ++m) _Pragma("unroll") for (int k = 0; k < 2; ++k) dst[m][k] = *(const PG8_LAS bf16x8*)(lds + PG8_SA(b, h) + aoff + m * 2048 + k * 1024); } while (0)
; #define PG8_MMA(ai, bj, At, Bt) do { __builtin_amdgcn_s_setprio(1); _Pragma("unroll") for (int m = 0; m < 4; ++m) _Pragma("unroll") for (int n = 0; n < 2; ++n) _Pragma("unroll") for (int k = 0; k < 2; ++k) \
;         acc[ai][bj][m][n] = __builtin_amdgcn_mfma_f32_16x16x32_bf16(Bt[n][k], At[m][k], acc[ai][bj][m][n], 0, 0, 0); __builtin_amdgcn_s_setprio(0); } while (0)
; #define PG8_WAIT_V(n) asm volatile("s_waitcnt vmcnt(" #n ")" ::: "memory")
; #define PG8_WAIT_L(n) asm volatile("s_waitcnt lgkmcnt(" #n ")" ::: "memory")
; #define PG8_BAR __builtin_amdgcn_s_barrier()
; #define PG8_SCHED __builtin_amdgcn_sched_barrier(0)
; template <class Epi, class Sched, bool ALIGN_EPI = false, bool SP2 = false>
; __device__ __forceinline__ void gemm_phase(PG8_LAS unsigned char* lds, const Gemm g, const Sched& S, const Epi& E) {
;     ...
;             PG8_WAIT_V(8); PG8_WAIT_L(0); PG8_BAR; PG8_MMA(0, 0, At, B0); PG8_MMA(0, 1, At, B1); PG8_BAR; PG8_SCHED;
;             PG8_LDA(At, 1, 1); PG8_STAGE(PG8_SB(1, 0), b3, voffB); PG8_STAGE(PG8_SB(1, 1), b3 + hstepB, voffB); PG8_STAGE(PG8_SA(1, 0), a3, voffA);
;             PG8_WAIT_V(8); PG8_WAIT_L(0); PG8_BAR; PG8_MMA(1, 0, At, B0); PG8_MMA(1, 1, At, B1); PG8_BAR; PG8_SCHED;
;     ...
;         if constexpr (ALIGN_EPI) { if (wr == 0) PG8_BAR; }
	s_setprio 1
	s_waitcnt lgkmcnt(0)
	v_mfma_f32_16x16x32_bf16 v[128:131], v[150:153], v[182:185], v[128:131]
	v_mfma_f32_16x16x32_bf16 v[124:127], v[158:161], v[182:185], v[124:127]
	v_mfma_f32_16x16x32_bf16 v[120:123], v[150:153], v[190:193], v[120:123]
	v_mfma_f32_16x16x32_bf16 v[112:115], v[158:161], v[190:193], v[112:115]
	v_mfma_f32_16x16x32_bf16 v[104:107], v[150:153], v[210:213], v[104:107]
	v_mfma_f32_16x16x32_bf16 v[96:99], v[158:161], v[210:213], v[96:99]
	v_mfma_f32_16x16x32_bf16 v[88:91], v[150:153], v[230:233], v[88:91]
	v_mfma_f32_16x16x32_bf16 v[80:83], v[158:161], v[230:233], v[80:83]
	v_mfma_f32_16x16x32_bf16 v[128:131], v[154:157], v[186:189], v[128:131]
	v_mfma_f32_16x16x32_bf16 v[124:127], v[162:165], v[186:189], v[124:127]
	v_mfma_f32_16x16x32_bf16 v[120:123], v[154:157], v[194:197], v[120:123]
	v_mfma_f32_16x16x32_bf16 v[112:115], v[162:165], v[194:197], v[112:115]
	v_mfma_f32_16x16x32_bf16 v[104:107], v[154:157], v[226:229], v[104:107]
	v_mfma_f32_16x16x32_bf16 v[96:99], v[162:165], v[226:229], v[96:99]
	v_mfma_f32_16x16x32_bf16 v[88:91], v[154:157], v[234:237], v[88:91]
	v_mfma_f32_16x16x32_bf16 v[80:83], v[162:165], v[234:237], v[80:83]
	s_setprio 0
	s_setprio 1
	v_mfma_f32_16x16x32_bf16 v[116:119], v[166:169], v[182:185], v[116:119]
	v_mfma_f32_16x16x32_bf16 v[108:111], v[174:177], v[182:185], v[108:111]
	v_mfma_f32_16x16x32_bf16 v[100:103], v[166:169], v[190:193], v[100:103]
	v_mfma_f32_16x16x32_bf16 v[92:95], v[174:177], v[190:193], v[92:95]
	v_mfma_f32_16x16x32_bf16 v[84:87], v[166:169], v[210:213], v[84:87]
	v_mfma_f32_16x16x32_bf16 v[76:79], v[174:177], v[210:213], v[76:79]
	v_mfma_f32_16x16x32_bf16 v[72:75], v[166:169], v[230:233], v[72:75]
	v_mfma_f32_16x16x32_bf16 v[68:71], v[174:177], v[230:233], v[68:71]
	v_mfma_f32_16x16x32_bf16 v[116:119], v[170:173], v[186:189], v[116:119]
	v_mfma_f32_16x16x32_bf16 v[108:111], v[178:181], v[186:189], v[108:111]
	v_mfma_f32_16x16x32_bf16 v[100:103], v[170:173], v[194:197], v[100:103]
	v_mfma_f32_16x16x32_bf16 v[92:95], v[178:181], v[194:197], v[92:95]
	v_mfma_f32_16x16x32_bf16 v[84:87], v[170:173], v[226:229], v[84:87]
	v_mfma_f32_16x16x32_bf16 v[76:79], v[178:181], v[226:229], v[76:79]
	v_mfma_f32_16x16x32_bf16 v[72:75], v[170:173], v[234:237], v[72:75]
	v_mfma_f32_16x16x32_bf16 v[68:71], v[178:181], v[234:237], v[68:71]
	s_setprio 0
	s_barrier
	s_add_i32 s26, s49, s34
	v_lshl_add_u64 v[144:145], v[144:145], 0, s[64:65]
	s_mov_b32 m0, s26
	ds_read_b128 v[182:185], v148 offset:49152
	ds_read_b128 v[186:189], v148 offset:50176
	ds_read_b128 v[190:193], v148 offset:51200
	ds_read_b128 v[194:197], v148 offset:52224
	ds_read_b128 v[210:213], v148 offset:53248
	ds_read_b128 v[226:229], v148 offset:54272
	ds_read_b128 v[230:233], v148 offset:55296
	ds_read_b128 v[234:237], v148 offset:56320
	global_load_lds_dwordx4 v[144:145], off
	s_add_i32 m0, s26, 0x2000
	s_add_u32 s24, s24, 0x40080
	v_lshl_add_u64 v[144:145], v[238:239], 0, s[64:65]
	s_addc_u32 s25, s25, 0
	s_add_i32 s26, s50, s34
	global_load_lds_dwordx4 v[144:145], off
	s_mov_b32 m0, s26
	v_lshl_add_u64 v[144:145], s[24:25], 0, v[134:135]
	global_load_lds_dwordx4 v[144:145], off
	s_add_i32 m0, s26, 0x2000
	v_lshl_add_u64 v[144:145], s[24:25], 0, v[138:139]
	global_load_lds_dwordx4 v[144:145], off
	s_waitcnt vmcnt(6)
	s_waitcnt lgkmcnt(0)
	s_barrier
	s_setprio 1
	s_waitcnt lgkmcnt(0)
	v_mfma_f32_16x16x32_bf16 v[64:67], v[150:153], v[182:185], v[64:67]
	v_mfma_f32_16x16x32_bf16 v[60:63], v[158:161], v[182:185], v[60:63]
	v_mfma_f32_16x16x32_bf16 v[56:59], v[150:153], v[190:193], v[56:59]
	v_mfma_f32_16x16x32_bf16 v[48:51], v[158:161], v[190:193], v[48:51]
	v_mfma_f32_16x16x32_bf16 v[40:43], v[150:153], v[210:213], v[40:43]
	v_mfma_f32_16x16x32_bf16 v[32:35], v[158:161], v[210:213], v[32:35]
	v_mfma_f32_16x16x32_bf16 v[24:27], v[150:153], v[230:233], v[24:27]
	v_mfma_f32_16x16x32_bf16 v[16:19], v[158:161], v[230:233], v[16:19]
	v_mfma_f32_16x16x32_bf16 v[64:67], v[154:157], v[186:189], v[64:67]
	v_mfma_f32_16x16x32_bf16 v[60:63], v[162:165], v[186:189], v[60:63]
	v_mfma_f32_16x16x32_bf16 v[56:59], v[154:157], v[194:197], v[56:59]
	v_mfma_f32_16x16x32_bf16 v[48:51], v[162:165], v[194:197], v[48:51]
	v_mfma_f32_16x16x32_bf16 v[40:43], v[154:157], v[226:229], v[40:43]
	v_mfma_f32_16x16x32_bf16 v[32:35], v[162:165], v[226:229], v[32:35]
	v_mfma_f32_16x16x32_bf16 v[24:27], v[154:157], v[234:237], v[24:27]
	v_mfma_f32_16x16x32_bf16 v[16:19], v[162:165], v[234:237], v[16:19]
	s_setprio 0
	s_setprio 1
	v_mfma_f32_16x16x32_bf16 v[52:55], v[166:169], v[182:185], v[52:55]
	v_mfma_f32_16x16x32_bf16 v[44:47], v[174:177], v[182:185], v[44:47]
	v_mfma_f32_16x16x32_bf16 v[36:39], v[166:169], v[190:193], v[36:39]
	v_mfma_f32_16x16x32_bf16 v[28:31], v[174:177], v[190:193], v[28:31]
	v_mfma_f32_16x16x32_bf16 v[20:23], v[166:169], v[210:213], v[20:23]
	v_mfma_f32_16x16x32_bf16 v[12:15], v[174:177], v[210:213], v[12:15]
	v_mfma_f32_16x16x32_bf16 v[8:11], v[166:169], v[230:233], v[8:11]
	v_mfma_f32_16x16x32_bf16 v[4:7], v[174:177], v[230:233], v[4:7]
	v_mfma_f32_16x16x32_bf16 v[52:55], v[170:173], v[186:189], v[52:55]
	v_mfma_f32_16x16x32_bf16 v[44:47], v[178:181], v[186:189], v[44:47]
	v_mfma_f32_16x16x32_bf16 v[36:39], v[170:173], v[194:197], v[36:39]
	v_mfma_f32_16x16x32_bf16 v[28:31], v[178:181], v[194:197], v[28:31]
	v_mfma_f32_16x16x32_bf16 v[20:23], v[170:173], v[226:229], v[20:23]
	v_mfma_f32_16x16x32_bf16 v[12:15], v[178:181], v[226:229], v[12:15]
	v_mfma_f32_16x16x32_bf16 v[8:11], v[170:173], v[234:237], v[8:11]
	v_mfma_f32_16x16x32_bf16 v[4:7], v[178:181], v[234:237], v[4:7]
	s_setprio 0
	s_barrier
	s_add_i32 s48, s48, 2
	s_add_u32 s46, s46, 0x100
	s_addc_u32 s47, s47, 0
	s_add_u32 s22, s22, 0x100
	s_addc_u32 s23, s23, 0
	s_cmp_gt_u32 s48, 13
	s_cbranch_scc0 .LBB0_1093
	s_and_b64 vcc, exec, s[10:11]
	s_cbranch_vccz .LBB0_1096
	s_barrier

; #define PG8_STAGE(bufoff, gbase, voff) do { _Pragma("unroll") for (int _i = 0; _i < 2; ++_i) \
;         __builtin_amdgcn_global_load_lds((const unsigned*)((const char*)(gbase) + (voff)[_i]), (PG8_LAS unsigned*)(lds + (bufoff) + ldsw + _i * 8192), 16, 0, 0); } while (0)
; #define PG8_LDA(dst, b, h) do { _Pragma("unroll") for (int m = 0; m < 4; ++m) _Pragma("unroll") for (int k = 0; k < 2; ++k) dst[m][k] = *(const PG8_LAS bf16x8*)(lds + PG8_SA(b, h) + aoff + m * 2048 + k * 1024); } while (0)
; #define PG8_LDB(dst, b, h) do { _Pragma("unroll") for (int n = 0; n < 2; ++n) _Pragma("unroll") for (int k = 0; k < 2; ++k) dst[n][k] = *(const PG8_LAS bf16x8*)(lds + PG8_SB(b, h) + boff + n * 2048 + k * 1024); } while (0)
; #define PG8_MMA(ai, bj, At, Bt) do { __builtin_amdgcn_s_setprio(1); _Pragma("unroll") for (int m = 0; m < 4; ++m) _Pragma("unroll") for (int n = 0; n < 2; ++n) _Pragma("unroll") for (int k = 0; k < 2; ++k) \
;         acc[ai][bj][m][n] = __builtin_amdgcn_mfma_f32_16x16x32_bf16(Bt[n][k], At[m][k], acc[ai][bj][m][n], 0, 0, 0); __builtin_amdgcn_s_setprio(0); } while (0)
; #define PG8_WAIT_V(n) asm volatile("s_waitcnt vmcnt(" #n ")" ::: "memory")
; #define PG8_WAIT_L(n) asm volatile("s_waitcnt lgkmcnt(" #n ")" ::: "memory")
; template <class Epi, class Sched, bool ALIGN_EPI = false, bool SP2 = false>
; __device__ __forceinline__ void gemm_phase(PG8_LAS unsigned char* lds, const Gemm g, const Sched& S, const Epi& E) {
;     ...
;             const bool last = (t == nt - 2);
;             const char* a1 = cA + (size_t)(t + 1) * kstep;
;             const char* a2 = last ? nA : cA + (size_t)(t + 2) * kstep; const char* b2 = last ? nB : cB + (size_t)(t + 2) * kstep;
;             const char* a3 = a2 + kstep; const char* b3 = b2 + kstep;
;             if (last && has_next) S.a_ready(nxt);
;             if constexpr (SP2) {
;             PG8_LDB(B0, 0, 0); PG8_LDB(B1, 0, 1); PG8_SCHED; PG8_LDA(At, 0, 0); PG8_STAGE(PG8_SA(1, 1), a1 + hstepA, voffA);
;             PG8_WAIT_V(8); PG8_WAIT_L(0); PG8_BAR; PG8_MMA(0, 0, At, B0); PG8_MMA(0, 1, At, B1); PG8_BAR; PG8_SCHED;
;             PG8_LDA(At, 0, 1); PG8_STAGE(PG8_SB(0, 0), b2, voffB); PG8_STAGE(PG8_SB(0, 1), b2 + hstepB, voffB); PG8_STAGE(PG8_SA(0, 0), a2, voffA);
;             PG8_WAIT_V(8); PG8_WAIT_L(0); PG8_BAR; PG8_MMA(1, 0, At, B0); PG8_MMA(1, 1, At, B1); PG8_BAR; PG8_SCHED;
.LBB0_1161:
	s_add_u32 s24, s22, 0xfffc0080
	s_addc_u32 s25, s23, -1
	s_add_i32 s49, 0, 0x10000
	s_cmp_eq_u32 s48, 12
	s_cselect_b32 s27, s19, s25
	s_cselect_b32 s26, s21, s24
	v_add_u32_e32 v149, s49, v154
	s_cselect_b32 s25, s44, s47
	s_cselect_b32 s24, s45, s46
	s_add_i32 s52, 0, 0x14000
	ds_read_b128 v[150:153], v149
	ds_read_b128 v[156:159], v149 offset:1024
	ds_read_b128 v[160:163], v149 offset:2048
	ds_read_b128 v[164:167], v149 offset:3072
	v_add_u32_e32 v149, s52, v154
	ds_read_b128 v[168:171], v149
	ds_read_b128 v[172:175], v149 offset:1024
	ds_read_b128 v[176:179], v149 offset:2048
	ds_read_b128 v[180:183], v149 offset:3072
	v_lshl_add_u64 v[196:197], s[22:23], 0, v[146:147]
	s_add_i32 m0, s31, 0xc000
	ds_read_b128 v[184:187], v155
	ds_read_b128 v[188:191], v155 offset:1024
	ds_read_b128 v[192:195], v155 offset:2048
	ds_read_b128 v[210:213], v155 offset:3072
	ds_read_b128 v[226:229], v155 offset:4096
	ds_read_b128 v[230:233], v155 offset:5120
	ds_read_b128 v[234:237], v155 offset:6144
	ds_read_b128 v[238:241], v155 offset:7168
	s_mov_b32 m0, s38
	v_lshl_add_u64 v[248:249], v[244:245], 0, s[64:65]
	global_load_lds_dwordx4 v[248:249], off
	s_mov_b32 m0, s39
	v_lshl_add_u64 v[248:249], v[246:247], 0, s[64:65]
	global_load_lds_dwordx4 v[248:249], off
	s_add_i32 m0, s31, 0xc000
	s_nop 0
	global_load_lds_dwordx4 v[196:197], off
	s_add_i32 m0, s31, 0xe000
	v_lshl_add_u64 v[196:197], s[22:23], 0, v[144:145]
	global_load_lds_dwordx4 v[196:197], off
	s_waitcnt vmcnt(8)
	s_waitcnt lgkmcnt(0)
	s_barrier
	s_setprio 1
	s_waitcnt lgkmcnt(0)
	v_mfma_f32_16x16x32_bf16 v[128:131], v[150:153], v[184:187], v[128:131]
	v_mfma_f32_16x16x32_bf16 v[124:127], v[160:163], v[184:187], v[124:127]
	v_mfma_f32_16x16x32_bf16 v[112:115], v[150:153], v[192:195], v[112:115]
	v_mfma_f32_16x16x32_bf16 v[108:111], v[160:163], v[192:195], v[108:111]
	v_mfma_f32_16x16x32_bf16 v[96:99], v[150:153], v[226:229], v[96:99]
	v_mfma_f32_16x16x32_bf16 v[92:95], v[160:163], v[226:229], v[92:95]
	v_mfma_f32_16x16x32_bf16 v[80:83], v[150:153], v[234:237], v[80:83]
	v_mfma_f32_16x16x32_bf16 v[76:79], v[160:163], v[234:237], v[76:79]
	v_mfma_f32_16x16x32_bf16 v[128:131], v[156:159], v[188:191], v[128:131]
	v_mfma_f32_16x16x32_bf16 v[124:127], v[164:167], v[188:191], v[124:127]
	v_mfma_f32_16x16x32_bf16 v[112:115], v[156:159], v[210:213], v[112:115]
	v_mfma_f32_16x16x32_bf16 v[108:111], v[164:167], v[210:213], v[108:111]
	v_mfma_f32_16x16x32_bf16 v[96:99], v[156:159], v[230:233], v[96:99]
	v_mfma_f32_16x16x32_bf16 v[92:95], v[164:167], v[230:233], v[92:95]
	v_mfma_f32_16x16x32_bf16 v[80:83], v[156:159], v[238:241], v[80:83]
	v_mfma_f32_16x16x32_bf16 v[76:79], v[164:167], v[238:241], v[76:79]
	s_setprio 0
	s_setprio 1
	v_mfma_f32_16x16x32_bf16 v[120:123], v[168:171], v[184:187], v[120:123]
	v_mfma_f32_16x16x32_bf16 v[116:119], v[176:179], v[184:187], v[116:119]
	v_mfma_f32_16x16x32_bf16 v[104:107], v[168:171], v[192:195], v[104:107]
	v_mfma_f32_16x16x32_bf16 v[100:103], v[176:179], v[192:195], v[100:103]
	v_mfma_f32_16x16x32_bf16 v[88:91], v[168:171], v[226:229], v[88:91]
	v_mfma_f32_16x16x32_bf16 v[84:87], v[176:179], v[226:229], v[84:87]
	v_mfma_f32_16x16x32_bf16 v[72:75], v[168:171], v[234:237], v[72:75]
	v_mfma_f32_16x16x32_bf16 v[68:71], v[176:179], v[234:237], v[68:71]
	v_mfma_f32_16x16x32_bf16 v[120:123], v[172:175], v[188:191], v[120:123]
	v_mfma_f32_16x16x32_bf16 v[116:119], v[180:183], v[188:191], v[116:119]
	v_mfma_f32_16x16x32_bf16 v[104:107], v[172:175], v[210:213], v[104:107]
	v_mfma_f32_16x16x32_bf16 v[100:103], v[180:183], v[210:213], v[100:103]
	v_mfma_f32_16x16x32_bf16 v[88:91], v[172:175], v[230:233], v[88:91]
	v_mfma_f32_16x16x32_bf16 v[84:87], v[180:183], v[230:233], v[84:87]
	v_mfma_f32_16x16x32_bf16 v[72:75], v[172:175], v[238:241], v[72:75]
	v_mfma_f32_16x16x32_bf16 v[68:71], v[180:183], v[238:241], v[68:71]
	s_setprio 0
	s_barrier
	s_add_i32 s49, s49, s30
	v_lshl_add_u64 v[196:197], s[24:25], 0, v[134:135]
	s_mov_b32 m0, s49
	ds_read_b128 v[184:187], v155 offset:16384
	ds_read_b128 v[188:191], v155 offset:17408
	ds_read_b128 v[192:195], v155 offset:18432
	ds_read_b128 v[210:213], v155 offset:19456
	ds_read_b128 v[226:229], v155 offset:20480
	ds_read_b128 v[230:233], v155 offset:21504
	ds_read_b128 v[234:237], v155 offset:22528
	ds_read_b128 v[238:241], v155 offset:23552
	global_load_lds_dwordx4 v[196:197], off
	s_add_i32 m0, s49, 0x2000
	s_add_u32 s50, s24, 0x40000
	v_lshl_add_u64 v[242:243], s[24:25], 0, v[138:139]
	s_addc_u32 s51, s25, 0
	s_add_i32 s49, s52, s30
	global_load_lds_dwordx4 v[242:243], off
	v_lshl_add_u64 v[244:245], s[50:51], 0, v[134:135]
	s_mov_b32 m0, s49
	v_lshl_add_u64 v[246:247], s[26:27], 0, v[136:137]
	global_load_lds_dwordx4 v[244:245], off
	s_add_i32 m0, s49, 0x2000
	v_lshl_add_u64 v[244:245], s[50:51], 0, v[138:139]
	global_load_lds_dwordx4 v[244:245], off
	v_lshl_add_u64 v[244:245], s[26:27], 0, v[132:133]
	s_waitcnt vmcnt(6)
	s_waitcnt lgkmcnt(0)
	s_barrier
; #define PG8_STAGE(bufoff, gbase, voff) do { _Pragma("unroll") for (int _i = 0; _i < 2; ++_i) \
;         __builtin_amdgcn_global_load_lds((const unsigned*)((const char*)(gbase) + (voff)[_i]), (PG8_LAS unsigned*)(lds + (bufoff) + ldsw + _i * 8192), 16, 0, 0); } while (0)
; #define PG8_LDA(dst, b, h) do { _Pragma("unroll") for (int m = 0; m < 4; ++m) _Pragma("unroll") for (int k = 0; k < 2; ++k) dst[m][k] = *(const PG8_LAS bf16x8*)(lds + PG8_SA(b, h) + aoff + m * 2048 + k * 1024); } while (0)
; #define PG8_LDB(dst, b, h) do { _Pragma("unroll") for (int n = 0; n < 2; ++n) _Pragma("unroll") for (int k = 0; k < 2; ++k) dst[n][k] = *(const PG8_LAS bf16x8*)(lds + PG8_SB(b, h) + boff + n * 2048 + k * 1024); } while (0)
; #define PG8_MMA(ai, bj, At, Bt) do { __builtin_amdgcn_s_setprio(1); _Pragma("unroll") for (int m = 0; m < 4; ++m) _Pragma("unroll") for (int n = 0; n < 2; ++n) _Pragma("unroll") for (int k = 0; k < 2; ++k) \
;         acc[ai][bj][m][n] = __builtin_amdgcn_mfma_f32_16x16x32_bf16(Bt[n][k], At[m][k], acc[ai][bj][m][n], 0, 0, 0); __builtin_amdgcn_s_setprio(0); } while (0)
; #define PG8_WAIT_V(n) asm volatile("s_waitcnt vmcnt(" #n ")" ::: "memory")
; #define PG8_WAIT_L(n) asm volatile("s_waitcnt lgkmcnt(" #n ")" ::: "memory")
; #define PG8_BAR __builtin_amdgcn_s_barrier()
; #define PG8_SCHED __builtin_amdgcn_sched_barrier(0)
; template <class Epi, class Sched, bool ALIGN_EPI = false, bool SP2 = false>
; __device__ __forceinline__ void gemm_phase(PG8_LAS unsigned char* lds, const Gemm g, const Sched& S, const Epi& E) {
;     ...
;             PG8_WAIT_V(8); PG8_WAIT_L(0); PG8_BAR; PG8_MMA(1, 0, At, B0); PG8_MMA(1, 1, At, B1); PG8_BAR; PG8_SCHED;
;             PG8_LDB(B0, 1, 0); PG8_LDB(B1, 1, 1); PG8_SCHED; PG8_LDA(At, 1, 0); PG8_STAGE(PG8_SA(0, 1), a2 + hstepA, voffA);
;             PG8_WAIT_V(8); PG8_WAIT_L(0); PG8_BAR; PG8_MMA(0, 0, At, B0); PG8_MMA(0, 1, At, B1); PG8_BAR; PG8_SCHED;
	s_setprio 1
	s_waitcnt lgkmcnt(0)
	v_mfma_f32_16x16x32_bf16 v[64:67], v[150:153], v[184:187], v[64:67]
	v_mfma_f32_16x16x32_bf16 v[60:63], v[160:163], v[184:187], v[60:63]
	v_mfma_f32_16x16x32_bf16 v[52:55], v[150:153], v[192:195], v[52:55]
	v_mfma_f32_16x16x32_bf16 v[44:47], v[160:163], v[192:195], v[44:47]
	v_mfma_f32_16x16x32_bf16 v[36:39], v[150:153], v[226:229], v[36:39]
	v_mfma_f32_16x16x32_bf16 v[28:31], v[160:163], v[226:229], v[28:31]
	v_mfma_f32_16x16x32_bf16 v[20:23], v[150:153], v[234:237], v[20:23]
	v_mfma_f32_16x16x32_bf16 v[12:15], v[160:163], v[234:237], v[12:15]
	v_mfma_f32_16x16x32_bf16 v[64:67], v[156:159], v[188:191], v[64:67]
	v_mfma_f32_16x16x32_bf16 v[60:63], v[164:167], v[188:191], v[60:63]
	v_mfma_f32_16x16x32_bf16 v[52:55], v[156:159], v[210:213], v[52:55]
	v_mfma_f32_16x16x32_bf16 v[44:47], v[164:167], v[210:213], v[44:47]
	v_mfma_f32_16x16x32_bf16 v[36:39], v[156:159], v[230:233], v[36:39]
	v_mfma_f32_16x16x32_bf16 v[28:31], v[164:167], v[230:233], v[28:31]
	v_mfma_f32_16x16x32_bf16 v[20:23], v[156:159], v[238:241], v[20:23]
	v_mfma_f32_16x16x32_bf16 v[12:15], v[164:167], v[238:241], v[12:15]
	s_setprio 0
	s_setprio 1
	v_mfma_f32_16x16x32_bf16 v[56:59], v[168:171], v[184:187], v[56:59]
	v_mfma_f32_16x16x32_bf16 v[48:51], v[176:179], v[184:187], v[48:51]
	v_mfma_f32_16x16x32_bf16 v[40:43], v[168:171], v[192:195], v[40:43]
	v_mfma_f32_16x16x32_bf16 v[32:35], v[176:179], v[192:195], v[32:35]
	v_mfma_f32_16x16x32_bf16 v[24:27], v[168:171], v[226:229], v[24:27]
	v_mfma_f32_16x16x32_bf16 v[16:19], v[176:179], v[226:229], v[16:19]
	v_mfma_f32_16x16x32_bf16 v[8:11], v[168:171], v[234:237], v[8:11]
	v_mfma_f32_16x16x32_bf16 v[4:7], v[176:179], v[234:237], v[4:7]
	v_mfma_f32_16x16x32_bf16 v[56:59], v[172:175], v[188:191], v[56:59]
	v_mfma_f32_16x16x32_bf16 v[48:51], v[180:183], v[188:191], v[48:51]
	v_mfma_f32_16x16x32_bf16 v[40:43], v[172:175], v[210:213], v[40:43]
	v_mfma_f32_16x16x32_bf16 v[32:35], v[180:183], v[210:213], v[32:35]
	v_mfma_f32_16x16x32_bf16 v[24:27], v[172:175], v[230:233], v[24:27]
	v_mfma_f32_16x16x32_bf16 v[16:19], v[180:183], v[230:233], v[16:19]
	v_mfma_f32_16x16x32_bf16 v[8:11], v[172:175], v[238:241], v[8:11]
	v_mfma_f32_16x16x32_bf16 v[4:7], v[180:183], v[238:241], v[4:7]
	s_setprio 0
	s_barrier
	s_add_i32 s49, 0, 0x18000
	v_add_u32_e32 v149, s49, v154
	s_add_i32 s50, 0, 0x1c000
	ds_read_b128 v[150:153], v149
	ds_read_b128 v[156:159], v149 offset:1024
	ds_read_b128 v[160:163], v149 offset:2048
	ds_read_b128 v[164:167], v149 offset:3072
	v_add_u32_e32 v149, s50, v154
	ds_read_b128 v[168:171], v149
	ds_read_b128 v[172:175], v149 offset:1024
	ds_read_b128 v[176:179], v149 offset:2048
	ds_read_b128 v[180:183], v149 offset:3072
	s_add_u32 s26, s26, 0x40000
	s_addc_u32 s27, s27, 0
	s_mov_b32 m0, s34
	v_lshl_add_u64 v[248:249], s[26:27], 0, v[132:133]
	ds_read_b128 v[184:187], v155 offset:32768
	ds_read_b128 v[188:191], v155 offset:33792
	ds_read_b128 v[192:195], v155 offset:34816
	ds_read_b128 v[210:213], v155 offset:35840
	ds_read_b128 v[226:229], v155 offset:36864
	ds_read_b128 v[230:233], v155 offset:37888
	ds_read_b128 v[234:237], v155 offset:38912
	s_mov_b32 m0, s31
	ds_read_b128 v[238:241], v155 offset:39936
	global_load_lds_dwordx4 v[244:245], off
	s_mov_b32 m0, s33
	s_nop 0
	global_load_lds_dwordx4 v[246:247], off
	s_mov_b32 m0, s34
	s_nop 0
	global_load_lds_dwordx4 v[248:249], off
	s_mov_b32 m0, s35
	v_lshl_add_u64 v[248:249], s[26:27], 0, v[136:137]
	global_load_lds_dwordx4 v[248:249], off
	s_waitcnt vmcnt(8)
	s_waitcnt lgkmcnt(0)
	s_barrier
; #define PG8_STAGE(bufoff, gbase, voff) do { _Pragma("unroll") for (int _i = 0; _i < 2; ++_i) \
;         __builtin_amdgcn_global_load_lds((const unsigned*)((const char*)(gbase) + (voff)[_i]), (PG8_LAS unsigned*)(lds + (bufoff) + ldsw + _i * 8192), 16, 0, 0); } while (0)
; #define PG8_LDA(dst, b, h) do { _Pragma("unroll") for (int m = 0; m < 4; ++m) _Pragma("unroll") for (int k = 0; k < 2; ++k) dst[m][k] = *(const PG8_LAS bf16x8*)(lds + PG8_SA(b, h) + aoff + m * 2048 + k * 1024); } while (0)
; #define PG8_MMA(ai, bj, At, Bt) do { __builtin_amdgcn_s_setprio(1); _Pragma("unroll") for (int m = 0; m < 4; ++m) _Pragma("unroll") for (int n = 0; n < 2; ++n) _Pragma("unroll") for (int k = 0; k < 2; ++k) \
;         acc[ai][bj][m][n] = __builtin_amdgcn_mfma_f32_16x16x32_bf16(Bt[n][k], At[m][k], acc[ai][bj][m][n], 0, 0, 0); __builtin_amdgcn_s_setprio(0); } while (0)
; #define PG8_WAIT_V(n) asm volatile("s_waitcnt vmcnt(" #n ")" ::: "memory")
; #define PG8_WAIT_L(n) asm volatile("s_waitcnt lgkmcnt(" #n ")" ::: "memory")
; #define PG8_BAR __builtin_amdgcn_s_barrier()
; #define PG8_SCHED __builtin_amdgcn_sched_barrier(0)
; template <class Epi, class Sched, bool ALIGN_EPI = false, bool SP2 = false>
; __device__ __forceinline__ void gemm_phase(PG8_LAS unsigned char* lds, const Gemm g, const Sched& S, const Epi& E) {
;     ...
;             PG8_WAIT_V(8); PG8_WAIT_L(0); PG8_BAR; PG8_MMA(0, 0, At, B0); PG8_MMA(0, 1, At, B1); PG8_BAR; PG8_SCHED;
;             PG8_LDA(At, 1, 1); PG8_STAGE(PG8_SB(1, 0), b3, voffB); PG8_STAGE(PG8_SB(1, 1), b3 + hstepB, voffB); PG8_STAGE(PG8_SA(1, 0), a3, voffA);
;             PG8_WAIT_V(8); PG8_WAIT_L(0); PG8_BAR; PG8_MMA(1, 0, At, B0); PG8_MMA(1, 1, At, B1); PG8_BAR; PG8_SCHED;
;     ...
;         if constexpr (ALIGN_EPI) { if (wr == 0) PG8_BAR; }
	s_setprio 1
	s_waitcnt lgkmcnt(0)
	v_mfma_f32_16x16x32_bf16 v[128:131], v[150:153], v[184:187], v[128:131]
	v_mfma_f32_16x16x32_bf16 v[124:127], v[160:163], v[184:187], v[124:127]
	v_mfma_f32_16x16x32_bf16 v[112:115], v[150:153], v[192:195], v[112:115]
	v_mfma_f32_16x16x32_bf16 v[108:111], v[160:163], v[192:195], v[108:111]
	v_mfma_f32_16x16x32_bf16 v[96:99], v[150:153], v[226:229], v[96:99]
	v_mfma_f32_16x16x32_bf16 v[92:95], v[160:163], v[226:229], v[92:95]
	v_mfma_f32_16x16x32_bf16 v[80:83], v[150:153], v[234:237], v[80:83]
	v_mfma_f32_16x16x32_bf16 v[76:79], v[160:163], v[234:237], v[76:79]
	v_mfma_f32_16x16x32_bf16 v[128:131], v[156:159], v[188:191], v[128:131]
	v_mfma_f32_16x16x32_bf16 v[124:127], v[164:167], v[188:191], v[124:127]
	v_mfma_f32_16x16x32_bf16 v[112:115], v[156:159], v[210:213], v[112:115]
	v_mfma_f32_16x16x32_bf16 v[108:111], v[164:167], v[210:213], v[108:111]
	v_mfma_f32_16x16x32_bf16 v[96:99], v[156:159], v[230:233], v[96:99]
	v_mfma_f32_16x16x32_bf16 v[92:95], v[164:167], v[230:233], v[92:95]
	v_mfma_f32_16x16x32_bf16 v[80:83], v[156:159], v[238:241], v[80:83]
	v_mfma_f32_16x16x32_bf16 v[76:79], v[164:167], v[238:241], v[76:79]
	s_setprio 0
	s_setprio 1
	v_mfma_f32_16x16x32_bf16 v[120:123], v[168:171], v[184:187], v[120:123]
	v_mfma_f32_16x16x32_bf16 v[116:119], v[176:179], v[184:187], v[116:119]
	v_mfma_f32_16x16x32_bf16 v[104:107], v[168:171], v[192:195], v[104:107]
	v_mfma_f32_16x16x32_bf16 v[100:103], v[176:179], v[192:195], v[100:103]
	v_mfma_f32_16x16x32_bf16 v[88:91], v[168:171], v[226:229], v[88:91]
	v_mfma_f32_16x16x32_bf16 v[84:87], v[176:179], v[226:229], v[84:87]
	v_mfma_f32_16x16x32_bf16 v[72:75], v[168:171], v[234:237], v[72:75]
	v_mfma_f32_16x16x32_bf16 v[68:71], v[176:179], v[234:237], v[68:71]
	v_mfma_f32_16x16x32_bf16 v[120:123], v[172:175], v[188:191], v[120:123]
	v_mfma_f32_16x16x32_bf16 v[116:119], v[180:183], v[188:191], v[116:119]
	v_mfma_f32_16x16x32_bf16 v[104:107], v[172:175], v[210:213], v[104:107]
	v_mfma_f32_16x16x32_bf16 v[100:103], v[180:183], v[210:213], v[100:103]
	v_mfma_f32_16x16x32_bf16 v[88:91], v[172:175], v[230:233], v[88:91]
	v_mfma_f32_16x16x32_bf16 v[84:87], v[180:183], v[230:233], v[84:87]
	v_mfma_f32_16x16x32_bf16 v[72:75], v[172:175], v[238:241], v[72:75]
	v_mfma_f32_16x16x32_bf16 v[68:71], v[180:183], v[238:241], v[68:71]
	s_setprio 0
	s_barrier
	s_add_i32 s26, s49, s30
	v_lshl_add_u64 v[196:197], v[196:197], 0, s[64:65]
	s_mov_b32 m0, s26
	ds_read_b128 v[184:187], v155 offset:49152
	ds_read_b128 v[188:191], v155 offset:50176
	ds_read_b128 v[192:195], v155 offset:51200
	ds_read_b128 v[210:213], v155 offset:52224
	ds_read_b128 v[226:229], v155 offset:53248
	ds_read_b128 v[230:233], v155 offset:54272
	ds_read_b128 v[234:237], v155 offset:55296
	ds_read_b128 v[238:241], v155 offset:56320
	global_load_lds_dwordx4 v[196:197], off
	s_add_i32 m0, s26, 0x2000
	s_add_u32 s24, s24, 0x40080
	v_lshl_add_u64 v[196:197], v[242:243], 0, s[64:65]
	s_addc_u32 s25, s25, 0
	s_add_i32 s26, s50, s30
	global_load_lds_dwordx4 v[196:197], off
	s_mov_b32 m0, s26
	v_lshl_add_u64 v[196:197], s[24:25], 0, v[134:135]
	global_load_lds_dwordx4 v[196:197], off
	s_add_i32 m0, s26, 0x2000
	v_lshl_add_u64 v[196:197], s[24:25], 0, v[138:139]
	global_load_lds_dwordx4 v[196:197], off
	s_waitcnt vmcnt(6)
	s_waitcnt lgkmcnt(0)
	s_barrier
	s_setprio 1
	s_waitcnt lgkmcnt(0)
	v_mfma_f32_16x16x32_bf16 v[64:67], v[150:153], v[184:187], v[64:67]
	v_mfma_f32_16x16x32_bf16 v[60:63], v[160:163], v[184:187], v[60:63]
	v_mfma_f32_16x16x32_bf16 v[52:55], v[150:153], v[192:195], v[52:55]
	v_mfma_f32_16x16x32_bf16 v[44:47], v[160:163], v[192:195], v[44:47]
	v_mfma_f32_16x16x32_bf16 v[36:39], v[150:153], v[226:229], v[36:39]
	v_mfma_f32_16x16x32_bf16 v[28:31], v[160:163], v[226:229], v[28:31]
	v_mfma_f32_16x16x32_bf16 v[20:23], v[150:153], v[234:237], v[20:23]
	v_mfma_f32_16x16x32_bf16 v[12:15], v[160:163], v[234:237], v[12:15]
	v_mfma_f32_16x16x32_bf16 v[64:67], v[156:159], v[188:191], v[64:67]
	v_mfma_f32_16x16x32_bf16 v[60:63], v[164:167], v[188:191], v[60:63]
	v_mfma_f32_16x16x32_bf16 v[52:55], v[156:159], v[210:213], v[52:55]
	v_mfma_f32_16x16x32_bf16 v[44:47], v[164:167], v[210:213], v[44:47]
	v_mfma_f32_16x16x32_bf16 v[36:39], v[156:159], v[230:233], v[36:39]
	v_mfma_f32_16x16x32_bf16 v[28:31], v[164:167], v[230:233], v[28:31]
	v_mfma_f32_16x16x32_bf16 v[20:23], v[156:159], v[238:241], v[20:23]
	v_mfma_f32_16x16x32_bf16 v[12:15], v[164:167], v[238:241], v[12:15]
	s_setprio 0
	s_setprio 1
	v_mfma_f32_16x16x32_bf16 v[56:59], v[168:171], v[184:187], v[56:59]
	v_mfma_f32_16x16x32_bf16 v[48:51], v[176:179], v[184:187], v[48:51]
	v_mfma_f32_16x16x32_bf16 v[40:43], v[168:171], v[192:195], v[40:43]
	v_mfma_f32_16x16x32_bf16 v[32:35], v[176:179], v[192:195], v[32:35]
	v_mfma_f32_16x16x32_bf16 v[24:27], v[168:171], v[226:229], v[24:27]
	v_mfma_f32_16x16x32_bf16 v[16:19], v[176:179], v[226:229], v[16:19]
	v_mfma_f32_16x16x32_bf16 v[8:11], v[168:171], v[234:237], v[8:11]
	v_mfma_f32_16x16x32_bf16 v[4:7], v[176:179], v[234:237], v[4:7]
	v_mfma_f32_16x16x32_bf16 v[56:59], v[172:175], v[188:191], v[56:59]
	v_mfma_f32_16x16x32_bf16 v[48:51], v[180:183], v[188:191], v[48:51]
	v_mfma_f32_16x16x32_bf16 v[40:43], v[172:175], v[210:213], v[40:43]
	v_mfma_f32_16x16x32_bf16 v[32:35], v[180:183], v[210:213], v[32:35]
	v_mfma_f32_16x16x32_bf16 v[24:27], v[172:175], v[230:233], v[24:27]
	v_mfma_f32_16x16x32_bf16 v[16:19], v[180:183], v[230:233], v[16:19]
	v_mfma_f32_16x16x32_bf16 v[8:11], v[172:175], v[238:241], v[8:11]
	v_mfma_f32_16x16x32_bf16 v[4:7], v[180:183], v[238:241], v[4:7]
	s_setprio 0
	s_barrier
	s_add_i32 s48, s48, 2
	s_add_u32 s46, s46, 0x100
	s_addc_u32 s47, s47, 0
	s_add_u32 s22, s22, 0x100
	s_addc_u32 s23, s23, 0
	s_cmp_gt_u32 s48, 13
	s_cbranch_scc0 .LBB0_1161
	s_and_b64 vcc, exec, s[12:13]
	s_cbranch_vccz .LBB0_1164
	s_barrier

; #define PG8_STAGE(bufoff, gbase, voff) do { _Pragma("unroll") for (int _i = 0; _i < 2; ++_i) \
;         __builtin_amdgcn_global_load_lds((const unsigned*)((const char*)(gbase) + (voff)[_i]), (PG8_LAS unsigned*)(lds + (bufoff) + ldsw + _i * 8192), 16, 0, 0); } while (0)
; #define PG8_LDA(dst, b, h) do { _Pragma("unroll") for (int m = 0; m < 4; ++m) _Pragma("unroll") for (int k = 0; k < 2; ++k) dst[m][k] = *(const PG8_LAS bf16x8*)(lds + PG8_SA(b, h) + aoff + m * 2048 + k * 1024); } while (0)
; #define PG8_LDB(dst, b, h) do { _Pragma("unroll") for (int n = 0; n < 2; ++n) _Pragma("unroll") for (int k = 0; k < 2; ++k) dst[n][k] = *(const PG8_LAS bf16x8*)(lds + PG8_SB(b, h) + boff + n * 2048 + k * 1024); } while (0)
; #define PG8_MMA(ai, bj, At, Bt) do { __builtin_amdgcn_s_setprio(1); _Pragma("unroll") for (int m = 0; m < 4; ++m) _Pragma("unroll") for (int n = 0; n < 2; ++n) _Pragma("unroll") for (int k = 0; k < 2; ++k) \
;         acc[ai][bj][m][n] = __builtin_amdgcn_mfma_f32_16x16x32_bf16(Bt[n][k], At[m][k], acc[ai][bj][m][n], 0, 0, 0); __builtin_amdgcn_s_setprio(0); } while (0)
; #define PG8_WAIT_V(n) asm volatile("s_waitcnt vmcnt(" #n ")" ::: "memory")
; #define PG8_WAIT_L(n) asm volatile("s_waitcnt lgkmcnt(" #n ")" ::: "memory")
; template <class Epi, class Sched, bool ALIGN_EPI = false, bool SP2 = false>
; __device__ __forceinline__ void gemm_phase(PG8_LAS unsigned char* lds, const Gemm g, const Sched& S, const Epi& E) {
;     ...
;             const bool last = (t == nt - 2);
;             const char* a1 = cA + (size_t)(t + 1) * kstep;
;             const char* a2 = last ? nA : cA + (size_t)(t + 2) * kstep; const char* b2 = last ? nB : cB + (size_t)(t + 2) * kstep;
;             const char* a3 = a2 + kstep; const char* b3 = b2 + kstep;
;             if (last && has_next) S.a_ready(nxt);
;             if constexpr (SP2) {
;             PG8_LDB(B0, 0, 0); PG8_LDB(B1, 0, 1); PG8_SCHED; PG8_LDA(At, 0, 0); PG8_STAGE(PG8_SA(1, 1), a1 + hstepA, voffA);
;             PG8_WAIT_V(8); PG8_WAIT_L(0); PG8_BAR; PG8_MMA(0, 0, At, B0); PG8_MMA(0, 1, At, B1); PG8_BAR; PG8_SCHED;
;             PG8_LDA(At, 0, 1); PG8_STAGE(PG8_SB(0, 0), b2, voffB); PG8_STAGE(PG8_SB(0, 1), b2 + hstepB, voffB); PG8_STAGE(PG8_SA(0, 0), a2, voffA);
;             PG8_WAIT_V(8); PG8_WAIT_L(0); PG8_BAR; PG8_MMA(1, 0, At, B0); PG8_MMA(1, 1, At, B1); PG8_BAR; PG8_SCHED;
.LBB0_1236:
	s_add_i32 s49, s18, 2
	s_add_u32 s19, s16, 0xfffc0080
	s_addc_u32 s20, s17, -1
	s_add_i32 s50, 0, 0x10000
	s_cmp_eq_u32 s37, s18
	s_cselect_b32 s21, s43, s20
	s_cselect_b32 s20, s44, s19
	s_cselect_b32 s19, s45, s48
	s_cselect_b32 s18, s46, s47
	s_add_i32 s52, 0, 0x14000
	v_add_u32_e32 v160, s50, v146
	v_add_u32_e32 v176, s52, v146
	ds_read_b128 v[148:151], v160
	ds_read_b128 v[152:155], v160 offset:1024
	ds_read_b128 v[156:159], v160 offset:2048
	ds_read_b128 v[160:163], v160 offset:3072
	ds_read_b128 v[164:167], v176
	ds_read_b128 v[168:171], v176 offset:1024
	ds_read_b128 v[172:175], v176 offset:2048
	ds_read_b128 v[176:179], v176 offset:3072
	v_lshl_add_u64 v[196:197], s[16:17], 0, v[144:145]
	s_add_i32 m0, s28, 0xc000
	ds_read_b128 v[180:183], v147
	ds_read_b128 v[184:187], v147 offset:1024
	ds_read_b128 v[188:191], v147 offset:2048
	ds_read_b128 v[192:195], v147 offset:3072
	ds_read_b128 v[210:213], v147 offset:4096
	ds_read_b128 v[226:229], v147 offset:5120
	ds_read_b128 v[230:233], v147 offset:6144
	ds_read_b128 v[234:237], v147 offset:7168
	global_load_lds_dwordx4 v[196:197], off
	s_add_i32 m0, s28, 0xe000
	v_lshl_add_u64 v[196:197], s[16:17], 0, v[142:143]
	global_load_lds_dwordx4 v[196:197], off
	s_waitcnt vmcnt(8)
	s_waitcnt lgkmcnt(0)
	s_barrier
	s_setprio 1
	s_waitcnt lgkmcnt(0)
	v_mfma_f32_16x16x32_bf16 v[124:127], v[148:151], v[180:183], v[124:127]
	v_mfma_f32_16x16x32_bf16 v[128:131], v[156:159], v[180:183], v[128:131]
	v_mfma_f32_16x16x32_bf16 v[112:115], v[148:151], v[188:191], v[112:115]
	v_mfma_f32_16x16x32_bf16 v[108:111], v[156:159], v[188:191], v[108:111]
	v_mfma_f32_16x16x32_bf16 v[96:99], v[148:151], v[210:213], v[96:99]
	v_mfma_f32_16x16x32_bf16 v[92:95], v[156:159], v[210:213], v[92:95]
	v_mfma_f32_16x16x32_bf16 v[80:83], v[148:151], v[230:233], v[80:83]
	v_mfma_f32_16x16x32_bf16 v[76:79], v[156:159], v[230:233], v[76:79]
	v_mfma_f32_16x16x32_bf16 v[124:127], v[152:155], v[184:187], v[124:127]
	v_mfma_f32_16x16x32_bf16 v[128:131], v[160:163], v[184:187], v[128:131]
	v_mfma_f32_16x16x32_bf16 v[112:115], v[152:155], v[192:195], v[112:115]
	v_mfma_f32_16x16x32_bf16 v[108:111], v[160:163], v[192:195], v[108:111]
	v_mfma_f32_16x16x32_bf16 v[96:99], v[152:155], v[226:229], v[96:99]
	v_mfma_f32_16x16x32_bf16 v[92:95], v[160:163], v[226:229], v[92:95]
	v_mfma_f32_16x16x32_bf16 v[80:83], v[152:155], v[234:237], v[80:83]
	v_mfma_f32_16x16x32_bf16 v[76:79], v[160:163], v[234:237], v[76:79]
	s_setprio 0
	s_setprio 1
	v_mfma_f32_16x16x32_bf16 v[120:123], v[164:167], v[180:183], v[120:123]
	v_mfma_f32_16x16x32_bf16 v[116:119], v[172:175], v[180:183], v[116:119]
	v_mfma_f32_16x16x32_bf16 v[104:107], v[164:167], v[188:191], v[104:107]
	v_mfma_f32_16x16x32_bf16 v[100:103], v[172:175], v[188:191], v[100:103]
	v_mfma_f32_16x16x32_bf16 v[88:91], v[164:167], v[210:213], v[88:91]
	v_mfma_f32_16x16x32_bf16 v[84:87], v[172:175], v[210:213], v[84:87]
	v_mfma_f32_16x16x32_bf16 v[72:75], v[164:167], v[230:233], v[72:75]
	v_mfma_f32_16x16x32_bf16 v[68:71], v[172:175], v[230:233], v[68:71]
	v_mfma_f32_16x16x32_bf16 v[120:123], v[168:171], v[184:187], v[120:123]
	v_mfma_f32_16x16x32_bf16 v[116:119], v[176:179], v[184:187], v[116:119]
	v_mfma_f32_16x16x32_bf16 v[104:107], v[168:171], v[192:195], v[104:107]
	v_mfma_f32_16x16x32_bf16 v[100:103], v[176:179], v[192:195], v[100:103]
	v_mfma_f32_16x16x32_bf16 v[88:91], v[168:171], v[226:229], v[88:91]
	v_mfma_f32_16x16x32_bf16 v[84:87], v[176:179], v[226:229], v[84:87]
	v_mfma_f32_16x16x32_bf16 v[72:75], v[168:171], v[234:237], v[72:75]
	v_mfma_f32_16x16x32_bf16 v[68:71], v[176:179], v[234:237], v[68:71]
	s_setprio 0
	s_barrier
	s_add_i32 s50, s50, s26
	v_lshl_add_u64 v[196:197], s[18:19], 0, v[134:135]
	s_mov_b32 m0, s50
	ds_read_b128 v[180:183], v147 offset:16384
	ds_read_b128 v[184:187], v147 offset:17408
	ds_read_b128 v[188:191], v147 offset:18432
	ds_read_b128 v[192:195], v147 offset:19456
	ds_read_b128 v[210:213], v147 offset:20480
	ds_read_b128 v[226:229], v147 offset:21504
	ds_read_b128 v[230:233], v147 offset:22528
	ds_read_b128 v[234:237], v147 offset:23552
	global_load_lds_dwordx4 v[196:197], off
	s_add_i32 m0, s50, 0x2000
	s_add_u32 s50, s18, 0x80000
	v_lshl_add_u64 v[238:239], s[18:19], 0, v[138:139]
	s_addc_u32 s51, s19, 0
	s_add_i32 s52, s52, s26
	global_load_lds_dwordx4 v[238:239], off
	v_lshl_add_u64 v[240:241], s[50:51], 0, v[134:135]
	s_mov_b32 m0, s52
	v_lshl_add_u64 v[242:243], s[20:21], 0, v[136:137]
	global_load_lds_dwordx4 v[240:241], off
	s_add_i32 m0, s52, 0x2000
	v_lshl_add_u64 v[240:241], s[50:51], 0, v[138:139]
	global_load_lds_dwordx4 v[240:241], off
	s_mov_b32 m0, s28
	v_lshl_add_u64 v[240:241], s[20:21], 0, v[132:133]
	global_load_lds_dwordx4 v[240:241], off
	s_mov_b32 m0, s29
	s_nop 0
	global_load_lds_dwordx4 v[242:243], off
	s_waitcnt vmcnt(8)
	s_waitcnt lgkmcnt(0)
	s_barrier
; #define PG8_STAGE(bufoff, gbase, voff) do { _Pragma("unroll") for (int _i = 0; _i < 2; ++_i) \
;         __builtin_amdgcn_global_load_lds((const unsigned*)((const char*)(gbase) + (voff)[_i]), (PG8_LAS unsigned*)(lds + (bufoff) + ldsw + _i * 8192), 16, 0, 0); } while (0)
; #define PG8_LDA(dst, b, h) do { _Pragma("unroll") for (int m = 0; m < 4; ++m) _Pragma("unroll") for (int k = 0; k < 2; ++k) dst[m][k] = *(const PG8_LAS bf16x8*)(lds + PG8_SA(b, h) + aoff + m * 2048 + k * 1024); } while (0)
; #define PG8_LDB(dst, b, h) do { _Pragma("unroll") for (int n = 0; n < 2; ++n) _Pragma("unroll") for (int k = 0; k < 2; ++k) dst[n][k] = *(const PG8_LAS bf16x8*)(lds + PG8_SB(b, h) + boff + n * 2048 + k * 1024); } while (0)
; #define PG8_MMA(ai, bj, At, Bt) do { __builtin_amdgcn_s_setprio(1); _Pragma("unroll") for (int m = 0; m < 4; ++m) _Pragma("unroll") for (int n = 0; n < 2; ++n) _Pragma("unroll") for (int k = 0; k < 2; ++k) \
;         acc[ai][bj][m][n] = __builtin_amdgcn_mfma_f32_16x16x32_bf16(Bt[n][k], At[m][k], acc[ai][bj][m][n], 0, 0, 0); __builtin_amdgcn_s_setprio(0); } while (0)
; #define PG8_WAIT_V(n) asm volatile("s_waitcnt vmcnt(" #n ")" ::: "memory")
; #define PG8_WAIT_L(n) asm volatile("s_waitcnt lgkmcnt(" #n ")" ::: "memory")
; #define PG8_BAR __builtin_amdgcn_s_barrier()
; #define PG8_SCHED __builtin_amdgcn_sched_barrier(0)
; template <class Epi, class Sched, bool ALIGN_EPI = false, bool SP2 = false>
; __device__ __forceinline__ void gemm_phase(PG8_LAS unsigned char* lds, const Gemm g, const Sched& S, const Epi& E) {
;     ...
;             PG8_WAIT_V(8); PG8_WAIT_L(0); PG8_BAR; PG8_MMA(1, 0, At, B0); PG8_MMA(1, 1, At, B1); PG8_BAR; PG8_SCHED;
;             PG8_LDB(B0, 1, 0); PG8_LDB(B1, 1, 1); PG8_SCHED; PG8_LDA(At, 1, 0); PG8_STAGE(PG8_SA(0, 1), a2 + hstepA, voffA);
;             PG8_WAIT_V(8); PG8_WAIT_L(0); PG8_BAR; PG8_MMA(0, 0, At, B0); PG8_MMA(0, 1, At, B1); PG8_BAR; PG8_SCHED;
	s_setprio 1
	s_waitcnt lgkmcnt(0)
	v_mfma_f32_16x16x32_bf16 v[64:67], v[148:151], v[180:183], v[64:67]
	v_mfma_f32_16x16x32_bf16 v[60:63], v[156:159], v[180:183], v[60:63]
	v_mfma_f32_16x16x32_bf16 v[48:51], v[148:151], v[188:191], v[48:51]
	v_mfma_f32_16x16x32_bf16 v[44:47], v[156:159], v[188:191], v[44:47]
	v_mfma_f32_16x16x32_bf16 v[32:35], v[148:151], v[210:213], v[32:35]
	v_mfma_f32_16x16x32_bf16 v[28:31], v[156:159], v[210:213], v[28:31]
	v_mfma_f32_16x16x32_bf16 v[16:19], v[148:151], v[230:233], v[16:19]
	v_mfma_f32_16x16x32_bf16 v[12:15], v[156:159], v[230:233], v[12:15]
	v_mfma_f32_16x16x32_bf16 v[64:67], v[152:155], v[184:187], v[64:67]
	v_mfma_f32_16x16x32_bf16 v[60:63], v[160:163], v[184:187], v[60:63]
	v_mfma_f32_16x16x32_bf16 v[48:51], v[152:155], v[192:195], v[48:51]
	v_mfma_f32_16x16x32_bf16 v[44:47], v[160:163], v[192:195], v[44:47]
	v_mfma_f32_16x16x32_bf16 v[32:35], v[152:155], v[226:229], v[32:35]
	v_mfma_f32_16x16x32_bf16 v[28:31], v[160:163], v[226:229], v[28:31]
	v_mfma_f32_16x16x32_bf16 v[16:19], v[152:155], v[234:237], v[16:19]
	v_mfma_f32_16x16x32_bf16 v[12:15], v[160:163], v[234:237], v[12:15]
	s_setprio 0
	s_setprio 1
	v_mfma_f32_16x16x32_bf16 v[56:59], v[164:167], v[180:183], v[56:59]
	v_mfma_f32_16x16x32_bf16 v[52:55], v[172:175], v[180:183], v[52:55]
	v_mfma_f32_16x16x32_bf16 v[40:43], v[164:167], v[188:191], v[40:43]
	v_mfma_f32_16x16x32_bf16 v[36:39], v[172:175], v[188:191], v[36:39]
	v_mfma_f32_16x16x32_bf16 v[24:27], v[164:167], v[210:213], v[24:27]
	v_mfma_f32_16x16x32_bf16 v[20:23], v[172:175], v[210:213], v[20:23]
	v_mfma_f32_16x16x32_bf16 v[8:11], v[164:167], v[230:233], v[8:11]
	v_mfma_f32_16x16x32_bf16 v[4:7], v[172:175], v[230:233], v[4:7]
	v_mfma_f32_16x16x32_bf16 v[56:59], v[168:171], v[184:187], v[56:59]
	v_mfma_f32_16x16x32_bf16 v[52:55], v[176:179], v[184:187], v[52:55]
	v_mfma_f32_16x16x32_bf16 v[40:43], v[168:171], v[192:195], v[40:43]
	v_mfma_f32_16x16x32_bf16 v[36:39], v[176:179], v[192:195], v[36:39]
	v_mfma_f32_16x16x32_bf16 v[24:27], v[168:171], v[226:229], v[24:27]
	v_mfma_f32_16x16x32_bf16 v[20:23], v[176:179], v[226:229], v[20:23]
	v_mfma_f32_16x16x32_bf16 v[8:11], v[168:171], v[234:237], v[8:11]
	v_mfma_f32_16x16x32_bf16 v[4:7], v[176:179], v[234:237], v[4:7]
	s_setprio 0
	s_barrier
	s_add_i32 s50, 0, 0x18000
	s_add_i32 s51, 0, 0x1c000
	v_add_u32_e32 v160, s50, v146
	v_add_u32_e32 v176, s51, v146
	ds_read_b128 v[148:151], v160
	ds_read_b128 v[152:155], v160 offset:1024
	ds_read_b128 v[156:159], v160 offset:2048
	ds_read_b128 v[160:163], v160 offset:3072
	ds_read_b128 v[164:167], v176
	ds_read_b128 v[168:171], v176 offset:1024
	ds_read_b128 v[172:175], v176 offset:2048
	ds_read_b128 v[176:179], v176 offset:3072
	s_add_u32 s20, s20, 0x40000
	s_addc_u32 s21, s21, 0
	s_mov_b32 m0, s30
	v_lshl_add_u64 v[244:245], s[20:21], 0, v[132:133]
	ds_read_b128 v[180:183], v147 offset:32768
	ds_read_b128 v[184:187], v147 offset:33792
	ds_read_b128 v[188:191], v147 offset:34816
	ds_read_b128 v[192:195], v147 offset:35840
	ds_read_b128 v[210:213], v147 offset:36864
	ds_read_b128 v[226:229], v147 offset:37888
	ds_read_b128 v[230:233], v147 offset:38912
	ds_read_b128 v[234:237], v147 offset:39936
	global_load_lds_dwordx4 v[244:245], off
	s_mov_b32 m0, s31
	v_lshl_add_u64 v[244:245], s[20:21], 0, v[136:137]
	global_load_lds_dwordx4 v[244:245], off
	s_waitcnt vmcnt(8)
	s_waitcnt lgkmcnt(0)
	s_barrier
	s_setprio 1
	s_waitcnt lgkmcnt(0)
	v_mfma_f32_16x16x32_bf16 v[124:127], v[148:151], v[180:183], v[124:127]
	v_mfma_f32_16x16x32_bf16 v[128:131], v[156:159], v[180:183], v[128:131]
	v_mfma_f32_16x16x32_bf16 v[112:115], v[148:151], v[188:191], v[112:115]
	v_mfma_f32_16x16x32_bf16 v[108:111], v[156:159], v[188:191], v[108:111]
	v_mfma_f32_16x16x32_bf16 v[96:99], v[148:151], v[210:213], v[96:99]
	v_mfma_f32_16x16x32_bf16 v[92:95], v[156:159], v[210:213], v[92:95]
	v_mfma_f32_16x16x32_bf16 v[80:83], v[148:151], v[230:233], v[80:83]
	v_mfma_f32_16x16x32_bf16 v[76:79], v[156:159], v[230:233], v[76:79]
	v_mfma_f32_16x16x32_bf16 v[124:127], v[152:155], v[184:187], v[124:127]
	v_mfma_f32_16x16x32_bf16 v[128:131], v[160:163], v[184:187], v[128:131]
	v_mfma_f32_16x16x32_bf16 v[112:115], v[152:155], v[192:195], v[112:115]
	v_mfma_f32_16x16x32_bf16 v[108:111], v[160:163], v[192:195], v[108:111]
	v_mfma_f32_16x16x32_bf16 v[96:99], v[152:155], v[226:229], v[96:99]
	v_mfma_f32_16x16x32_bf16 v[92:95], v[160:163], v[226:229], v[92:95]
	v_mfma_f32_16x16x32_bf16 v[80:83], v[152:155], v[234:237], v[80:83]
	v_mfma_f32_16x16x32_bf16 v[76:79], v[160:163], v[234:237], v[76:79]
	s_setprio 0
	s_setprio 1
	v_mfma_f32_16x16x32_bf16 v[120:123], v[164:167], v[180:183], v[120:123]
	v_mfma_f32_16x16x32_bf16 v[116:119], v[172:175], v[180:183], v[116:119]
	v_mfma_f32_16x16x32_bf16 v[104:107], v[164:167], v[188:191], v[104:107]
	v_mfma_f32_16x16x32_bf16 v[100:103], v[172:175], v[188:191], v[100:103]
	v_mfma_f32_16x16x32_bf16 v[88:91], v[164:167], v[210:213], v[88:91]
	v_mfma_f32_16x16x32_bf16 v[84:87], v[172:175], v[210:213], v[84:87]
	v_mfma_f32_16x16x32_bf16 v[72:75], v[164:167], v[230:233], v[72:75]
	v_mfma_f32_16x16x32_bf16 v[68:71], v[172:175], v[230:233], v[68:71]
	v_mfma_f32_16x16x32_bf16 v[120:123], v[168:171], v[184:187], v[120:123]
	v_mfma_f32_16x16x32_bf16 v[116:119], v[176:179], v[184:187], v[116:119]
	v_mfma_f32_16x16x32_bf16 v[104:107], v[168:171], v[192:195], v[104:107]
	v_mfma_f32_16x16x32_bf16 v[100:103], v[176:179], v[192:195], v[100:103]
	v_mfma_f32_16x16x32_bf16 v[88:91], v[168:171], v[226:229], v[88:91]
	v_mfma_f32_16x16x32_bf16 v[84:87], v[176:179], v[226:229], v[84:87]
	v_mfma_f32_16x16x32_bf16 v[72:75], v[168:171], v[234:237], v[72:75]
	v_mfma_f32_16x16x32_bf16 v[68:71], v[176:179], v[234:237], v[68:71]
	s_setprio 0
	s_barrier
; #define PG8_STAGE(bufoff, gbase, voff) do { _Pragma("unroll") for (int _i = 0; _i < 2; ++_i) \
;         __builtin_amdgcn_global_load_lds((const unsigned*)((const char*)(gbase) + (voff)[_i]), (PG8_LAS unsigned*)(lds + (bufoff) + ldsw + _i * 8192), 16, 0, 0); } while (0)
; #define PG8_LDA(dst, b, h) do { _Pragma("unroll") for (int m = 0; m < 4; ++m) _Pragma("unroll") for (int k = 0; k < 2; ++k) dst[m][k] = *(const PG8_LAS bf16x8*)(lds + PG8_SA(b, h) + aoff + m * 2048 + k * 1024); } while (0)
; #define PG8_MMA(ai, bj, At, Bt) do { __builtin_amdgcn_s_setprio(1); _Pragma("unroll") for (int m = 0; m < 4; ++m) _Pragma("unroll") for (int n = 0; n < 2; ++n) _Pragma("unroll") for (int k = 0; k < 2; ++k) \
;         acc[ai][bj][m][n] = __builtin_amdgcn_mfma_f32_16x16x32_bf16(Bt[n][k], At[m][k], acc[ai][bj][m][n], 0, 0, 0); __builtin_amdgcn_s_setprio(0); } while (0)
; #define PG8_WAIT_V(n) asm volatile("s_waitcnt vmcnt(" #n ")" ::: "memory")
; #define PG8_WAIT_L(n) asm volatile("s_waitcnt lgkmcnt(" #n ")" ::: "memory")
; #define PG8_BAR __builtin_amdgcn_s_barrier()
; #define PG8_SCHED __builtin_amdgcn_sched_barrier(0)
; template <class Epi, class Sched, bool ALIGN_EPI = false, bool SP2 = false>
; __device__ __forceinline__ void gemm_phase(PG8_LAS unsigned char* lds, const Gemm g, const Sched& S, const Epi& E) {
;     ...
;             PG8_LDA(At, 1, 1); PG8_STAGE(PG8_SB(1, 0), b3, voffB); PG8_STAGE(PG8_SB(1, 1), b3 + hstepB, voffB); PG8_STAGE(PG8_SA(1, 0), a3, voffA);
;             PG8_WAIT_V(8); PG8_WAIT_L(0); PG8_BAR; PG8_MMA(1, 0, At, B0); PG8_MMA(1, 1, At, B1); PG8_BAR; PG8_SCHED;
	s_add_i32 s20, s50, s26
	v_lshl_add_u64 v[196:197], v[196:197], 0, s[64:65]
	s_mov_b32 m0, s20
	ds_read_b128 v[180:183], v147 offset:49152
	ds_read_b128 v[184:187], v147 offset:50176
	ds_read_b128 v[188:191], v147 offset:51200
	ds_read_b128 v[192:195], v147 offset:52224
	ds_read_b128 v[210:213], v147 offset:53248
	ds_read_b128 v[226:229], v147 offset:54272
	ds_read_b128 v[230:233], v147 offset:55296
	ds_read_b128 v[234:237], v147 offset:56320
	global_load_lds_dwordx4 v[196:197], off
	s_add_i32 m0, s20, 0x2000
	s_add_u32 s18, s18, 0x80080
	v_lshl_add_u64 v[196:197], v[238:239], 0, s[64:65]
	s_addc_u32 s19, s19, 0
	s_add_i32 s20, s51, s26
	global_load_lds_dwordx4 v[196:197], off
	s_mov_b32 m0, s20
	v_lshl_add_u64 v[196:197], s[18:19], 0, v[134:135]
	global_load_lds_dwordx4 v[196:197], off
	s_add_i32 m0, s20, 0x2000
	v_lshl_add_u64 v[196:197], s[18:19], 0, v[138:139]
	global_load_lds_dwordx4 v[196:197], off
	s_mov_b32 m0, s34
	v_lshl_add_u64 v[196:197], v[240:241], 0, s[64:65]
	global_load_lds_dwordx4 v[196:197], off
	s_mov_b32 m0, s35
	v_lshl_add_u64 v[196:197], v[242:243], 0, s[64:65]
	global_load_lds_dwordx4 v[196:197], off
	s_waitcnt vmcnt(8)
	s_waitcnt lgkmcnt(0)
	s_barrier
	s_setprio 1
	s_waitcnt lgkmcnt(0)
	v_mfma_f32_16x16x32_bf16 v[64:67], v[148:151], v[180:183], v[64:67]
	v_mfma_f32_16x16x32_bf16 v[60:63], v[156:159], v[180:183], v[60:63]
	v_mfma_f32_16x16x32_bf16 v[48:51], v[148:151], v[188:191], v[48:51]
	v_mfma_f32_16x16x32_bf16 v[44:47], v[156:159], v[188:191], v[44:47]
	v_mfma_f32_16x16x32_bf16 v[32:35], v[148:151], v[210:213], v[32:35]
	v_mfma_f32_16x16x32_bf16 v[28:31], v[156:159], v[210:213], v[28:31]
	v_mfma_f32_16x16x32_bf16 v[16:19], v[148:151], v[230:233], v[16:19]
	v_mfma_f32_16x16x32_bf16 v[12:15], v[156:159], v[230:233], v[12:15]
	v_mfma_f32_16x16x32_bf16 v[64:67], v[152:155], v[184:187], v[64:67]
	v_mfma_f32_16x16x32_bf16 v[60:63], v[160:163], v[184:187], v[60:63]
	v_mfma_f32_16x16x32_bf16 v[48:51], v[152:155], v[192:195], v[48:51]
	v_mfma_f32_16x16x32_bf16 v[44:47], v[160:163], v[192:195], v[44:47]
	v_mfma_f32_16x16x32_bf16 v[32:35], v[152:155], v[226:229], v[32:35]
	v_mfma_f32_16x16x32_bf16 v[28:31], v[160:163], v[226:229], v[28:31]
	v_mfma_f32_16x16x32_bf16 v[16:19], v[152:155], v[234:237], v[16:19]
	v_mfma_f32_16x16x32_bf16 v[12:15], v[160:163], v[234:237], v[12:15]
	s_setprio 0
	s_setprio 1
	v_mfma_f32_16x16x32_bf16 v[56:59], v[164:167], v[180:183], v[56:59]
	v_mfma_f32_16x16x32_bf16 v[52:55], v[172:175], v[180:183], v[52:55]
	v_mfma_f32_16x16x32_bf16 v[40:43], v[164:167], v[188:191], v[40:43]
	v_mfma_f32_16x16x32_bf16 v[36:39], v[172:175], v[188:191], v[36:39]
	v_mfma_f32_16x16x32_bf16 v[24:27], v[164:167], v[210:213], v[24:27]
	v_mfma_f32_16x16x32_bf16 v[20:23], v[172:175], v[210:213], v[20:23]
	v_mfma_f32_16x16x32_bf16 v[8:11], v[164:167], v[230:233], v[8:11]
	v_mfma_f32_16x16x32_bf16 v[4:7], v[172:175], v[230:233], v[4:7]
	v_mfma_f32_16x16x32_bf16 v[56:59], v[168:171], v[184:187], v[56:59]
	v_mfma_f32_16x16x32_bf16 v[52:55], v[176:179], v[184:187], v[52:55]
	v_mfma_f32_16x16x32_bf16 v[40:43], v[168:171], v[192:195], v[40:43]
	v_mfma_f32_16x16x32_bf16 v[36:39], v[176:179], v[192:195], v[36:39]
	v_mfma_f32_16x16x32_bf16 v[24:27], v[168:171], v[226:229], v[24:27]
	v_mfma_f32_16x16x32_bf16 v[20:23], v[176:179], v[226:229], v[20:23]
	v_mfma_f32_16x16x32_bf16 v[8:11], v[168:171], v[234:237], v[8:11]
	v_mfma_f32_16x16x32_bf16 v[4:7], v[176:179], v[234:237], v[4:7]
	s_setprio 0
	s_barrier
	s_add_u32 s47, s47, 0x100
	s_addc_u32 s48, s48, 0
	s_add_u32 s16, s16, 0x100
	s_addc_u32 s17, s17, 0
	s_cmp_ge_i32 s49, s33
	s_mov_b32 s18, s49
	s_cbranch_scc0 .LBB0_1236

; #define PG8_STAGE(bufoff, gbase, voff) do { _Pragma("unroll") for (int _i = 0; _i < 2; ++_i) \
;         __builtin_amdgcn_global_load_lds((const unsigned*)((const char*)(gbase) + (voff)[_i]), (PG8_LAS unsigned*)(lds + (bufoff) + ldsw + _i * 8192), 16, 0, 0); } while (0)
; #define PG8_LDA(dst, b, h) do { _Pragma("unroll") for (int m = 0; m < 4; ++m) _Pragma("unroll") for (int k = 0; k < 2; ++k) dst[m][k] = *(const PG8_LAS bf16x8*)(lds + PG8_SA(b, h) + aoff + m * 2048 + k * 1024); } while (0)
; #define PG8_LDB(dst, b, h) do { _Pragma("unroll") for (int n = 0; n < 2; ++n) _Pragma("unroll") for (int k = 0; k < 2; ++k) dst[n][k] = *(const PG8_LAS bf16x8*)(lds + PG8_SB(b, h) + boff + n * 2048 + k * 1024); } while (0)
; #define PG8_MMA(ai, bj, At, Bt) do { __builtin_amdgcn_s_setprio(1); _Pragma("unroll") for (int m = 0; m < 4; ++m) _Pragma("unroll") for (int n = 0; n < 2; ++n) _Pragma("unroll") for (int k = 0; k < 2; ++k) \
;         acc[ai][bj][m][n] = __builtin_amdgcn_mfma_f32_16x16x32_bf16(Bt[n][k], At[m][k], acc[ai][bj][m][n], 0, 0, 0); __builtin_amdgcn_s_setprio(0); } while (0)
; #define PG8_WAIT_V(n) asm volatile("s_waitcnt vmcnt(" #n ")" ::: "memory")
; #define PG8_WAIT_L(n) asm volatile("s_waitcnt lgkmcnt(" #n ")" ::: "memory")
; template <class Epi, class Sched, bool ALIGN_EPI = false, bool SP2 = false>
; __device__ __forceinline__ void gemm_phase(PG8_LAS unsigned char* lds, const Gemm g, const Sched& S, const Epi& E) {
;     ...
;             const bool last = (t == nt - 2);
;             const char* a1 = cA + (size_t)(t + 1) * kstep;
;             const char* a2 = last ? nA : cA + (size_t)(t + 2) * kstep; const char* b2 = last ? nB : cB + (size_t)(t + 2) * kstep;
;             const char* a3 = a2 + kstep; const char* b3 = b2 + kstep;
;             if (last && has_next) S.a_ready(nxt);
;             if constexpr (SP2) {
;             PG8_LDB(B0, 0, 0); PG8_LDB(B1, 0, 1); PG8_SCHED; PG8_LDA(At, 0, 0); PG8_STAGE(PG8_SA(1, 1), a1 + hstepA, voffA);
;             PG8_WAIT_V(8); PG8_WAIT_L(0); PG8_BAR; PG8_MMA(0, 0, At, B0); PG8_MMA(0, 1, At, B1); PG8_BAR; PG8_SCHED;
;             PG8_LDA(At, 0, 1); PG8_STAGE(PG8_SB(0, 0), b2, voffB); PG8_STAGE(PG8_SB(0, 1), b2 + hstepB, voffB); PG8_STAGE(PG8_SA(0, 0), a2, voffA);
;             PG8_WAIT_V(8); PG8_WAIT_L(0); PG8_BAR; PG8_MMA(1, 0, At, B0); PG8_MMA(1, 1, At, B1); PG8_BAR; PG8_SCHED;
.LBB0_1247:
	s_add_u32 s10, s23, s8
	s_addc_u32 s11, s30, s9
	s_add_u32 s10, s10, 0xb000100
	s_addc_u32 s11, s11, 0
	s_add_u32 s33, s28, s8
	s_addc_u32 s34, s29, s9
	s_add_i32 s35, 0, 0x10000
	s_cmpk_eq_i32 s8, 0x700
	s_cselect_b32 s13, s7, s11
	s_cselect_b32 s12, s6, s10
	v_add_u32_e32 v147, s35, v145
	s_cselect_b32 s11, s5, s34
	s_cselect_b32 s10, s4, s33
	s_add_i32 s33, 0, 0x14000
	ds_read_b128 v[148:151], v147
	ds_read_b128 v[152:155], v147 offset:1024
	ds_read_b128 v[156:159], v147 offset:2048
	ds_read_b128 v[160:163], v147 offset:3072
	v_add_u32_e32 v147, s33, v145
	ds_read_b128 v[164:167], v147
	ds_read_b128 v[168:171], v147 offset:1024
	ds_read_b128 v[172:175], v147 offset:2048
	ds_read_b128 v[176:179], v147 offset:3072
	v_lshl_add_u64 v[196:197], v[142:143], 0, s[8:9]
	s_add_i32 m0, s19, 0xc000
	ds_read_b128 v[180:183], v146
	ds_read_b128 v[184:187], v146 offset:1024
	ds_read_b128 v[188:191], v146 offset:2048
	ds_read_b128 v[192:195], v146 offset:3072
	ds_read_b128 v[210:213], v146 offset:4096
	ds_read_b128 v[226:229], v146 offset:5120
	ds_read_b128 v[230:233], v146 offset:6144
	ds_read_b128 v[234:237], v146 offset:7168
	global_load_lds_dwordx4 v[196:197], off
	s_add_i32 m0, s19, 0xe000
	v_lshl_add_u64 v[196:197], v[140:141], 0, s[8:9]
	global_load_lds_dwordx4 v[196:197], off
	s_waitcnt vmcnt(8)
	s_waitcnt lgkmcnt(0)
	s_barrier
	s_setprio 1
	s_waitcnt lgkmcnt(0)
	v_mfma_f32_16x16x32_bf16 v[128:131], v[148:151], v[180:183], v[128:131]
	v_mfma_f32_16x16x32_bf16 v[124:127], v[156:159], v[180:183], v[124:127]
	v_mfma_f32_16x16x32_bf16 v[116:119], v[148:151], v[188:191], v[116:119]
	v_mfma_f32_16x16x32_bf16 v[108:111], v[156:159], v[188:191], v[108:111]
	v_mfma_f32_16x16x32_bf16 v[104:107], v[148:151], v[210:213], v[104:107]
	v_mfma_f32_16x16x32_bf16 v[96:99], v[156:159], v[210:213], v[96:99]
	v_mfma_f32_16x16x32_bf16 v[88:91], v[148:151], v[230:233], v[88:91]
	v_mfma_f32_16x16x32_bf16 v[80:83], v[156:159], v[230:233], v[80:83]
	v_mfma_f32_16x16x32_bf16 v[128:131], v[152:155], v[184:187], v[128:131]
	v_mfma_f32_16x16x32_bf16 v[124:127], v[160:163], v[184:187], v[124:127]
	v_mfma_f32_16x16x32_bf16 v[116:119], v[152:155], v[192:195], v[116:119]
	v_mfma_f32_16x16x32_bf16 v[108:111], v[160:163], v[192:195], v[108:111]
	v_mfma_f32_16x16x32_bf16 v[104:107], v[152:155], v[226:229], v[104:107]
	v_mfma_f32_16x16x32_bf16 v[96:99], v[160:163], v[226:229], v[96:99]
	v_mfma_f32_16x16x32_bf16 v[88:91], v[152:155], v[234:237], v[88:91]
	v_mfma_f32_16x16x32_bf16 v[80:83], v[160:163], v[234:237], v[80:83]
	s_setprio 0
	s_setprio 1
	v_mfma_f32_16x16x32_bf16 v[120:123], v[164:167], v[180:183], v[120:123]
	v_mfma_f32_16x16x32_bf16 v[112:115], v[172:175], v[180:183], v[112:115]
	v_mfma_f32_16x16x32_bf16 v[100:103], v[164:167], v[188:191], v[100:103]
	v_mfma_f32_16x16x32_bf16 v[92:95], v[172:175], v[188:191], v[92:95]
	v_mfma_f32_16x16x32_bf16 v[84:87], v[164:167], v[210:213], v[84:87]
	v_mfma_f32_16x16x32_bf16 v[76:79], v[172:175], v[210:213], v[76:79]
	v_mfma_f32_16x16x32_bf16 v[72:75], v[164:167], v[230:233], v[72:75]
	v_mfma_f32_16x16x32_bf16 v[68:71], v[172:175], v[230:233], v[68:71]
	v_mfma_f32_16x16x32_bf16 v[120:123], v[168:171], v[184:187], v[120:123]
	v_mfma_f32_16x16x32_bf16 v[112:115], v[176:179], v[184:187], v[112:115]
	v_mfma_f32_16x16x32_bf16 v[100:103], v[168:171], v[192:195], v[100:103]
	v_mfma_f32_16x16x32_bf16 v[92:95], v[176:179], v[192:195], v[92:95]
	v_mfma_f32_16x16x32_bf16 v[84:87], v[168:171], v[226:229], v[84:87]
	v_mfma_f32_16x16x32_bf16 v[76:79], v[176:179], v[226:229], v[76:79]
	v_mfma_f32_16x16x32_bf16 v[72:75], v[168:171], v[234:237], v[72:75]
	v_mfma_f32_16x16x32_bf16 v[68:71], v[176:179], v[234:237], v[68:71]
	s_setprio 0
	s_barrier
	s_add_i32 s34, s35, s18
	v_lshl_add_u64 v[196:197], s[10:11], 0, v[134:135]
	s_mov_b32 m0, s34
	ds_read_b128 v[180:183], v146 offset:16384
	ds_read_b128 v[184:187], v146 offset:17408
	ds_read_b128 v[188:191], v146 offset:18432
	ds_read_b128 v[192:195], v146 offset:19456
	ds_read_b128 v[210:213], v146 offset:20480
	ds_read_b128 v[226:229], v146 offset:21504
	ds_read_b128 v[230:233], v146 offset:22528
	ds_read_b128 v[234:237], v146 offset:23552
	global_load_lds_dwordx4 v[196:197], off
	s_add_i32 m0, s34, 0x2000
	s_add_u32 s34, s10, 0x40000
	v_lshl_add_u64 v[238:239], s[10:11], 0, v[138:139]
	s_addc_u32 s35, s11, 0
	s_add_i32 s33, s33, s18
	global_load_lds_dwordx4 v[238:239], off
	v_lshl_add_u64 v[240:241], s[34:35], 0, v[134:135]
	s_mov_b32 m0, s33
	v_lshl_add_u64 v[242:243], s[12:13], 0, v[136:137]
	global_load_lds_dwordx4 v[240:241], off
	s_add_i32 m0, s33, 0x2000
	v_lshl_add_u64 v[240:241], s[34:35], 0, v[138:139]
	global_load_lds_dwordx4 v[240:241], off
	s_mov_b32 m0, s19
	v_lshl_add_u64 v[240:241], s[12:13], 0, v[132:133]
	global_load_lds_dwordx4 v[240:241], off
	s_mov_b32 m0, s20
	s_nop 0
	global_load_lds_dwordx4 v[242:243], off
	s_waitcnt vmcnt(8)
	s_waitcnt lgkmcnt(0)
	s_barrier
; #define PG8_STAGE(bufoff, gbase, voff) do { _Pragma("unroll") for (int _i = 0; _i < 2; ++_i) \
;         __builtin_amdgcn_global_load_lds((const unsigned*)((const char*)(gbase) + (voff)[_i]), (PG8_LAS unsigned*)(lds + (bufoff) + ldsw + _i * 8192), 16, 0, 0); } while (0)
; #define PG8_LDA(dst, b, h) do { _Pragma("unroll") for (int m = 0; m < 4; ++m) _Pragma("unroll") for (int k = 0; k < 2; ++k) dst[m][k] = *(const PG8_LAS bf16x8*)(lds + PG8_SA(b, h) + aoff + m * 2048 + k * 1024); } while (0)
; #define PG8_LDB(dst, b, h) do { _Pragma("unroll") for (int n = 0; n < 2; ++n) _Pragma("unroll") for (int k = 0; k < 2; ++k) dst[n][k] = *(const PG8_LAS bf16x8*)(lds + PG8_SB(b, h) + boff + n * 2048 + k * 1024); } while (0)
; #define PG8_MMA(ai, bj, At, Bt) do { __builtin_amdgcn_s_setprio(1); _Pragma("unroll") for (int m = 0; m < 4; ++m) _Pragma("unroll") for (int n = 0; n < 2; ++n) _Pragma("unroll") for (int k = 0; k < 2; ++k) \
;         acc[ai][bj][m][n] = __builtin_amdgcn_mfma_f32_16x16x32_bf16(Bt[n][k], At[m][k], acc[ai][bj][m][n], 0, 0, 0); __builtin_amdgcn_s_setprio(0); } while (0)
; #define PG8_WAIT_V(n) asm volatile("s_waitcnt vmcnt(" #n ")" ::: "memory")
; #define PG8_WAIT_L(n) asm volatile("s_waitcnt lgkmcnt(" #n ")" ::: "memory")
; #define PG8_BAR __builtin_amdgcn_s_barrier()
; #define PG8_SCHED __builtin_amdgcn_sched_barrier(0)
; template <class Epi, class Sched, bool ALIGN_EPI = false, bool SP2 = false>
; __device__ __forceinline__ void gemm_phase(PG8_LAS unsigned char* lds, const Gemm g, const Sched& S, const Epi& E) {
;     ...
;             PG8_WAIT_V(8); PG8_WAIT_L(0); PG8_BAR; PG8_MMA(1, 0, At, B0); PG8_MMA(1, 1, At, B1); PG8_BAR; PG8_SCHED;
;             PG8_LDB(B0, 1, 0); PG8_LDB(B1, 1, 1); PG8_SCHED; PG8_LDA(At, 1, 0); PG8_STAGE(PG8_SA(0, 1), a2 + hstepA, voffA);
;             PG8_WAIT_V(8); PG8_WAIT_L(0); PG8_BAR; PG8_MMA(0, 0, At, B0); PG8_MMA(0, 1, At, B1); PG8_BAR; PG8_SCHED;
	s_setprio 1
	s_waitcnt lgkmcnt(0)
	v_mfma_f32_16x16x32_bf16 v[64:67], v[148:151], v[180:183], v[64:67]
	v_mfma_f32_16x16x32_bf16 v[60:63], v[156:159], v[180:183], v[60:63]
	v_mfma_f32_16x16x32_bf16 v[52:55], v[148:151], v[188:191], v[52:55]
	v_mfma_f32_16x16x32_bf16 v[44:47], v[156:159], v[188:191], v[44:47]
	v_mfma_f32_16x16x32_bf16 v[40:43], v[148:151], v[210:213], v[40:43]
	v_mfma_f32_16x16x32_bf16 v[32:35], v[156:159], v[210:213], v[32:35]
	v_mfma_f32_16x16x32_bf16 v[24:27], v[148:151], v[230:233], v[24:27]
	v_mfma_f32_16x16x32_bf16 v[16:19], v[156:159], v[230:233], v[16:19]
	v_mfma_f32_16x16x32_bf16 v[64:67], v[152:155], v[184:187], v[64:67]
	v_mfma_f32_16x16x32_bf16 v[60:63], v[160:163], v[184:187], v[60:63]
	v_mfma_f32_16x16x32_bf16 v[52:55], v[152:155], v[192:195], v[52:55]
	v_mfma_f32_16x16x32_bf16 v[44:47], v[160:163], v[192:195], v[44:47]
	v_mfma_f32_16x16x32_bf16 v[40:43], v[152:155], v[226:229], v[40:43]
	v_mfma_f32_16x16x32_bf16 v[32:35], v[160:163], v[226:229], v[32:35]
	v_mfma_f32_16x16x32_bf16 v[24:27], v[152:155], v[234:237], v[24:27]
	v_mfma_f32_16x16x32_bf16 v[16:19], v[160:163], v[234:237], v[16:19]
	s_setprio 0
	s_setprio 1
	v_mfma_f32_16x16x32_bf16 v[56:59], v[164:167], v[180:183], v[56:59]
	v_mfma_f32_16x16x32_bf16 v[48:51], v[172:175], v[180:183], v[48:51]
	v_mfma_f32_16x16x32_bf16 v[36:39], v[164:167], v[188:191], v[36:39]
	v_mfma_f32_16x16x32_bf16 v[28:31], v[172:175], v[188:191], v[28:31]
	v_mfma_f32_16x16x32_bf16 v[20:23], v[164:167], v[210:213], v[20:23]
	v_mfma_f32_16x16x32_bf16 v[12:15], v[172:175], v[210:213], v[12:15]
	v_mfma_f32_16x16x32_bf16 v[8:11], v[164:167], v[230:233], v[8:11]
	v_mfma_f32_16x16x32_bf16 v[4:7], v[172:175], v[230:233], v[4:7]
	v_mfma_f32_16x16x32_bf16 v[56:59], v[168:171], v[184:187], v[56:59]
	v_mfma_f32_16x16x32_bf16 v[48:51], v[176:179], v[184:187], v[48:51]
	v_mfma_f32_16x16x32_bf16 v[36:39], v[168:171], v[192:195], v[36:39]
	v_mfma_f32_16x16x32_bf16 v[28:31], v[176:179], v[192:195], v[28:31]
	v_mfma_f32_16x16x32_bf16 v[20:23], v[168:171], v[226:229], v[20:23]
	v_mfma_f32_16x16x32_bf16 v[12:15], v[176:179], v[226:229], v[12:15]
	v_mfma_f32_16x16x32_bf16 v[8:11], v[168:171], v[234:237], v[8:11]
	v_mfma_f32_16x16x32_bf16 v[4:7], v[176:179], v[234:237], v[4:7]
	s_setprio 0
	s_barrier
	s_add_i32 s33, 0, 0x18000
	v_add_u32_e32 v147, s33, v145
	s_add_i32 s34, 0, 0x1c000
	ds_read_b128 v[148:151], v147
	ds_read_b128 v[152:155], v147 offset:1024
	ds_read_b128 v[156:159], v147 offset:2048
	ds_read_b128 v[160:163], v147 offset:3072
	v_add_u32_e32 v147, s34, v145
	ds_read_b128 v[164:167], v147
	ds_read_b128 v[168:171], v147 offset:1024
	ds_read_b128 v[172:175], v147 offset:2048
	ds_read_b128 v[176:179], v147 offset:3072
	s_add_u32 s12, s12, 0x40000
	s_addc_u32 s13, s13, 0
	s_mov_b32 m0, s21
	v_lshl_add_u64 v[244:245], s[12:13], 0, v[132:133]
	ds_read_b128 v[180:183], v146 offset:32768
	ds_read_b128 v[184:187], v146 offset:33792
	ds_read_b128 v[188:191], v146 offset:34816
	ds_read_b128 v[192:195], v146 offset:35840
	ds_read_b128 v[210:213], v146 offset:36864
	ds_read_b128 v[226:229], v146 offset:37888
	ds_read_b128 v[230:233], v146 offset:38912
	ds_read_b128 v[234:237], v146 offset:39936
	global_load_lds_dwordx4 v[244:245], off
	s_mov_b32 m0, s24
	v_lshl_add_u64 v[244:245], s[12:13], 0, v[136:137]
	global_load_lds_dwordx4 v[244:245], off
	s_waitcnt vmcnt(8)
	s_waitcnt lgkmcnt(0)
	s_barrier
	s_setprio 1
	s_waitcnt lgkmcnt(0)
	v_mfma_f32_16x16x32_bf16 v[128:131], v[148:151], v[180:183], v[128:131]
	v_mfma_f32_16x16x32_bf16 v[124:127], v[156:159], v[180:183], v[124:127]
	v_mfma_f32_16x16x32_bf16 v[116:119], v[148:151], v[188:191], v[116:119]
	v_mfma_f32_16x16x32_bf16 v[108:111], v[156:159], v[188:191], v[108:111]
	v_mfma_f32_16x16x32_bf16 v[104:107], v[148:151], v[210:213], v[104:107]
	v_mfma_f32_16x16x32_bf16 v[96:99], v[156:159], v[210:213], v[96:99]
	v_mfma_f32_16x16x32_bf16 v[88:91], v[148:151], v[230:233], v[88:91]
	v_mfma_f32_16x16x32_bf16 v[80:83], v[156:159], v[230:233], v[80:83]
	v_mfma_f32_16x16x32_bf16 v[128:131], v[152:155], v[184:187], v[128:131]
	v_mfma_f32_16x16x32_bf16 v[124:127], v[160:163], v[184:187], v[124:127]
	v_mfma_f32_16x16x32_bf16 v[116:119], v[152:155], v[192:195], v[116:119]
	v_mfma_f32_16x16x32_bf16 v[108:111], v[160:163], v[192:195], v[108:111]
	v_mfma_f32_16x16x32_bf16 v[104:107], v[152:155], v[226:229], v[104:107]
	v_mfma_f32_16x16x32_bf16 v[96:99], v[160:163], v[226:229], v[96:99]
	v_mfma_f32_16x16x32_bf16 v[88:91], v[152:155], v[234:237], v[88:91]
	v_mfma_f32_16x16x32_bf16 v[80:83], v[160:163], v[234:237], v[80:83]
	s_setprio 0
	s_setprio 1
	v_mfma_f32_16x16x32_bf16 v[120:123], v[164:167], v[180:183], v[120:123]
	v_mfma_f32_16x16x32_bf16 v[112:115], v[172:175], v[180:183], v[112:115]
	v_mfma_f32_16x16x32_bf16 v[100:103], v[164:167], v[188:191], v[100:103]
	v_mfma_f32_16x16x32_bf16 v[92:95], v[172:175], v[188:191], v[92:95]
	v_mfma_f32_16x16x32_bf16 v[84:87], v[164:167], v[210:213], v[84:87]
	v_mfma_f32_16x16x32_bf16 v[76:79], v[172:175], v[210:213], v[76:79]
	v_mfma_f32_16x16x32_bf16 v[72:75], v[164:167], v[230:233], v[72:75]
	v_mfma_f32_16x16x32_bf16 v[68:71], v[172:175], v[230:233], v[68:71]
	v_mfma_f32_16x16x32_bf16 v[120:123], v[168:171], v[184:187], v[120:123]
	v_mfma_f32_16x16x32_bf16 v[112:115], v[176:179], v[184:187], v[112:115]
	v_mfma_f32_16x16x32_bf16 v[100:103], v[168:171], v[192:195], v[100:103]
	v_mfma_f32_16x16x32_bf16 v[92:95], v[176:179], v[192:195], v[92:95]
	v_mfma_f32_16x16x32_bf16 v[84:87], v[168:171], v[226:229], v[84:87]
	v_mfma_f32_16x16x32_bf16 v[76:79], v[176:179], v[226:229], v[76:79]
	v_mfma_f32_16x16x32_bf16 v[72:75], v[168:171], v[234:237], v[72:75]
	v_mfma_f32_16x16x32_bf16 v[68:71], v[176:179], v[234:237], v[68:71]
	s_setprio 0
	s_barrier
; #define PG8_STAGE(bufoff, gbase, voff) do { _Pragma("unroll") for (int _i = 0; _i < 2; ++_i) \
;         __builtin_amdgcn_global_load_lds((const unsigned*)((const char*)(gbase) + (voff)[_i]), (PG8_LAS unsigned*)(lds + (bufoff) + ldsw + _i * 8192), 16, 0, 0); } while (0)
; #define PG8_LDA(dst, b, h) do { _Pragma("unroll") for (int m = 0; m < 4; ++m) _Pragma("unroll") for (int k = 0; k < 2; ++k) dst[m][k] = *(const PG8_LAS bf16x8*)(lds + PG8_SA(b, h) + aoff + m * 2048 + k * 1024); } while (0)
; #define PG8_MMA(ai, bj, At, Bt) do { __builtin_amdgcn_s_setprio(1); _Pragma("unroll") for (int m = 0; m < 4; ++m) _Pragma("unroll") for (int n = 0; n < 2; ++n) _Pragma("unroll") for (int k = 0; k < 2; ++k) \
;         acc[ai][bj][m][n] = __builtin_amdgcn_mfma_f32_16x16x32_bf16(Bt[n][k], At[m][k], acc[ai][bj][m][n], 0, 0, 0); __builtin_amdgcn_s_setprio(0); } while (0)
; #define PG8_WAIT_V(n) asm volatile("s_waitcnt vmcnt(" #n ")" ::: "memory")
; #define PG8_WAIT_L(n) asm volatile("s_waitcnt lgkmcnt(" #n ")" ::: "memory")
; #define PG8_BAR __builtin_amdgcn_s_barrier()
; #define PG8_SCHED __builtin_amdgcn_sched_barrier(0)
; template <class Epi, class Sched, bool ALIGN_EPI = false, bool SP2 = false>
; __device__ __forceinline__ void gemm_phase(PG8_LAS unsigned char* lds, const Gemm g, const Sched& S, const Epi& E) {
;     ...
;             PG8_WAIT_V(8); PG8_WAIT_L(0); PG8_BAR; PG8_MMA(0, 0, At, B0); PG8_MMA(0, 1, At, B1); PG8_BAR; PG8_SCHED;
;             PG8_LDA(At, 1, 1); PG8_STAGE(PG8_SB(1, 0), b3, voffB); PG8_STAGE(PG8_SB(1, 1), b3 + hstepB, voffB); PG8_STAGE(PG8_SA(1, 0), a3, voffA);
;             PG8_WAIT_V(8); PG8_WAIT_L(0); PG8_BAR; PG8_MMA(1, 0, At, B0); PG8_MMA(1, 1, At, B1); PG8_BAR; PG8_SCHED;
;     ...
;         if constexpr (ALIGN_EPI) { if (wr == 0) PG8_BAR; }
	s_add_i32 s12, s33, s18
	v_lshl_add_u64 v[196:197], v[196:197], 0, s[64:65]
	s_mov_b32 m0, s12
	ds_read_b128 v[180:183], v146 offset:49152
	ds_read_b128 v[184:187], v146 offset:50176
	ds_read_b128 v[188:191], v146 offset:51200
	ds_read_b128 v[192:195], v146 offset:52224
	ds_read_b128 v[210:213], v146 offset:53248
	ds_read_b128 v[226:229], v146 offset:54272
	ds_read_b128 v[230:233], v146 offset:55296
	ds_read_b128 v[234:237], v146 offset:56320
	global_load_lds_dwordx4 v[196:197], off
	s_add_i32 m0, s12, 0x2000
	s_add_u32 s10, s10, 0x40080
	v_lshl_add_u64 v[196:197], v[238:239], 0, s[64:65]
	s_addc_u32 s11, s11, 0
	s_add_i32 s12, s34, s18
	global_load_lds_dwordx4 v[196:197], off
	s_mov_b32 m0, s12
	v_lshl_add_u64 v[196:197], s[10:11], 0, v[134:135]
	global_load_lds_dwordx4 v[196:197], off
	s_add_i32 m0, s12, 0x2000
	v_lshl_add_u64 v[196:197], s[10:11], 0, v[138:139]
	global_load_lds_dwordx4 v[196:197], off
	s_mov_b32 m0, s26
	v_lshl_add_u64 v[196:197], v[240:241], 0, s[64:65]
	global_load_lds_dwordx4 v[196:197], off
	s_mov_b32 m0, s27
	v_lshl_add_u64 v[196:197], v[242:243], 0, s[64:65]
	global_load_lds_dwordx4 v[196:197], off
	s_waitcnt vmcnt(8)
	s_waitcnt lgkmcnt(0)
	s_barrier
	s_setprio 1
	s_waitcnt lgkmcnt(0)
	v_mfma_f32_16x16x32_bf16 v[64:67], v[148:151], v[180:183], v[64:67]
	v_mfma_f32_16x16x32_bf16 v[60:63], v[156:159], v[180:183], v[60:63]
	v_mfma_f32_16x16x32_bf16 v[52:55], v[148:151], v[188:191], v[52:55]
	v_mfma_f32_16x16x32_bf16 v[44:47], v[156:159], v[188:191], v[44:47]
	v_mfma_f32_16x16x32_bf16 v[40:43], v[148:151], v[210:213], v[40:43]
	v_mfma_f32_16x16x32_bf16 v[32:35], v[156:159], v[210:213], v[32:35]
	v_mfma_f32_16x16x32_bf16 v[24:27], v[148:151], v[230:233], v[24:27]
	v_mfma_f32_16x16x32_bf16 v[16:19], v[156:159], v[230:233], v[16:19]
	v_mfma_f32_16x16x32_bf16 v[64:67], v[152:155], v[184:187], v[64:67]
	v_mfma_f32_16x16x32_bf16 v[60:63], v[160:163], v[184:187], v[60:63]
	v_mfma_f32_16x16x32_bf16 v[52:55], v[152:155], v[192:195], v[52:55]
	v_mfma_f32_16x16x32_bf16 v[44:47], v[160:163], v[192:195], v[44:47]
	v_mfma_f32_16x16x32_bf16 v[40:43], v[152:155], v[226:229], v[40:43]
	v_mfma_f32_16x16x32_bf16 v[32:35], v[160:163], v[226:229], v[32:35]
	v_mfma_f32_16x16x32_bf16 v[24:27], v[152:155], v[234:237], v[24:27]
	v_mfma_f32_16x16x32_bf16 v[16:19], v[160:163], v[234:237], v[16:19]
	s_setprio 0
	s_setprio 1
	v_mfma_f32_16x16x32_bf16 v[56:59], v[164:167], v[180:183], v[56:59]
	v_mfma_f32_16x16x32_bf16 v[48:51], v[172:175], v[180:183], v[48:51]
	v_mfma_f32_16x16x32_bf16 v[36:39], v[164:167], v[188:191], v[36:39]
	v_mfma_f32_16x16x32_bf16 v[28:31], v[172:175], v[188:191], v[28:31]
	v_mfma_f32_16x16x32_bf16 v[20:23], v[164:167], v[210:213], v[20:23]
	v_mfma_f32_16x16x32_bf16 v[12:15], v[172:175], v[210:213], v[12:15]
	v_mfma_f32_16x16x32_bf16 v[8:11], v[164:167], v[230:233], v[8:11]
	v_mfma_f32_16x16x32_bf16 v[4:7], v[172:175], v[230:233], v[4:7]
	v_mfma_f32_16x16x32_bf16 v[56:59], v[168:171], v[184:187], v[56:59]
	v_mfma_f32_16x16x32_bf16 v[48:51], v[176:179], v[184:187], v[48:51]
	v_mfma_f32_16x16x32_bf16 v[36:39], v[168:171], v[192:195], v[36:39]
	v_mfma_f32_16x16x32_bf16 v[28:31], v[176:179], v[192:195], v[28:31]
	v_mfma_f32_16x16x32_bf16 v[20:23], v[168:171], v[226:229], v[20:23]
	v_mfma_f32_16x16x32_bf16 v[12:15], v[176:179], v[226:229], v[12:15]
	v_mfma_f32_16x16x32_bf16 v[8:11], v[168:171], v[234:237], v[8:11]
	v_mfma_f32_16x16x32_bf16 v[4:7], v[176:179], v[234:237], v[4:7]
	s_setprio 0
	s_barrier
	s_add_i32 s31, s31, 2
	s_add_u32 s8, s8, 0x100
	s_addc_u32 s9, s9, 0
	s_cmp_gt_u32 s31, 13
	s_cbranch_scc0 .LBB0_1247
	s_cmpk_lt_u32 s16, 0x100
	s_cbranch_scc0 .LBB0_1250
	s_barrier

; #define PG8_STAGE(bufoff, gbase, voff) do { _Pragma("unroll") for (int _i = 0; _i < 2; ++_i) \
;         __builtin_amdgcn_global_load_lds((const unsigned*)((const char*)(gbase) + (voff)[_i]), (PG8_LAS unsigned*)(lds + (bufoff) + ldsw + _i * 8192), 16, 0, 0); } while (0)
; #define PG8_LDA(dst, b, h) do { _Pragma("unroll") for (int m = 0; m < 4; ++m) _Pragma("unroll") for (int k = 0; k < 2; ++k) dst[m][k] = *(const PG8_LAS bf16x8*)(lds + PG8_SA(b, h) + aoff + m * 2048 + k * 1024); } while (0)
; #define PG8_LDB(dst, b, h) do { _Pragma("unroll") for (int n = 0; n < 2; ++n) _Pragma("unroll") for (int k = 0; k < 2; ++k) dst[n][k] = *(const PG8_LAS bf16x8*)(lds + PG8_SB(b, h) + boff + n * 2048 + k * 1024); } while (0)
; #define PG8_MMA(ai, bj, At, Bt) do { __builtin_amdgcn_s_setprio(1); _Pragma("unroll") for (int m = 0; m < 4; ++m) _Pragma("unroll") for (int n = 0; n < 2; ++n) _Pragma("unroll") for (int k = 0; k < 2; ++k) \
;         acc[ai][bj][m][n] = __builtin_amdgcn_mfma_f32_16x16x32_bf16(Bt[n][k], At[m][k], acc[ai][bj][m][n], 0, 0, 0); __builtin_amdgcn_s_setprio(0); } while (0)
; #define PG8_WAIT_V(n) asm volatile("s_waitcnt vmcnt(" #n ")" ::: "memory")
; #define PG8_WAIT_L(n) asm volatile("s_waitcnt lgkmcnt(" #n ")" ::: "memory")
; template <class Epi, class Sched, bool ALIGN_EPI = false, bool SP2 = false>
; __device__ __forceinline__ void gemm_phase(PG8_LAS unsigned char* lds, const Gemm g, const Sched& S, const Epi& E) {
;     ...
;             const bool last = (t == nt - 2);
;             const char* a1 = cA + (size_t)(t + 1) * kstep;
;             const char* a2 = last ? nA : cA + (size_t)(t + 2) * kstep; const char* b2 = last ? nB : cB + (size_t)(t + 2) * kstep;
;             const char* a3 = a2 + kstep; const char* b3 = b2 + kstep;
;             if (last && has_next) S.a_ready(nxt);
;             if constexpr (SP2) {
;             PG8_LDB(B0, 0, 0); PG8_LDB(B1, 0, 1); PG8_SCHED; PG8_LDA(At, 0, 0); PG8_STAGE(PG8_SA(1, 1), a1 + hstepA, voffA);
;             PG8_WAIT_V(8); PG8_WAIT_L(0); PG8_BAR; PG8_MMA(0, 0, At, B0); PG8_MMA(0, 1, At, B1); PG8_BAR; PG8_SCHED;
;             PG8_LDA(At, 0, 1); PG8_STAGE(PG8_SB(0, 0), b2, voffB); PG8_STAGE(PG8_SB(0, 1), b2 + hstepB, voffB); PG8_STAGE(PG8_SA(0, 0), a2, voffA);
;             PG8_WAIT_V(8); PG8_WAIT_L(0); PG8_BAR; PG8_MMA(1, 0, At, B0); PG8_MMA(1, 1, At, B1); PG8_BAR; PG8_SCHED;
.LBB0_1693:
	s_add_u32 s22, s20, 0xfffc0080
	s_addc_u32 s23, s21, -1
	s_add_i32 s46, 0, 0x10000
	s_cmp_eq_u32 s45, 12
	s_cselect_b32 s25, s13, s23
	s_cselect_b32 s24, s41, s22
	v_add_u32_e32 v144, s46, v146
	s_cselect_b32 s23, s11, s44
	s_cselect_b32 s22, s42, s43
	s_add_i32 s48, 0, 0x14000
	ds_read_b128 v[150:153], v144
	ds_read_b128 v[154:157], v144 offset:1024
	ds_read_b128 v[158:161], v144 offset:2048
	ds_read_b128 v[162:165], v144 offset:3072
	v_add_u32_e32 v144, s48, v146
	ds_read_b128 v[166:169], v144
	ds_read_b128 v[170:173], v144 offset:1024
	ds_read_b128 v[174:177], v144 offset:2048
	ds_read_b128 v[178:181], v144 offset:3072
	v_lshl_add_u64 v[144:145], s[20:21], 0, v[142:143]
	s_add_i32 m0, s15, 0xc000
	ds_read_b128 v[182:185], v148
	ds_read_b128 v[186:189], v148 offset:1024
	ds_read_b128 v[190:193], v148 offset:2048
	ds_read_b128 v[194:197], v148 offset:3072
	ds_read_b128 v[210:213], v148 offset:4096
	ds_read_b128 v[226:229], v148 offset:5120
	ds_read_b128 v[230:233], v148 offset:6144
	ds_read_b128 v[234:237], v148 offset:7168
	s_mov_b32 m0, s36
	v_lshl_add_u64 v[244:245], v[240:241], 0, s[64:65]
	global_load_lds_dwordx4 v[244:245], off
	s_mov_b32 m0, s37
	v_lshl_add_u64 v[244:245], v[242:243], 0, s[64:65]
	global_load_lds_dwordx4 v[244:245], off
	s_add_i32 m0, s15, 0xc000
	s_nop 0
	global_load_lds_dwordx4 v[144:145], off
	s_add_i32 m0, s15, 0xe000
	v_lshl_add_u64 v[144:145], s[20:21], 0, v[140:141]
	global_load_lds_dwordx4 v[144:145], off
	s_waitcnt vmcnt(8)
	s_waitcnt lgkmcnt(0)
	s_barrier
	s_setprio 1
	s_waitcnt lgkmcnt(0)
	v_mfma_f32_16x16x32_bf16 v[128:131], v[150:153], v[182:185], v[128:131]
	v_mfma_f32_16x16x32_bf16 v[124:127], v[158:161], v[182:185], v[124:127]
	v_mfma_f32_16x16x32_bf16 v[120:123], v[150:153], v[190:193], v[120:123]
	v_mfma_f32_16x16x32_bf16 v[112:115], v[158:161], v[190:193], v[112:115]
	v_mfma_f32_16x16x32_bf16 v[104:107], v[150:153], v[210:213], v[104:107]
	v_mfma_f32_16x16x32_bf16 v[96:99], v[158:161], v[210:213], v[96:99]
	v_mfma_f32_16x16x32_bf16 v[88:91], v[150:153], v[230:233], v[88:91]
	v_mfma_f32_16x16x32_bf16 v[80:83], v[158:161], v[230:233], v[80:83]
	v_mfma_f32_16x16x32_bf16 v[128:131], v[154:157], v[186:189], v[128:131]
	v_mfma_f32_16x16x32_bf16 v[124:127], v[162:165], v[186:189], v[124:127]
	v_mfma_f32_16x16x32_bf16 v[120:123], v[154:157], v[194:197], v[120:123]
	v_mfma_f32_16x16x32_bf16 v[112:115], v[162:165], v[194:197], v[112:115]
	v_mfma_f32_16x16x32_bf16 v[104:107], v[154:157], v[226:229], v[104:107]
	v_mfma_f32_16x16x32_bf16 v[96:99], v[162:165], v[226:229], v[96:99]
	v_mfma_f32_16x16x32_bf16 v[88:91], v[154:157], v[234:237], v[88:91]
	v_mfma_f32_16x16x32_bf16 v[80:83], v[162:165], v[234:237], v[80:83]
	s_setprio 0
	s_setprio 1
	v_mfma_f32_16x16x32_bf16 v[116:119], v[166:169], v[182:185], v[116:119]
	v_mfma_f32_16x16x32_bf16 v[108:111], v[174:177], v[182:185], v[108:111]
	v_mfma_f32_16x16x32_bf16 v[100:103], v[166:169], v[190:193], v[100:103]
	v_mfma_f32_16x16x32_bf16 v[92:95], v[174:177], v[190:193], v[92:95]
	v_mfma_f32_16x16x32_bf16 v[84:87], v[166:169], v[210:213], v[84:87]
	v_mfma_f32_16x16x32_bf16 v[76:79], v[174:177], v[210:213], v[76:79]
	v_mfma_f32_16x16x32_bf16 v[72:75], v[166:169], v[230:233], v[72:75]
	v_mfma_f32_16x16x32_bf16 v[68:71], v[174:177], v[230:233], v[68:71]
	v_mfma_f32_16x16x32_bf16 v[116:119], v[170:173], v[186:189], v[116:119]
	v_mfma_f32_16x16x32_bf16 v[108:111], v[178:181], v[186:189], v[108:111]
	v_mfma_f32_16x16x32_bf16 v[100:103], v[170:173], v[194:197], v[100:103]
	v_mfma_f32_16x16x32_bf16 v[92:95], v[178:181], v[194:197], v[92:95]
	v_mfma_f32_16x16x32_bf16 v[84:87], v[170:173], v[226:229], v[84:87]
	v_mfma_f32_16x16x32_bf16 v[76:79], v[178:181], v[226:229], v[76:79]
	v_mfma_f32_16x16x32_bf16 v[72:75], v[170:173], v[234:237], v[72:75]
	v_mfma_f32_16x16x32_bf16 v[68:71], v[178:181], v[234:237], v[68:71]
	s_setprio 0
	s_barrier
	s_add_i32 s46, s46, s31
	v_lshl_add_u64 v[144:145], s[22:23], 0, v[134:135]
	s_mov_b32 m0, s46
	ds_read_b128 v[182:185], v148 offset:16384
	ds_read_b128 v[186:189], v148 offset:17408
	ds_read_b128 v[190:193], v148 offset:18432
	ds_read_b128 v[194:197], v148 offset:19456
	ds_read_b128 v[210:213], v148 offset:20480
	ds_read_b128 v[226:229], v148 offset:21504
	ds_read_b128 v[230:233], v148 offset:22528
	ds_read_b128 v[234:237], v148 offset:23552
	global_load_lds_dwordx4 v[144:145], off
	s_add_i32 m0, s46, 0x2000
	s_add_u32 s46, s22, 0x40000
	v_lshl_add_u64 v[238:239], s[22:23], 0, v[138:139]
	s_addc_u32 s47, s23, 0
	s_add_i32 s48, s48, s31
	global_load_lds_dwordx4 v[238:239], off
	v_lshl_add_u64 v[240:241], s[46:47], 0, v[134:135]
	s_mov_b32 m0, s48
	v_lshl_add_u64 v[242:243], s[24:25], 0, v[136:137]
	global_load_lds_dwordx4 v[240:241], off
	s_add_i32 m0, s48, 0x2000
	v_lshl_add_u64 v[240:241], s[46:47], 0, v[138:139]
	global_load_lds_dwordx4 v[240:241], off
	v_lshl_add_u64 v[240:241], s[24:25], 0, v[132:133]
	s_waitcnt vmcnt(6)
	s_waitcnt lgkmcnt(0)
	s_barrier
; #define PG8_STAGE(bufoff, gbase, voff) do { _Pragma("unroll") for (int _i = 0; _i < 2; ++_i) \
;         __builtin_amdgcn_global_load_lds((const unsigned*)((const char*)(gbase) + (voff)[_i]), (PG8_LAS unsigned*)(lds + (bufoff) + ldsw + _i * 8192), 16, 0, 0); } while (0)
; #define PG8_LDA(dst, b, h) do { _Pragma("unroll") for (int m = 0; m < 4; ++m) _Pragma("unroll") for (int k = 0; k < 2; ++k) dst[m][k] = *(const PG8_LAS bf16x8*)(lds + PG8_SA(b, h) + aoff + m * 2048 + k * 1024); } while (0)
; #define PG8_LDB(dst, b, h) do { _Pragma("unroll") for (int n = 0; n < 2; ++n) _Pragma("unroll") for (int k = 0; k < 2; ++k) dst[n][k] = *(const PG8_LAS bf16x8*)(lds + PG8_SB(b, h) + boff + n * 2048 + k * 1024); } while (0)
; #define PG8_MMA(ai, bj, At, Bt) do { __builtin_amdgcn_s_setprio(1); _Pragma("unroll") for (int m = 0; m < 4; ++m) _Pragma("unroll") for (int n = 0; n < 2; ++n) _Pragma("unroll") for (int k = 0; k < 2; ++k) \
;         acc[ai][bj][m][n] = __builtin_amdgcn_mfma_f32_16x16x32_bf16(Bt[n][k], At[m][k], acc[ai][bj][m][n], 0, 0, 0); __builtin_amdgcn_s_setprio(0); } while (0)
; #define PG8_WAIT_V(n) asm volatile("s_waitcnt vmcnt(" #n ")" ::: "memory")
; #define PG8_WAIT_L(n) asm volatile("s_waitcnt lgkmcnt(" #n ")" ::: "memory")
; #define PG8_BAR __builtin_amdgcn_s_barrier()
; #define PG8_SCHED __builtin_amdgcn_sched_barrier(0)
; template <class Epi, class Sched, bool ALIGN_EPI = false, bool SP2 = false>
; __device__ __forceinline__ void gemm_phase(PG8_LAS unsigned char* lds, const Gemm g, const Sched& S, const Epi& E) {
;     ...
;             PG8_WAIT_V(8); PG8_WAIT_L(0); PG8_BAR; PG8_MMA(1, 0, At, B0); PG8_MMA(1, 1, At, B1); PG8_BAR; PG8_SCHED;
;             PG8_LDB(B0, 1, 0); PG8_LDB(B1, 1, 1); PG8_SCHED; PG8_LDA(At, 1, 0); PG8_STAGE(PG8_SA(0, 1), a2 + hstepA, voffA);
	s_setprio 1
	s_waitcnt lgkmcnt(0)
	v_mfma_f32_16x16x32_bf16 v[64:67], v[150:153], v[182:185], v[64:67]
	v_mfma_f32_16x16x32_bf16 v[60:63], v[158:161], v[182:185], v[60:63]
	v_mfma_f32_16x16x32_bf16 v[56:59], v[150:153], v[190:193], v[56:59]
	v_mfma_f32_16x16x32_bf16 v[48:51], v[158:161], v[190:193], v[48:51]
	v_mfma_f32_16x16x32_bf16 v[40:43], v[150:153], v[210:213], v[40:43]
	v_mfma_f32_16x16x32_bf16 v[32:35], v[158:161], v[210:213], v[32:35]
	v_mfma_f32_16x16x32_bf16 v[24:27], v[150:153], v[230:233], v[24:27]
	v_mfma_f32_16x16x32_bf16 v[16:19], v[158:161], v[230:233], v[16:19]
	v_mfma_f32_16x16x32_bf16 v[64:67], v[154:157], v[186:189], v[64:67]
	v_mfma_f32_16x16x32_bf16 v[60:63], v[162:165], v[186:189], v[60:63]
	v_mfma_f32_16x16x32_bf16 v[56:59], v[154:157], v[194:197], v[56:59]
	v_mfma_f32_16x16x32_bf16 v[48:51], v[162:165], v[194:197], v[48:51]
	v_mfma_f32_16x16x32_bf16 v[40:43], v[154:157], v[226:229], v[40:43]
	v_mfma_f32_16x16x32_bf16 v[32:35], v[162:165], v[226:229], v[32:35]
	v_mfma_f32_16x16x32_bf16 v[24:27], v[154:157], v[234:237], v[24:27]
	v_mfma_f32_16x16x32_bf16 v[16:19], v[162:165], v[234:237], v[16:19]
	s_setprio 0
	s_setprio 1
	v_mfma_f32_16x16x32_bf16 v[52:55], v[166:169], v[182:185], v[52:55]
	v_mfma_f32_16x16x32_bf16 v[44:47], v[174:177], v[182:185], v[44:47]
	v_mfma_f32_16x16x32_bf16 v[36:39], v[166:169], v[190:193], v[36:39]
	v_mfma_f32_16x16x32_bf16 v[28:31], v[174:177], v[190:193], v[28:31]
	v_mfma_f32_16x16x32_bf16 v[20:23], v[166:169], v[210:213], v[20:23]
	v_mfma_f32_16x16x32_bf16 v[12:15], v[174:177], v[210:213], v[12:15]
	v_mfma_f32_16x16x32_bf16 v[8:11], v[166:169], v[230:233], v[8:11]
	v_mfma_f32_16x16x32_bf16 v[4:7], v[174:177], v[230:233], v[4:7]
	v_mfma_f32_16x16x32_bf16 v[52:55], v[170:173], v[186:189], v[52:55]
	v_mfma_f32_16x16x32_bf16 v[44:47], v[178:181], v[186:189], v[44:47]
	v_mfma_f32_16x16x32_bf16 v[36:39], v[170:173], v[194:197], v[36:39]
	v_mfma_f32_16x16x32_bf16 v[28:31], v[178:181], v[194:197], v[28:31]
	v_mfma_f32_16x16x32_bf16 v[20:23], v[170:173], v[226:229], v[20:23]
	v_mfma_f32_16x16x32_bf16 v[12:15], v[178:181], v[226:229], v[12:15]
	v_mfma_f32_16x16x32_bf16 v[8:11], v[170:173], v[234:237], v[8:11]
	v_mfma_f32_16x16x32_bf16 v[4:7], v[178:181], v[234:237], v[4:7]
	s_setprio 0
	s_barrier
	s_add_i32 s46, 0, 0x18000
	v_add_u32_e32 v149, s46, v146
	s_add_i32 s47, 0, 0x1c000
	ds_read_b128 v[150:153], v149
	ds_read_b128 v[154:157], v149 offset:1024
	ds_read_b128 v[158:161], v149 offset:2048
	ds_read_b128 v[162:165], v149 offset:3072
	v_add_u32_e32 v149, s47, v146
	ds_read_b128 v[166:169], v149
	ds_read_b128 v[170:173], v149 offset:1024
	ds_read_b128 v[174:177], v149 offset:2048
	ds_read_b128 v[178:181], v149 offset:3072
	s_add_u32 s24, s24, 0x40000
	s_addc_u32 s25, s25, 0
	s_mov_b32 m0, s34
	v_lshl_add_u64 v[244:245], s[24:25], 0, v[132:133]
	ds_read_b128 v[182:185], v148 offset:32768
	ds_read_b128 v[186:189], v148 offset:33792
	ds_read_b128 v[190:193], v148 offset:34816
	ds_read_b128 v[194:197], v148 offset:35840
	ds_read_b128 v[210:213], v148 offset:36864
	ds_read_b128 v[226:229], v148 offset:37888
	ds_read_b128 v[230:233], v148 offset:38912
	s_mov_b32 m0, s15
	ds_read_b128 v[234:237], v148 offset:39936
	global_load_lds_dwordx4 v[240:241], off
	s_mov_b32 m0, s33
	s_nop 0
	global_load_lds_dwordx4 v[242:243], off
	s_mov_b32 m0, s34
	s_nop 0
	global_load_lds_dwordx4 v[244:245], off
	s_mov_b32 m0, s35
	v_lshl_add_u64 v[244:245], s[24:25], 0, v[136:137]
	global_load_lds_dwordx4 v[244:245], off
	s_waitcnt vmcnt(8)
	s_waitcnt lgkmcnt(0)
	s_barrier
; #define PG8_STAGE(bufoff, gbase, voff) do { _Pragma("unroll") for (int _i = 0; _i < 2; ++_i) \
;         __builtin_amdgcn_global_load_lds((const unsigned*)((const char*)(gbase) + (voff)[_i]), (PG8_LAS unsigned*)(lds + (bufoff) + ldsw + _i * 8192), 16, 0, 0); } while (0)
; #define PG8_LDA(dst, b, h) do { _Pragma("unroll") for (int m = 0; m < 4; ++m) _Pragma("unroll") for (int k = 0; k < 2; ++k) dst[m][k] = *(const PG8_LAS bf16x8*)(lds + PG8_SA(b, h) + aoff + m * 2048 + k * 1024); } while (0)
; #define PG8_MMA(ai, bj, At, Bt) do { __builtin_amdgcn_s_setprio(1); _Pragma("unroll") for (int m = 0; m < 4; ++m) _Pragma("unroll") for (int n = 0; n < 2; ++n) _Pragma("unroll") for (int k = 0; k < 2; ++k) \
;         acc[ai][bj][m][n] = __builtin_amdgcn_mfma_f32_16x16x32_bf16(Bt[n][k], At[m][k], acc[ai][bj][m][n], 0, 0, 0); __builtin_amdgcn_s_setprio(0); } while (0)
; #define PG8_WAIT_V(n) asm volatile("s_waitcnt vmcnt(" #n ")" ::: "memory")
; #define PG8_WAIT_L(n) asm volatile("s_waitcnt lgkmcnt(" #n ")" ::: "memory")
; #define PG8_BAR __builtin_amdgcn_s_barrier()
; #define PG8_SCHED __builtin_amdgcn_sched_barrier(0)
; template <class Epi, class Sched, bool ALIGN_EPI = false, bool SP2 = false>
; __device__ __forceinline__ void gemm_phase(PG8_LAS unsigned char* lds, const Gemm g, const Sched& S, const Epi& E) {
;     ...
;             PG8_WAIT_V(8); PG8_WAIT_L(0); PG8_BAR; PG8_MMA(0, 0, At, B0); PG8_MMA(0, 1, At, B1); PG8_BAR; PG8_SCHED;
;             PG8_LDA(At, 1, 1); PG8_STAGE(PG8_SB(1, 0), b3, voffB); PG8_STAGE(PG8_SB(1, 1), b3 + hstepB, voffB); PG8_STAGE(PG8_SA(1, 0), a3, voffA);
;             PG8_WAIT_V(8); PG8_WAIT_L(0); PG8_BAR; PG8_MMA(1, 0, At, B0); PG8_MMA(1, 1, At, B1); PG8_BAR; PG8_SCHED;
	s_setprio 1
	s_waitcnt lgkmcnt(0)
	v_mfma_f32_16x16x32_bf16 v[128:131], v[150:153], v[182:185], v[128:131]
	v_mfma_f32_16x16x32_bf16 v[124:127], v[158:161], v[182:185], v[124:127]
	v_mfma_f32_16x16x32_bf16 v[120:123], v[150:153], v[190:193], v[120:123]
	v_mfma_f32_16x16x32_bf16 v[112:115], v[158:161], v[190:193], v[112:115]
	v_mfma_f32_16x16x32_bf16 v[104:107], v[150:153], v[210:213], v[104:107]
	v_mfma_f32_16x16x32_bf16 v[96:99], v[158:161], v[210:213], v[96:99]
	v_mfma_f32_16x16x32_bf16 v[88:91], v[150:153], v[230:233], v[88:91]
	v_mfma_f32_16x16x32_bf16 v[80:83], v[158:161], v[230:233], v[80:83]
	v_mfma_f32_16x16x32_bf16 v[128:131], v[154:157], v[186:189], v[128:131]
	v_mfma_f32_16x16x32_bf16 v[124:127], v[162:165], v[186:189], v[124:127]
	v_mfma_f32_16x16x32_bf16 v[120:123], v[154:157], v[194:197], v[120:123]
	v_mfma_f32_16x16x32_bf16 v[112:115], v[162:165], v[194:197], v[112:115]
	v_mfma_f32_16x16x32_bf16 v[104:107], v[154:157], v[226:229], v[104:107]
	v_mfma_f32_16x16x32_bf16 v[96:99], v[162:165], v[226:229], v[96:99]
	v_mfma_f32_16x16x32_bf16 v[88:91], v[154:157], v[234:237], v[88:91]
	v_mfma_f32_16x16x32_bf16 v[80:83], v[162:165], v[234:237], v[80:83]
	s_setprio 0
	s_setprio 1
	v_mfma_f32_16x16x32_bf16 v[116:119], v[166:169], v[182:185], v[116:119]
	v_mfma_f32_16x16x32_bf16 v[108:111], v[174:177], v[182:185], v[108:111]
	v_mfma_f32_16x16x32_bf16 v[100:103], v[166:169], v[190:193], v[100:103]
	v_mfma_f32_16x16x32_bf16 v[92:95], v[174:177], v[190:193], v[92:95]
	v_mfma_f32_16x16x32_bf16 v[84:87], v[166:169], v[210:213], v[84:87]
	v_mfma_f32_16x16x32_bf16 v[76:79], v[174:177], v[210:213], v[76:79]
	v_mfma_f32_16x16x32_bf16 v[72:75], v[166:169], v[230:233], v[72:75]
	v_mfma_f32_16x16x32_bf16 v[68:71], v[174:177], v[230:233], v[68:71]
	v_mfma_f32_16x16x32_bf16 v[116:119], v[170:173], v[186:189], v[116:119]
	v_mfma_f32_16x16x32_bf16 v[108:111], v[178:181], v[186:189], v[108:111]
	v_mfma_f32_16x16x32_bf16 v[100:103], v[170:173], v[194:197], v[100:103]
	v_mfma_f32_16x16x32_bf16 v[92:95], v[178:181], v[194:197], v[92:95]
	v_mfma_f32_16x16x32_bf16 v[84:87], v[170:173], v[226:229], v[84:87]
	v_mfma_f32_16x16x32_bf16 v[76:79], v[178:181], v[226:229], v[76:79]
	v_mfma_f32_16x16x32_bf16 v[72:75], v[170:173], v[234:237], v[72:75]
	v_mfma_f32_16x16x32_bf16 v[68:71], v[178:181], v[234:237], v[68:71]
	s_setprio 0
	s_barrier
	s_add_i32 s24, s46, s31
	v_lshl_add_u64 v[144:145], v[144:145], 0, s[64:65]
	s_mov_b32 m0, s24
	ds_read_b128 v[182:185], v148 offset:49152
	ds_read_b128 v[186:189], v148 offset:50176
	ds_read_b128 v[190:193], v148 offset:51200
	ds_read_b128 v[194:197], v148 offset:52224
	ds_read_b128 v[210:213], v148 offset:53248
	ds_read_b128 v[226:229], v148 offset:54272
	ds_read_b128 v[230:233], v148 offset:55296
	ds_read_b128 v[234:237], v148 offset:56320
	global_load_lds_dwordx4 v[144:145], off
	s_add_i32 m0, s24, 0x2000
	s_add_u32 s22, s22, 0x40080
	v_lshl_add_u64 v[144:145], v[238:239], 0, s[64:65]
	s_addc_u32 s23, s23, 0
	s_add_i32 s24, s47, s31
	global_load_lds_dwordx4 v[144:145], off
	s_mov_b32 m0, s24
	v_lshl_add_u64 v[144:145], s[22:23], 0, v[134:135]
	global_load_lds_dwordx4 v[144:145], off
	s_add_i32 m0, s24, 0x2000
	v_lshl_add_u64 v[144:145], s[22:23], 0, v[138:139]
	global_load_lds_dwordx4 v[144:145], off
	s_waitcnt vmcnt(6)
	s_waitcnt lgkmcnt(0)
	s_barrier
	s_setprio 1
	s_waitcnt lgkmcnt(0)
	v_mfma_f32_16x16x32_bf16 v[64:67], v[150:153], v[182:185], v[64:67]
	v_mfma_f32_16x16x32_bf16 v[60:63], v[158:161], v[182:185], v[60:63]
	v_mfma_f32_16x16x32_bf16 v[56:59], v[150:153], v[190:193], v[56:59]
	v_mfma_f32_16x16x32_bf16 v[48:51], v[158:161], v[190:193], v[48:51]
	v_mfma_f32_16x16x32_bf16 v[40:43], v[150:153], v[210:213], v[40:43]
	v_mfma_f32_16x16x32_bf16 v[32:35], v[158:161], v[210:213], v[32:35]
	v_mfma_f32_16x16x32_bf16 v[24:27], v[150:153], v[230:233], v[24:27]
	v_mfma_f32_16x16x32_bf16 v[16:19], v[158:161], v[230:233], v[16:19]
	v_mfma_f32_16x16x32_bf16 v[64:67], v[154:157], v[186:189], v[64:67]
	v_mfma_f32_16x16x32_bf16 v[60:63], v[162:165], v[186:189], v[60:63]
	v_mfma_f32_16x16x32_bf16 v[56:59], v[154:157], v[194:197], v[56:59]
	v_mfma_f32_16x16x32_bf16 v[48:51], v[162:165], v[194:197], v[48:51]
	v_mfma_f32_16x16x32_bf16 v[40:43], v[154:157], v[226:229], v[40:43]
	v_mfma_f32_16x16x32_bf16 v[32:35], v[162:165], v[226:229], v[32:35]
	v_mfma_f32_16x16x32_bf16 v[24:27], v[154:157], v[234:237], v[24:27]
	v_mfma_f32_16x16x32_bf16 v[16:19], v[162:165], v[234:237], v[16:19]
	s_setprio 0
	s_setprio 1
	v_mfma_f32_16x16x32_bf16 v[52:55], v[166:169], v[182:185], v[52:55]
	v_mfma_f32_16x16x32_bf16 v[44:47], v[174:177], v[182:185], v[44:47]
	v_mfma_f32_16x16x32_bf16 v[36:39], v[166:169], v[190:193], v[36:39]
	v_mfma_f32_16x16x32_bf16 v[28:31], v[174:177], v[190:193], v[28:31]
	v_mfma_f32_16x16x32_bf16 v[20:23], v[166:169], v[210:213], v[20:23]
	v_mfma_f32_16x16x32_bf16 v[12:15], v[174:177], v[210:213], v[12:15]
	v_mfma_f32_16x16x32_bf16 v[8:11], v[166:169], v[230:233], v[8:11]
	v_mfma_f32_16x16x32_bf16 v[4:7], v[174:177], v[230:233], v[4:7]
	v_mfma_f32_16x16x32_bf16 v[52:55], v[170:173], v[186:189], v[52:55]
	v_mfma_f32_16x16x32_bf16 v[44:47], v[178:181], v[186:189], v[44:47]
	v_mfma_f32_16x16x32_bf16 v[36:39], v[170:173], v[194:197], v[36:39]
	v_mfma_f32_16x16x32_bf16 v[28:31], v[178:181], v[194:197], v[28:31]
	v_mfma_f32_16x16x32_bf16 v[20:23], v[170:173], v[226:229], v[20:23]
	v_mfma_f32_16x16x32_bf16 v[12:15], v[178:181], v[226:229], v[12:15]
	v_mfma_f32_16x16x32_bf16 v[8:11], v[170:173], v[234:237], v[8:11]
	v_mfma_f32_16x16x32_bf16 v[4:7], v[178:181], v[234:237], v[4:7]
	s_setprio 0
	s_barrier
	s_add_i32 s45, s45, 2
	s_add_u32 s43, s43, 0x100
	s_addc_u32 s44, s44, 0
	s_add_u32 s20, s20, 0x100
	s_addc_u32 s21, s21, 0
	s_cmp_gt_u32 s45, 13
	s_cbranch_scc0 .LBB0_1693
	s_and_b64 vcc, exec, s[8:9]
	s_cbranch_vccz .LBB0_1696
	s_barrier
